# adds: RG-LRU row scans fold the DPP shift into the multiply-add (v_fmac_f32_dpp / v_mul_f32_dpp, 2 instead of 6 instructions per step, same values) in both passes
# speedup vs baseline: 1.0097x; 1.0047x over previous
; #define LAS __attribute__((address_space(3)))
; __device__ __forceinline__ float fsigmoid(float x) { return __builtin_amdgcn_rcpf(1.0f + __expf(-x)); }
; template <int PASS, bool REV> ...
;     ...
;         for (int kk = 0; kk < 2; ++kk) { const bf16x8 wa = wcur[0][kk], wx = wcur[1][kk]; bf16x8 uf[4][2];
; #pragma unroll
;             for (int tg = 0; tg < 4; ++tg) uf[tg][kk] = *(const LAS bf16x8*)(UB + (tg * 16 + fr) * 264 + blk * 64 + kk * 32 + fq * 8);
; #pragma unroll
;             for (int tg = 0; tg < 4; ++tg) { aa[tg] = __builtin_amdgcn_mfma_f32_16x16x32_bf16(wa, uf[tg][kk], aa[tg], 0, 0, 0); ax[tg] = __builtin_amdgcn_mfma_f32_16x16x32_bf16(wx, uf[tg][kk], ax[tg], 0, 0, 0); } }
;         { const int ng1 = (ng + 1 < ng_hi) ? ng + 1 : ng_lo;
; #pragma unroll
;             for (int gt = 0; gt < 2; ++gt)
; #pragma unroll
;                 for (int kk = 0; kk < 2; ++kk) wcur[gt][kk] = *(const bf16x8*)(Wg + ((size_t)(gt * 4 + blk) * 64 + ng1 * 16 + fr) * 64 + kk * 32 + fq * 8); }
;         if (PASS == 2 && REV && emit) {
; #pragma unroll
;             for (int tg = 0; tg < 4; ++tg) gwv[tg] = *(const v2u*)(P + (size_t)(R0 + tg * 16 + fr) * PROJ + C_RGG + blk * 64 + ng * 16 + fq * 4); }
;         const int ch = blk * 64 + ng * 16 + fq * 4; const f32x4 sp = *(const LAS f32x4*)(cst + ch), bav = *(const LAS f32x4*)(cst + 256 + ch), bxv = *(const LAS f32x4*)(cst + 512 + ch);
; #pragma unroll
;         for (int tg = 0; tg < 4; ++tg) { const v2u uw = *(const LAS v2u*)(UB + (tg * 16 + fr) * 264 + ch); const float uv[4] = {bflo(uw.x), bfhi(uw.x), bflo(uw.y), bfhi(uw.y)};
; #pragma unroll
;             for (int j = 0; j < 4; ++j) { const float r = fsigmoid(aa[tg][j] + bav[j]), ig = fsigmoid(ax[tg][j] + bxv[j]); const float la = -8.0f * r * sp[j];
;                 float Av = __expf(la); const float om = __builtin_fmaf(-Av, Av, 1.0f);
;                 float Bv = __builtin_amdgcn_sqrtf(om) * (ig * uv[j]);
;                 rg_scan_step<REV, 1>(Av, Bv); rg_scan_step<REV, 2>(Av, Bv); rg_scan_step<REV, 4>(Av, Bv); rg_scan_step<REV, 8>(Av, Bv);
;                 aa[tg][j] = Av; ax[tg][j] = Bv; } }
.LBB0_553:
	s_add_i32 s0, s9, s13
	s_waitcnt vmcnt(0) lgkmcnt(7)
	v_mfma_f32_16x16x32_bf16 v[48:51], v[40:43], v[0:3], 0
	s_add_i32 s0, s0, 1
	s_cmp_lt_u32 s0, s8
	s_cselect_b32 s0, s0, s9
	v_mfma_f32_16x16x32_bf16 v[52:55], v[44:47], v[0:3], 0
	v_lshl_add_u32 v180, s0, 4, v99
	v_add_u32_e32 v118, 0, v116
	s_waitcnt lgkmcnt(5)
	v_mfma_f32_16x16x32_bf16 v[56:59], v[40:43], v[8:11], 0
	s_waitcnt lgkmcnt(3)
	v_mfma_f32_16x16x32_bf16 v[64:67], v[40:43], v[16:19], 0
	s_waitcnt lgkmcnt(1)
	v_mfma_f32_16x16x32_bf16 v[40:43], v[40:43], v[24:27], 0
	v_mfma_f32_16x16x32_bf16 v[60:63], v[44:47], v[8:11], 0
	v_mfma_f32_16x16x32_bf16 v[68:71], v[44:47], v[16:19], 0
	v_mfma_f32_16x16x32_bf16 v[44:47], v[44:47], v[24:27], 0
	v_mfma_f32_16x16x32_bf16 v[88:91], v[32:35], v[4:7], v[48:51]
	v_mfma_f32_16x16x32_bf16 v[84:87], v[36:39], v[4:7], v[52:55]
	v_mfma_f32_16x16x32_bf16 v[80:83], v[32:35], v[12:15], v[56:59]
	v_mfma_f32_16x16x32_bf16 v[72:75], v[32:35], v[20:23], v[64:67]
	s_waitcnt lgkmcnt(0)
	v_mfma_f32_16x16x32_bf16 v[52:55], v[32:35], v[28:31], v[40:43]
	v_lshlrev_b64 v[32:33], 7, v[180:181]
	v_add_u32_e32 v180, 0x100, v180
	v_lshl_add_u64 v[32:33], v[94:95], 0, v[32:33]
	v_mfma_f32_16x16x32_bf16 v[76:79], v[36:39], v[12:15], v[60:63]
	global_load_dwordx4 v[40:43], v[32:33], off
	s_nop 0
	global_load_dwordx4 v[32:35], v[32:33], off offset:64
	v_add_u32_e32 v60, 0, v117
	v_add_u32_e32 v61, 0x12000, v60
	v_mfma_f32_16x16x32_bf16 v[68:71], v[36:39], v[20:23], v[68:71]
	v_add_u32_e32 v56, 0x11c00, v60
	v_add_u32_e32 v60, 0x12400, v60
	v_mfma_f32_16x16x32_bf16 v[48:51], v[36:39], v[28:31], v[44:47]
	v_lshlrev_b64 v[36:37], 7, v[180:181]
	v_lshl_add_u64 v[36:37], v[94:95], 0, v[36:37]
	s_nop 0
	global_load_dwordx4 v[44:47], v[36:37], off
	s_nop 0
	global_load_dwordx4 v[36:39], v[36:37], off offset:64
	ds_read_b128 v[64:67], v61
	ds_read_b64 v[120:121], v118
	ds_read_b128 v[56:59], v56
	ds_read_b128 v[60:63], v60
	s_waitcnt lgkmcnt(3)
	v_add_f32_e32 v88, v88, v64
	v_mul_f32_e32 v88, 0xbfb8aa3b, v88
	v_exp_f32_e32 v88, v88
	s_waitcnt lgkmcnt(0)
	v_add_f32_e32 v84, v84, v60
	v_mul_f32_e32 v84, 0xbfb8aa3b, v84
	v_exp_f32_e32 v84, v84
	v_add_f32_e32 v88, 1.0, v88
	v_rcp_f32_e32 v88, v88
	v_add_f32_e32 v89, v89, v65
	v_mul_f32_e32 v89, 0xbfb8aa3b, v89
	v_exp_f32_e32 v89, v89
	v_mul_f32_e32 v88, 0xc1000000, v88
	v_mul_f32_e32 v88, v56, v88
	v_mul_f32_e32 v88, 0x3fb8aa3b, v88
	v_exp_f32_e32 v88, v88
	v_add_f32_e32 v84, 1.0, v84
	v_rcp_f32_e32 v84, v84
	v_add_f32_e32 v89, 1.0, v89
	v_fma_f32 v123, -v88, v88, 1.0
	v_sqrt_f32_e32 v123, v123
	v_rcp_f32_e32 v89, v89
	v_lshlrev_b32_e32 v119, 16, v120
	v_mul_f32_e32 v84, v84, v119
	v_mul_f32_e32 v84, v84, v123
	v_add_f32_e32 v85, v85, v61
	v_mul_f32_e32 v89, 0xc1000000, v89
	v_fmac_f32_dpp v84, v84, v88 row_shl:1 row_mask:0xf bank_mask:0xf bound_ctrl:1
	v_mul_f32_dpp v88, v88, v88 row_shl:1 row_mask:0xf bank_mask:0xf
	v_mul_f32_e32 v85, 0xbfb8aa3b, v85
	v_mul_f32_e32 v89, v57, v89
	v_exp_f32_e32 v85, v85
	v_mul_f32_e32 v89, 0x3fb8aa3b, v89
	v_add_f32_e32 v90, v90, v66
	v_fmac_f32_dpp v84, v84, v88 row_shl:2 row_mask:0xf bank_mask:0xf bound_ctrl:1
	v_mul_f32_dpp v88, v88, v88 row_shl:2 row_mask:0xf bank_mask:0xf
	v_exp_f32_e32 v89, v89
	v_mul_f32_e32 v90, 0xbfb8aa3b, v90
	v_exp_f32_e32 v90, v90
	v_fmac_f32_dpp v84, v84, v88 row_shl:4 row_mask:0xf bank_mask:0xf bound_ctrl:1
	v_mul_f32_dpp v88, v88, v88 row_shl:4 row_mask:0xf bank_mask:0xf
	v_add_f32_e32 v85, 1.0, v85
	v_fmac_f32_dpp v84, v84, v88 row_shl:8 row_mask:0xf bank_mask:0xf bound_ctrl:1
	v_mul_f32_dpp v88, v88, v88 row_shl:8 row_mask:0xf bank_mask:0xf
	v_rcp_f32_e32 v85, v85
	v_fma_f32 v119, -v89, v89, 1.0
	v_sqrt_f32_e32 v119, v119
	v_add_f32_e32 v90, 1.0, v90
	v_rcp_f32_e32 v90, v90
	v_and_b32_e32 v120, 0xffff0000, v120
	v_mul_f32_e32 v85, v85, v120
	v_mul_f32_e32 v85, v85, v119
	v_add_f32_e32 v86, v86, v62
	v_mul_f32_e32 v90, 0xc1000000, v90
	v_fmac_f32_dpp v85, v85, v89 row_shl:1 row_mask:0xf bank_mask:0xf bound_ctrl:1
	v_mul_f32_dpp v89, v89, v89 row_shl:1 row_mask:0xf bank_mask:0xf
	v_mul_f32_e32 v86, 0xbfb8aa3b, v86
	v_mul_f32_e32 v90, v58, v90
	v_exp_f32_e32 v86, v86
	v_mul_f32_e32 v90, 0x3fb8aa3b, v90
	v_add_f32_e32 v91, v91, v67
	v_fmac_f32_dpp v85, v85, v89 row_shl:2 row_mask:0xf bank_mask:0xf bound_ctrl:1
	v_mul_f32_dpp v89, v89, v89 row_shl:2 row_mask:0xf bank_mask:0xf
	v_exp_f32_e32 v90, v90
	v_mul_f32_e32 v91, 0xbfb8aa3b, v91
	v_exp_f32_e32 v91, v91
	v_fmac_f32_dpp v85, v85, v89 row_shl:4 row_mask:0xf bank_mask:0xf bound_ctrl:1
	v_mul_f32_dpp v89, v89, v89 row_shl:4 row_mask:0xf bank_mask:0xf
	v_add_f32_e32 v86, 1.0, v86
	v_fmac_f32_dpp v85, v85, v89 row_shl:8 row_mask:0xf bank_mask:0xf bound_ctrl:1
	v_mul_f32_dpp v89, v89, v89 row_shl:8 row_mask:0xf bank_mask:0xf
	v_rcp_f32_e32 v86, v86
	v_fma_f32 v119, -v90, v90, 1.0
	v_sqrt_f32_e32 v119, v119
	v_add_f32_e32 v91, 1.0, v91
	v_rcp_f32_e32 v91, v91
	v_lshlrev_b32_e32 v122, 16, v121
	v_mul_f32_e32 v86, v86, v122
	v_mul_f32_e32 v86, v86, v119
	v_add_f32_e32 v87, v87, v63
	v_mul_f32_e32 v91, 0xc1000000, v91
	v_fmac_f32_dpp v86, v86, v90 row_shl:1 row_mask:0xf bank_mask:0xf bound_ctrl:1
	v_mul_f32_dpp v90, v90, v90 row_shl:1 row_mask:0xf bank_mask:0xf
	v_mul_f32_e32 v87, 0xbfb8aa3b, v87
	v_mul_f32_e32 v91, v59, v91
	v_exp_f32_e32 v87, v87
	v_mul_f32_e32 v91, 0x3fb8aa3b, v91
	v_fmac_f32_dpp v86, v86, v90 row_shl:2 row_mask:0xf bank_mask:0xf bound_ctrl:1
	v_mul_f32_dpp v90, v90, v90 row_shl:2 row_mask:0xf bank_mask:0xf
	v_exp_f32_e32 v91, v91
	v_add_f32_e32 v80, v80, v64
	v_fmac_f32_dpp v86, v86, v90 row_shl:4 row_mask:0xf bank_mask:0xf bound_ctrl:1
	v_mul_f32_dpp v90, v90, v90 row_shl:4 row_mask:0xf bank_mask:0xf
; #define LAS __attribute__((address_space(3)))
; __device__ __forceinline__ float fsigmoid(float x) { return __builtin_amdgcn_rcpf(1.0f + __expf(-x)); }
; template <int PASS, bool REV> ...
;     ...
;         const int ch = blk * 64 + ng * 16 + fq * 4; const f32x4 sp = *(const LAS f32x4*)(cst + ch), bav = *(const LAS f32x4*)(cst + 256 + ch), bxv = *(const LAS f32x4*)(cst + 512 + ch);
; #pragma unroll
;         for (int tg = 0; tg < 4; ++tg) { const v2u uw = *(const LAS v2u*)(UB + (tg * 16 + fr) * 264 + ch); const float uv[4] = {bflo(uw.x), bfhi(uw.x), bflo(uw.y), bfhi(uw.y)};
; #pragma unroll
;             for (int j = 0; j < 4; ++j) { const float r = fsigmoid(aa[tg][j] + bav[j]), ig = fsigmoid(ax[tg][j] + bxv[j]); const float la = -8.0f * r * sp[j];
;                 float Av = __expf(la); const float om = __builtin_fmaf(-Av, Av, 1.0f);
;                 float Bv = __builtin_amdgcn_sqrtf(om) * (ig * uv[j]);
;                 rg_scan_step<REV, 1>(Av, Bv); rg_scan_step<REV, 2>(Av, Bv); rg_scan_step<REV, 4>(Av, Bv); rg_scan_step<REV, 8>(Av, Bv);
;                 aa[tg][j] = Av; ax[tg][j] = Bv; } }
	v_mul_f32_e32 v80, 0xbfb8aa3b, v80
	v_add_f32_e32 v87, 1.0, v87
	v_exp_f32_e32 v80, v80
	v_fmac_f32_dpp v86, v86, v90 row_shl:8 row_mask:0xf bank_mask:0xf bound_ctrl:1
	v_mul_f32_dpp v90, v90, v90 row_shl:8 row_mask:0xf bank_mask:0xf
	v_rcp_f32_e32 v87, v87
	v_fma_f32 v119, -v91, v91, 1.0
	v_sqrt_f32_e32 v119, v119
	v_and_b32_e32 v121, 0xffff0000, v121
	v_add_f32_e32 v80, 1.0, v80
	v_mul_f32_e32 v87, v87, v121
	v_rcp_f32_e32 v80, v80
	v_mul_f32_e32 v87, v87, v119
	v_add_f32_e32 v76, v76, v60
	s_nop 0
	v_fmac_f32_dpp v87, v87, v91 row_shl:1 row_mask:0xf bank_mask:0xf bound_ctrl:1
	v_mul_f32_dpp v91, v91, v91 row_shl:1 row_mask:0xf bank_mask:0xf
	v_mul_f32_e32 v80, 0xc1000000, v80
	v_fmac_f32_dpp v87, v87, v91 row_shl:2 row_mask:0xf bank_mask:0xf bound_ctrl:1
	v_mul_f32_e32 v76, 0xbfb8aa3b, v76
	v_mul_f32_e32 v80, v56, v80
	v_mul_f32_dpp v91, v91, v91 row_shl:2 row_mask:0xf bank_mask:0xf
	v_exp_f32_e32 v76, v76
	v_mul_f32_e32 v80, 0x3fb8aa3b, v80
	v_add_f32_e32 v81, v81, v65
	v_fmac_f32_dpp v87, v87, v91 row_shl:4 row_mask:0xf bank_mask:0xf bound_ctrl:1
	v_exp_f32_e32 v80, v80
	v_mul_f32_e32 v81, 0xbfb8aa3b, v81
	v_mul_f32_dpp v91, v91, v91 row_shl:4 row_mask:0xf bank_mask:0xf
	v_exp_f32_e32 v81, v81
	v_fmac_f32_dpp v87, v87, v91 row_shl:8 row_mask:0xf bank_mask:0xf bound_ctrl:1
	ds_read_b64 v[120:121], v118 offset:8448
	v_add_f32_e32 v76, 1.0, v76
	v_rcp_f32_e32 v76, v76
	v_fma_f32 v123, -v80, v80, 1.0
	v_sqrt_f32_e32 v123, v123
	v_add_f32_e32 v81, 1.0, v81
	v_rcp_f32_e32 v81, v81
	v_mul_f32_dpp v91, v91, v91 row_shl:8 row_mask:0xf bank_mask:0xf
	s_waitcnt lgkmcnt(0)
	v_lshlrev_b32_e32 v119, 16, v120
	v_mul_f32_e32 v76, v76, v119
	v_mul_f32_e32 v76, v123, v76
	v_add_f32_e32 v77, v77, v61
	v_mul_f32_e32 v81, 0xc1000000, v81
	v_fmac_f32_dpp v76, v76, v80 row_shl:1 row_mask:0xf bank_mask:0xf bound_ctrl:1
	v_mul_f32_dpp v80, v80, v80 row_shl:1 row_mask:0xf bank_mask:0xf
	v_mul_f32_e32 v77, 0xbfb8aa3b, v77
	v_mul_f32_e32 v81, v57, v81
	v_exp_f32_e32 v77, v77
	v_mul_f32_e32 v81, 0x3fb8aa3b, v81
	v_add_f32_e32 v82, v82, v66
	v_fmac_f32_dpp v76, v76, v80 row_shl:2 row_mask:0xf bank_mask:0xf bound_ctrl:1
	v_mul_f32_dpp v80, v80, v80 row_shl:2 row_mask:0xf bank_mask:0xf
	v_exp_f32_e32 v81, v81
	v_mul_f32_e32 v82, 0xbfb8aa3b, v82
	v_exp_f32_e32 v82, v82
	v_fmac_f32_dpp v76, v76, v80 row_shl:4 row_mask:0xf bank_mask:0xf bound_ctrl:1
	v_mul_f32_dpp v80, v80, v80 row_shl:4 row_mask:0xf bank_mask:0xf
	v_add_f32_e32 v77, 1.0, v77
	v_fmac_f32_dpp v76, v76, v80 row_shl:8 row_mask:0xf bank_mask:0xf bound_ctrl:1
	v_mul_f32_dpp v80, v80, v80 row_shl:8 row_mask:0xf bank_mask:0xf
	v_rcp_f32_e32 v77, v77
	v_fma_f32 v119, -v81, v81, 1.0
	v_sqrt_f32_e32 v119, v119
	v_add_f32_e32 v82, 1.0, v82
	v_rcp_f32_e32 v82, v82
	v_and_b32_e32 v120, 0xffff0000, v120
	v_mul_f32_e32 v77, v77, v120
	v_mul_f32_e32 v77, v119, v77
	v_add_f32_e32 v78, v78, v62
	v_mul_f32_e32 v82, 0xc1000000, v82
	v_fmac_f32_dpp v77, v77, v81 row_shl:1 row_mask:0xf bank_mask:0xf bound_ctrl:1
	v_mul_f32_dpp v81, v81, v81 row_shl:1 row_mask:0xf bank_mask:0xf
	v_mul_f32_e32 v78, 0xbfb8aa3b, v78
	v_mul_f32_e32 v82, v58, v82
	v_exp_f32_e32 v78, v78
	v_mul_f32_e32 v82, 0x3fb8aa3b, v82
	v_add_f32_e32 v83, v83, v67
	v_fmac_f32_dpp v77, v77, v81 row_shl:2 row_mask:0xf bank_mask:0xf bound_ctrl:1
	v_mul_f32_dpp v81, v81, v81 row_shl:2 row_mask:0xf bank_mask:0xf
	v_exp_f32_e32 v82, v82
	v_mul_f32_e32 v83, 0xbfb8aa3b, v83
	v_exp_f32_e32 v83, v83
	v_fmac_f32_dpp v77, v77, v81 row_shl:4 row_mask:0xf bank_mask:0xf bound_ctrl:1
	v_mul_f32_dpp v81, v81, v81 row_shl:4 row_mask:0xf bank_mask:0xf
	v_add_f32_e32 v78, 1.0, v78
	v_fmac_f32_dpp v77, v77, v81 row_shl:8 row_mask:0xf bank_mask:0xf bound_ctrl:1
	v_mul_f32_dpp v81, v81, v81 row_shl:8 row_mask:0xf bank_mask:0xf
	v_rcp_f32_e32 v78, v78
	v_fma_f32 v119, -v82, v82, 1.0
	v_sqrt_f32_e32 v119, v119
	v_add_f32_e32 v83, 1.0, v83
	v_rcp_f32_e32 v83, v83
	v_lshlrev_b32_e32 v122, 16, v121
	v_mul_f32_e32 v78, v78, v122
	v_mul_f32_e32 v78, v119, v78
	v_add_f32_e32 v79, v79, v63
	v_mul_f32_e32 v83, 0xc1000000, v83
	v_fmac_f32_dpp v78, v78, v82 row_shl:1 row_mask:0xf bank_mask:0xf bound_ctrl:1
	v_mul_f32_dpp v82, v82, v82 row_shl:1 row_mask:0xf bank_mask:0xf
	v_mul_f32_e32 v79, 0xbfb8aa3b, v79
	v_mul_f32_e32 v83, v59, v83
	v_exp_f32_e32 v79, v79
	v_mul_f32_e32 v83, 0x3fb8aa3b, v83
	v_fmac_f32_dpp v78, v78, v82 row_shl:2 row_mask:0xf bank_mask:0xf bound_ctrl:1
	v_mul_f32_dpp v82, v82, v82 row_shl:2 row_mask:0xf bank_mask:0xf
	v_exp_f32_e32 v83, v83
	v_add_f32_e32 v72, v72, v64
	v_fmac_f32_dpp v78, v78, v82 row_shl:4 row_mask:0xf bank_mask:0xf bound_ctrl:1
	v_mul_f32_dpp v82, v82, v82 row_shl:4 row_mask:0xf bank_mask:0xf
	v_mul_f32_e32 v72, 0xbfb8aa3b, v72
	v_add_f32_e32 v79, 1.0, v79
	v_exp_f32_e32 v72, v72
	v_fmac_f32_dpp v78, v78, v82 row_shl:8 row_mask:0xf bank_mask:0xf bound_ctrl:1
	v_mul_f32_dpp v82, v82, v82 row_shl:8 row_mask:0xf bank_mask:0xf
	v_rcp_f32_e32 v79, v79
	v_fma_f32 v119, -v83, v83, 1.0
	v_sqrt_f32_e32 v119, v119
	v_and_b32_e32 v121, 0xffff0000, v121
	v_add_f32_e32 v72, 1.0, v72
	v_mul_f32_e32 v79, v79, v121
	v_rcp_f32_e32 v72, v72
	v_mul_f32_e32 v79, v119, v79
	v_add_f32_e32 v68, v68, v60
	s_nop 0
	v_fmac_f32_dpp v79, v79, v83 row_shl:1 row_mask:0xf bank_mask:0xf bound_ctrl:1
	v_mul_f32_dpp v83, v83, v83 row_shl:1 row_mask:0xf bank_mask:0xf
	v_mul_f32_e32 v72, 0xc1000000, v72
	v_fmac_f32_dpp v79, v79, v83 row_shl:2 row_mask:0xf bank_mask:0xf bound_ctrl:1
	v_mul_f32_e32 v68, 0xbfb8aa3b, v68
	v_mul_f32_e32 v72, v56, v72
	v_mul_f32_dpp v83, v83, v83 row_shl:2 row_mask:0xf bank_mask:0xf
	v_exp_f32_e32 v68, v68
	v_mul_f32_e32 v72, 0x3fb8aa3b, v72
	v_add_f32_e32 v73, v73, v65
	v_fmac_f32_dpp v79, v79, v83 row_shl:4 row_mask:0xf bank_mask:0xf bound_ctrl:1
	v_exp_f32_e32 v72, v72
	v_mul_f32_e32 v73, 0xbfb8aa3b, v73
	v_mul_f32_dpp v83, v83, v83 row_shl:4 row_mask:0xf bank_mask:0xf
	v_exp_f32_e32 v73, v73
	v_fmac_f32_dpp v79, v79, v83 row_shl:8 row_mask:0xf bank_mask:0xf bound_ctrl:1
	ds_read_b64 v[120:121], v118 offset:16896
	v_add_f32_e32 v68, 1.0, v68
	v_rcp_f32_e32 v68, v68
	v_fma_f32 v123, -v72, v72, 1.0
	v_add_f32_e32 v52, v52, v64
	v_sqrt_f32_e32 v123, v123
	v_add_f32_e32 v73, 1.0, v73
	v_mul_f32_e32 v52, 0xbfb8aa3b, v52
	v_rcp_f32_e32 v73, v73
	v_exp_f32_e32 v52, v52
	v_mul_f32_dpp v83, v83, v83 row_shl:8 row_mask:0xf bank_mask:0xf
	s_waitcnt lgkmcnt(0)
; #define LAS __attribute__((address_space(3)))
; __device__ __forceinline__ float fsigmoid(float x) { return __builtin_amdgcn_rcpf(1.0f + __expf(-x)); }
; template <int PASS, bool REV> ...
;     ...
;         const int ch = blk * 64 + ng * 16 + fq * 4; const f32x4 sp = *(const LAS f32x4*)(cst + ch), bav = *(const LAS f32x4*)(cst + 256 + ch), bxv = *(const LAS f32x4*)(cst + 512 + ch);
; #pragma unroll
;         for (int tg = 0; tg < 4; ++tg) { const v2u uw = *(const LAS v2u*)(UB + (tg * 16 + fr) * 264 + ch); const float uv[4] = {bflo(uw.x), bfhi(uw.x), bflo(uw.y), bfhi(uw.y)};
; #pragma unroll
;             for (int j = 0; j < 4; ++j) { const float r = fsigmoid(aa[tg][j] + bav[j]), ig = fsigmoid(ax[tg][j] + bxv[j]); const float la = -8.0f * r * sp[j];
;                 float Av = __expf(la); const float om = __builtin_fmaf(-Av, Av, 1.0f);
;                 float Bv = __builtin_amdgcn_sqrtf(om) * (ig * uv[j]);
;                 rg_scan_step<REV, 1>(Av, Bv); rg_scan_step<REV, 2>(Av, Bv); rg_scan_step<REV, 4>(Av, Bv); rg_scan_step<REV, 8>(Av, Bv);
;                 aa[tg][j] = Av; ax[tg][j] = Bv; } }
	v_lshlrev_b32_e32 v119, 16, v120
	v_mul_f32_e32 v68, v68, v119
	v_mul_f32_e32 v68, v123, v68
	v_add_f32_e32 v70, v70, v62
	v_add_f32_e32 v69, v69, v61
	v_mul_f32_e32 v73, 0xc1000000, v73
	v_mul_f32_e32 v70, 0xbfb8aa3b, v70
	v_add_f32_e32 v52, 1.0, v52
	v_fmac_f32_dpp v68, v68, v72 row_shl:1 row_mask:0xf bank_mask:0xf bound_ctrl:1
	v_mul_f32_dpp v72, v72, v72 row_shl:1 row_mask:0xf bank_mask:0xf
	v_mul_f32_e32 v69, 0xbfb8aa3b, v69
	v_mul_f32_e32 v73, v57, v73
	v_exp_f32_e32 v70, v70
	v_rcp_f32_e32 v52, v52
	v_exp_f32_e32 v69, v69
	v_mul_f32_e32 v73, 0x3fb8aa3b, v73
	v_add_f32_e32 v74, v74, v66
	v_fmac_f32_dpp v68, v68, v72 row_shl:2 row_mask:0xf bank_mask:0xf bound_ctrl:1
	v_mul_f32_dpp v72, v72, v72 row_shl:2 row_mask:0xf bank_mask:0xf
	v_exp_f32_e32 v73, v73
	v_mul_f32_e32 v74, 0xbfb8aa3b, v74
	v_exp_f32_e32 v74, v74
	v_add_f32_e32 v71, v71, v63
	v_fmac_f32_dpp v68, v68, v72 row_shl:4 row_mask:0xf bank_mask:0xf bound_ctrl:1
	v_mul_f32_dpp v72, v72, v72 row_shl:4 row_mask:0xf bank_mask:0xf
	v_add_f32_e32 v70, 1.0, v70
	v_mul_f32_e32 v71, 0xbfb8aa3b, v71
	v_add_f32_e32 v48, v48, v60
	v_mul_f32_e32 v52, 0xc1000000, v52
	v_add_f32_e32 v69, 1.0, v69
	v_rcp_f32_e32 v70, v70
	v_exp_f32_e32 v71, v71
	v_mul_f32_e32 v48, 0xbfb8aa3b, v48
	v_mul_f32_e32 v52, v56, v52
	v_fmac_f32_dpp v68, v68, v72 row_shl:8 row_mask:0xf bank_mask:0xf bound_ctrl:1
	v_mul_f32_dpp v72, v72, v72 row_shl:8 row_mask:0xf bank_mask:0xf
	v_rcp_f32_e32 v69, v69
	v_fma_f32 v119, -v73, v73, 1.0
	v_exp_f32_e32 v48, v48
	v_mul_f32_e32 v52, 0x3fb8aa3b, v52
	v_sqrt_f32_e32 v119, v119
	v_add_f32_e32 v74, 1.0, v74
	v_exp_f32_e32 v52, v52
	v_lshlrev_b32_e32 v122, 16, v121
	v_rcp_f32_e32 v74, v74
	v_and_b32_e32 v120, 0xffff0000, v120
	v_mul_f32_e32 v70, v70, v122
	v_add_f32_e32 v71, 1.0, v71
	ds_read_b64 v[122:123], v118 offset:25344
	v_mul_f32_e32 v69, v69, v120
	v_rcp_f32_e32 v71, v71
	v_add_f32_e32 v48, 1.0, v48
	v_mul_f32_e32 v69, v119, v69
	v_rcp_f32_e32 v48, v48
	v_fma_f32 v56, -v52, v52, 1.0
	v_mul_f32_e32 v74, 0xc1000000, v74
	v_sqrt_f32_e32 v56, v56
	v_and_b32_e32 v121, 0xffff0000, v121
	v_fmac_f32_dpp v69, v69, v73 row_shl:1 row_mask:0xf bank_mask:0xf bound_ctrl:1
	v_mul_f32_dpp v73, v73, v73 row_shl:1 row_mask:0xf bank_mask:0xf
	v_mul_f32_e32 v74, v58, v74
	v_mul_f32_e32 v74, 0x3fb8aa3b, v74
	v_add_f32_e32 v75, v75, v67
	v_mul_f32_e32 v71, v71, v121
	s_waitcnt lgkmcnt(0)
	v_lshlrev_b32_e32 v121, 16, v122
	v_fmac_f32_dpp v69, v69, v73 row_shl:2 row_mask:0xf bank_mask:0xf bound_ctrl:1
	v_mul_f32_dpp v73, v73, v73 row_shl:2 row_mask:0xf bank_mask:0xf
	v_exp_f32_e32 v74, v74
	v_mul_f32_e32 v75, 0xbfb8aa3b, v75
	v_mul_f32_e32 v48, v48, v121
	v_exp_f32_e32 v75, v75
	v_mul_f32_e32 v56, v56, v48
	v_fmac_f32_dpp v69, v69, v73 row_shl:4 row_mask:0xf bank_mask:0xf bound_ctrl:1
	v_mul_f32_dpp v73, v73, v73 row_shl:4 row_mask:0xf bank_mask:0xf
	v_mov_b32_e32 v48, v52
	v_fmac_f32_dpp v56, v56, v52 row_shl:1 row_mask:0xf bank_mask:0xf bound_ctrl:1
	v_mul_f32_dpp v48, v52, v52 row_shl:1 row_mask:0xf bank_mask:0xf
	v_fmac_f32_dpp v69, v69, v73 row_shl:8 row_mask:0xf bank_mask:0xf bound_ctrl:1
	v_mul_f32_dpp v73, v73, v73 row_shl:8 row_mask:0xf bank_mask:0xf
	v_fma_f32 v119, -v74, v74, 1.0
	v_sqrt_f32_e32 v119, v119
	v_add_f32_e32 v75, 1.0, v75
	v_fmac_f32_dpp v56, v56, v48 row_shl:2 row_mask:0xf bank_mask:0xf bound_ctrl:1
	v_mul_f32_dpp v48, v48, v48 row_shl:2 row_mask:0xf bank_mask:0xf
	v_rcp_f32_e32 v75, v75
	v_fmac_f32_dpp v56, v56, v48 row_shl:4 row_mask:0xf bank_mask:0xf bound_ctrl:1
	v_mul_f32_dpp v48, v48, v48 row_shl:4 row_mask:0xf bank_mask:0xf
	v_mul_f32_e32 v70, v119, v70
	v_fmac_f32_dpp v56, v56, v48 row_shl:8 row_mask:0xf bank_mask:0xf bound_ctrl:1
	v_mul_f32_dpp v48, v48, v48 row_shl:8 row_mask:0xf bank_mask:0xf
	v_add_f32_e32 v52, v53, v65
	v_mul_f32_e32 v75, 0xc1000000, v75
	v_mul_f32_e32 v52, 0xbfb8aa3b, v52
	v_fmac_f32_dpp v70, v70, v74 row_shl:1 row_mask:0xf bank_mask:0xf bound_ctrl:1
	v_mul_f32_dpp v74, v74, v74 row_shl:1 row_mask:0xf bank_mask:0xf
	v_mul_f32_e32 v75, v59, v75
	v_exp_f32_e32 v52, v52
	v_mul_f32_e32 v75, 0x3fb8aa3b, v75
	v_fmac_f32_dpp v70, v70, v74 row_shl:2 row_mask:0xf bank_mask:0xf bound_ctrl:1
	v_mul_f32_dpp v74, v74, v74 row_shl:2 row_mask:0xf bank_mask:0xf
	v_exp_f32_e32 v75, v75
	v_fmac_f32_dpp v70, v70, v74 row_shl:4 row_mask:0xf bank_mask:0xf bound_ctrl:1
	v_mul_f32_dpp v74, v74, v74 row_shl:4 row_mask:0xf bank_mask:0xf
	v_add_f32_e32 v52, 1.0, v52
	v_rcp_f32_e32 v52, v52
	v_fmac_f32_dpp v70, v70, v74 row_shl:8 row_mask:0xf bank_mask:0xf bound_ctrl:1
	v_mul_f32_dpp v74, v74, v74 row_shl:8 row_mask:0xf bank_mask:0xf
	v_fma_f32 v119, -v75, v75, 1.0
	v_sqrt_f32_e32 v119, v119
	v_add_f32_e32 v49, v49, v61
	v_mul_f32_e32 v52, 0xc1000000, v52
	v_mul_f32_e32 v49, 0xbfb8aa3b, v49
	v_mul_f32_e32 v52, v57, v52
	v_mul_f32_e32 v71, v119, v71
	v_exp_f32_e32 v49, v49
	v_mul_f32_e32 v52, 0x3fb8aa3b, v52
	v_exp_f32_e32 v52, v52
	v_fmac_f32_dpp v71, v71, v75 row_shl:1 row_mask:0xf bank_mask:0xf bound_ctrl:1
	v_mul_f32_dpp v75, v75, v75 row_shl:1 row_mask:0xf bank_mask:0xf
	s_nop 0
	v_fmac_f32_dpp v71, v71, v75 row_shl:2 row_mask:0xf bank_mask:0xf bound_ctrl:1
	v_add_f32_e32 v49, 1.0, v49
	v_mul_f32_dpp v75, v75, v75 row_shl:2 row_mask:0xf bank_mask:0xf
	v_rcp_f32_e32 v49, v49
	v_fma_f32 v53, -v52, v52, 1.0
	v_fmac_f32_dpp v71, v71, v75 row_shl:4 row_mask:0xf bank_mask:0xf bound_ctrl:1
	v_sqrt_f32_e32 v53, v53
; #define LAS __attribute__((address_space(3)))
; __device__ __forceinline__ float fsigmoid(float x) { return __builtin_amdgcn_rcpf(1.0f + __expf(-x)); }
; __device__ __forceinline__ float bperm_f(int idx4, float x) { return __builtin_bit_cast(float, __builtin_amdgcn_ds_bpermute(idx4, __builtin_bit_cast(int, x))); }
; template <int PASS, bool REV> ...
;     ...
;         for (int tg = 0; tg < 4; ++tg) { const v2u uw = *(const LAS v2u*)(UB + (tg * 16 + fr) * 264 + ch); const float uv[4] = {bflo(uw.x), bfhi(uw.x), bflo(uw.y), bfhi(uw.y)};
; #pragma unroll
;             for (int j = 0; j < 4; ++j) { const float r = fsigmoid(aa[tg][j] + bav[j]), ig = fsigmoid(ax[tg][j] + bxv[j]); const float la = -8.0f * r * sp[j];
;                 float Av = __expf(la); const float om = __builtin_fmaf(-Av, Av, 1.0f);
;                 float Bv = __builtin_amdgcn_sqrtf(om) * (ig * uv[j]);
;                 rg_scan_step<REV, 1>(Av, Bv); rg_scan_step<REV, 2>(Av, Bv); rg_scan_step<REV, 4>(Av, Bv); rg_scan_step<REV, 8>(Av, Bv);
;                 aa[tg][j] = Av; ax[tg][j] = Bv; } }
;         const int lastl4 = ((lane & 48) | (REV ? 0 : 15)) << 2;
;         if (PASS == 1) {
;             f32x4 At = (f32x4){1.f, 1.f, 1.f, 1.f}, Bt = (f32x4){0.f, 0.f, 0.f, 0.f};
; #pragma unroll
;             for (int t4 = 0; t4 < 4; ++t4) { const int tg = REV ? 3 - t4 : t4;
; #pragma unroll
;                 for (int j = 0; j < 4; ++j) { const float ta = bperm_f(lastl4, aa[tg][j]), tb = bperm_f(lastl4, ax[tg][j]); Bt[j] = ta * Bt[j] + tb; At[j] = At[j] * ta; } }
;             if (fr == 0) { f32x4* cp = (f32x4*)(CAR + ((size_t)u * 2 + d) * 256 + ch); cp[0] = (f32x4){At[0], Bt[0], At[1], Bt[1]}; cp[1] = (f32x4){At[2], Bt[2], At[3], Bt[3]}; }
	v_mul_f32_dpp v75, v75, v75 row_shl:4 row_mask:0xf bank_mask:0xf
	v_fmac_f32_dpp v71, v71, v75 row_shl:8 row_mask:0xf bank_mask:0xf bound_ctrl:1
	v_and_b32_e32 v120, 0xffff0000, v122
	v_mul_f32_e32 v49, v49, v120
	v_mul_f32_e32 v53, v53, v49
	v_add_f32_e32 v50, v50, v62
	v_mov_b32_e32 v49, v52
	v_fmac_f32_dpp v53, v53, v52 row_shl:1 row_mask:0xf bank_mask:0xf bound_ctrl:1
	v_mul_f32_dpp v49, v52, v52 row_shl:1 row_mask:0xf bank_mask:0xf
	v_mul_f32_e32 v50, 0xbfb8aa3b, v50
	v_fmac_f32_dpp v53, v53, v49 row_shl:2 row_mask:0xf bank_mask:0xf bound_ctrl:1
	v_mul_f32_dpp v49, v49, v49 row_shl:2 row_mask:0xf bank_mask:0xf
	v_exp_f32_e32 v50, v50
	v_fmac_f32_dpp v53, v53, v49 row_shl:4 row_mask:0xf bank_mask:0xf bound_ctrl:1
	v_mul_f32_dpp v49, v49, v49 row_shl:4 row_mask:0xf bank_mask:0xf
	v_add_f32_e32 v50, 1.0, v50
	v_fmac_f32_dpp v53, v53, v49 row_shl:8 row_mask:0xf bank_mask:0xf bound_ctrl:1
	v_mul_f32_dpp v49, v49, v49 row_shl:8 row_mask:0xf bank_mask:0xf
	v_add_f32_e32 v52, v54, v66
	v_mul_f32_e32 v52, 0xbfb8aa3b, v52
	v_exp_f32_e32 v52, v52
	v_rcp_f32_e32 v50, v50
	v_add_f32_e32 v52, 1.0, v52
	v_rcp_f32_e32 v52, v52
	v_mul_f32_dpp v75, v75, v75 row_shl:8 row_mask:0xf bank_mask:0xf
	v_lshlrev_b32_e32 v119, 16, v123
	v_mul_f32_e32 v52, 0xc1000000, v52
	v_mul_f32_e32 v52, v58, v52
	v_mul_f32_e32 v52, 0x3fb8aa3b, v52
	v_exp_f32_e32 v52, v52
	v_mul_f32_e32 v50, v50, v119
	v_add_f32_e32 v51, v51, v63
	v_mul_f32_e32 v51, 0xbfb8aa3b, v51
	v_fma_f32 v54, -v52, v52, 1.0
	v_sqrt_f32_e32 v54, v54
	v_exp_f32_e32 v51, v51
	v_and_b32_e32 v118, 0xffff0000, v123
	ds_bpermute_b32 v48, v101, v48
	v_mul_f32_e32 v54, v54, v50
	v_add_f32_e32 v51, 1.0, v51
	v_mov_b32_e32 v50, v52
	v_fmac_f32_dpp v54, v54, v52 row_shl:1 row_mask:0xf bank_mask:0xf bound_ctrl:1
	v_mul_f32_dpp v50, v52, v52 row_shl:1 row_mask:0xf bank_mask:0xf
	v_rcp_f32_e32 v51, v51
	v_fmac_f32_dpp v54, v54, v50 row_shl:2 row_mask:0xf bank_mask:0xf bound_ctrl:1
	v_mul_f32_dpp v50, v50, v50 row_shl:2 row_mask:0xf bank_mask:0xf
	v_mul_f32_e32 v51, v51, v118
	v_fmac_f32_dpp v54, v54, v50 row_shl:4 row_mask:0xf bank_mask:0xf bound_ctrl:1
	v_mul_f32_dpp v50, v50, v50 row_shl:4 row_mask:0xf bank_mask:0xf
	ds_bpermute_b32 v49, v101, v49
	v_fmac_f32_dpp v54, v54, v50 row_shl:8 row_mask:0xf bank_mask:0xf bound_ctrl:1
	v_mul_f32_dpp v50, v50, v50 row_shl:8 row_mask:0xf bank_mask:0xf
	v_add_f32_e32 v52, v55, v67
	v_mul_f32_e32 v52, 0xbfb8aa3b, v52
	v_exp_f32_e32 v52, v52
	ds_bpermute_b32 v53, v101, v53
	ds_bpermute_b32 v50, v101, v50
	v_add_f32_e32 v52, 1.0, v52
	v_rcp_f32_e32 v52, v52
	ds_bpermute_b32 v54, v101, v54
	ds_bpermute_b32 v60, v101, v68
	ds_bpermute_b32 v61, v101, v69
	v_mul_f32_e32 v52, 0xc1000000, v52
	v_mul_f32_e32 v52, v59, v52
	v_mul_f32_e32 v52, 0x3fb8aa3b, v52
	v_exp_f32_e32 v52, v52
	ds_bpermute_b32 v58, v101, v74
	ds_bpermute_b32 v62, v101, v70
	ds_bpermute_b32 v59, v101, v75
	v_fma_f32 v55, -v52, v52, 1.0
	v_sqrt_f32_e32 v55, v55
	ds_bpermute_b32 v63, v101, v71
	ds_bpermute_b32 v64, v101, v80
	ds_bpermute_b32 v68, v101, v76
	v_mul_f32_e32 v55, v55, v51
	ds_bpermute_b32 v65, v101, v81
	v_mov_b32_e32 v51, v52
	v_fmac_f32_dpp v55, v55, v52 row_shl:1 row_mask:0xf bank_mask:0xf bound_ctrl:1
	v_mul_f32_dpp v51, v52, v52 row_shl:1 row_mask:0xf bank_mask:0xf
	ds_bpermute_b32 v69, v101, v77
	v_fmac_f32_dpp v55, v55, v51 row_shl:2 row_mask:0xf bank_mask:0xf bound_ctrl:1
	v_mul_f32_dpp v51, v51, v51 row_shl:2 row_mask:0xf bank_mask:0xf
	ds_bpermute_b32 v66, v101, v82
	v_fmac_f32_dpp v55, v55, v51 row_shl:4 row_mask:0xf bank_mask:0xf bound_ctrl:1
	v_mul_f32_dpp v51, v51, v51 row_shl:4 row_mask:0xf bank_mask:0xf
	ds_bpermute_b32 v70, v101, v78
	v_fmac_f32_dpp v55, v55, v51 row_shl:8 row_mask:0xf bank_mask:0xf bound_ctrl:1
	v_mul_f32_dpp v51, v51, v51 row_shl:8 row_mask:0xf bank_mask:0xf
	ds_bpermute_b32 v52, v101, v56
	ds_bpermute_b32 v51, v101, v51
	ds_bpermute_b32 v55, v101, v55
	ds_bpermute_b32 v56, v101, v72
	ds_bpermute_b32 v57, v101, v73
	ds_bpermute_b32 v67, v101, v83
	ds_bpermute_b32 v71, v101, v79
	ds_bpermute_b32 v72, v101, v88
	ds_bpermute_b32 v76, v101, v84
	ds_bpermute_b32 v73, v101, v89
	ds_bpermute_b32 v77, v101, v85
	ds_bpermute_b32 v74, v101, v90
	ds_bpermute_b32 v78, v101, v86
	ds_bpermute_b32 v75, v101, v91
	ds_bpermute_b32 v79, v101, v87
	s_and_saveexec_b64 s[0:1], s[36:37]
	s_cbranch_execz .LBB0_552
	s_waitcnt lgkmcnt(10)
	v_pk_mul_f32 v[80:81], v[48:49], v[56:57]
	v_pk_fma_f32 v[48:49], v[48:49], 0, v[52:53] op_sel_hi:[1,0,1]
	v_pk_mul_f32 v[80:81], v[80:81], v[64:65]
	v_pk_fma_f32 v[48:49], v[48:49], v[56:57], v[60:61]
	v_pk_mul_f32 v[82:83], v[50:51], v[58:59]
	v_pk_fma_f32 v[48:49], v[48:49], v[64:65], v[68:69]
	s_waitcnt lgkmcnt(5)
	v_pk_mul_f32 v[80:81], v[80:81], v[72:73]
	s_waitcnt lgkmcnt(4)
	v_pk_fma_f32 v[52:53], v[48:49], v[72:73], v[76:77]
	v_pk_fma_f32 v[48:49], v[50:51], 0, v[54:55] op_sel_hi:[1,0,1]
	v_pk_mul_f32 v[82:83], v[82:83], v[66:67]
	v_pk_fma_f32 v[48:49], v[48:49], v[58:59], v[62:63]
	s_waitcnt lgkmcnt(1)
	v_pk_mul_f32 v[82:83], v[82:83], v[74:75]
	v_pk_fma_f32 v[48:49], v[48:49], v[66:67], v[70:71]
	v_mov_b32_e32 v50, v80
	s_waitcnt lgkmcnt(0)
	v_pk_fma_f32 v[54:55], v[48:49], v[74:75], v[78:79]
	v_mov_b32_e32 v51, v52
	v_mov_b32_e32 v52, v81
	global_store_dwordx4 v[102:103], v[50:53], off offset:-16
	s_nop 1
	v_mov_b32_e32 v52, v82
	v_mov_b32_e32 v53, v54
	v_mov_b32_e32 v54, v83
	global_store_dwordx4 v[102:103], v[52:55], off
	s_branch .LBB0_552

; #define LAS __attribute__((address_space(3)))
; __device__ __forceinline__ float fsigmoid(float x) { return __builtin_amdgcn_rcpf(1.0f + __expf(-x)); }
; template <int PASS, bool REV> ...
;     ...
;     for (int ng = ng_lo; ng < ng_hi; ++ng) {
;         f32x4 aa[4], ax[4];
;         v2u gwv[4];
; #pragma unroll
;         for (int tg = 0; tg < 4; ++tg) { aa[tg] = (f32x4){0.f, 0.f, 0.f, 0.f}; ax[tg] = (f32x4){0.f, 0.f, 0.f, 0.f}; }
; #pragma unroll
;         for (int kk = 0; kk < 2; ++kk) { const bf16x8 wa = wcur[0][kk], wx = wcur[1][kk]; bf16x8 uf[4][2];
; #pragma unroll
;             for (int tg = 0; tg < 4; ++tg) uf[tg][kk] = *(const LAS bf16x8*)(UB + (tg * 16 + fr) * 264 + blk * 64 + kk * 32 + fq * 8);
; #pragma unroll
;             for (int tg = 0; tg < 4; ++tg) { aa[tg] = __builtin_amdgcn_mfma_f32_16x16x32_bf16(wa, uf[tg][kk], aa[tg], 0, 0, 0); ax[tg] = __builtin_amdgcn_mfma_f32_16x16x32_bf16(wx, uf[tg][kk], ax[tg], 0, 0, 0); } }
;         { const int ng1 = (ng + 1 < ng_hi) ? ng + 1 : ng_lo;
; #pragma unroll
;             for (int gt = 0; gt < 2; ++gt)
; #pragma unroll
;                 for (int kk = 0; kk < 2; ++kk) wcur[gt][kk] = *(const bf16x8*)(Wg + ((size_t)(gt * 4 + blk) * 64 + ng1 * 16 + fr) * 64 + kk * 32 + fq * 8); }
;         if (PASS == 2 && REV && emit) {
; #pragma unroll
;             for (int tg = 0; tg < 4; ++tg) gwv[tg] = *(const v2u*)(P + (size_t)(R0 + tg * 16 + fr) * PROJ + C_RGG + blk * 64 + ng * 16 + fq * 4); }
;         const int ch = blk * 64 + ng * 16 + fq * 4; const f32x4 sp = *(const LAS f32x4*)(cst + ch), bav = *(const LAS f32x4*)(cst + 256 + ch), bxv = *(const LAS f32x4*)(cst + 512 + ch);
; #pragma unroll
;         for (int tg = 0; tg < 4; ++tg) { const v2u uw = *(const LAS v2u*)(UB + (tg * 16 + fr) * 264 + ch); const float uv[4] = {bflo(uw.x), bfhi(uw.x), bflo(uw.y), bfhi(uw.y)};
; #pragma unroll
;             for (int j = 0; j < 4; ++j) { const float r = fsigmoid(aa[tg][j] + bav[j]), ig = fsigmoid(ax[tg][j] + bxv[j]); const float la = -8.0f * r * sp[j];
;                 float Av = __expf(la); const float om = __builtin_fmaf(-Av, Av, 1.0f);
;                 float Bv = __builtin_amdgcn_sqrtf(om) * (ig * uv[j]);
;                 rg_scan_step<REV, 1>(Av, Bv); rg_scan_step<REV, 2>(Av, Bv); rg_scan_step<REV, 4>(Av, Bv); rg_scan_step<REV, 8>(Av, Bv);
;                 aa[tg][j] = Av; ax[tg][j] = Bv; } }
.LBB0_568:
	s_add_i32 s12, s12, 1
	s_waitcnt vmcnt(0) lgkmcnt(7)
	v_mfma_f32_16x16x32_bf16 v[48:51], v[40:43], v[0:3], 0
	s_cmp_ge_u32 s12, s8
	s_cselect_b64 s[24:25], -1, 0
	s_cmp_lt_u32 s12, s8
	v_mfma_f32_16x16x32_bf16 v[52:55], v[44:47], v[0:3], 0
	s_cselect_b32 s0, s12, s9
	v_lshl_add_u32 v180, s0, 4, v105
	v_add_u32_e32 v103, 0, v116
	s_waitcnt lgkmcnt(5)
	v_mfma_f32_16x16x32_bf16 v[56:59], v[40:43], v[8:11], 0
	s_waitcnt lgkmcnt(3)
	v_mfma_f32_16x16x32_bf16 v[64:67], v[40:43], v[16:19], 0
	s_waitcnt lgkmcnt(1)
	v_mfma_f32_16x16x32_bf16 v[40:43], v[40:43], v[24:27], 0
	v_mfma_f32_16x16x32_bf16 v[60:63], v[44:47], v[8:11], 0
	v_mfma_f32_16x16x32_bf16 v[68:71], v[44:47], v[16:19], 0
	v_mfma_f32_16x16x32_bf16 v[44:47], v[44:47], v[24:27], 0
	v_mfma_f32_16x16x32_bf16 v[88:91], v[32:35], v[4:7], v[48:51]
	v_mfma_f32_16x16x32_bf16 v[84:87], v[36:39], v[4:7], v[52:55]
	v_mfma_f32_16x16x32_bf16 v[80:83], v[32:35], v[12:15], v[56:59]
	v_mfma_f32_16x16x32_bf16 v[72:75], v[32:35], v[20:23], v[64:67]
	s_waitcnt lgkmcnt(0)
	v_mfma_f32_16x16x32_bf16 v[52:55], v[32:35], v[28:31], v[40:43]
	v_lshlrev_b64 v[32:33], 7, v[180:181]
	v_add_u32_e32 v180, 0x100, v180
	v_lshl_add_u64 v[32:33], v[94:95], 0, v[32:33]
	v_mfma_f32_16x16x32_bf16 v[76:79], v[36:39], v[12:15], v[60:63]
	global_load_dwordx4 v[40:43], v[32:33], off
	s_nop 0
	global_load_dwordx4 v[32:35], v[32:33], off offset:64
	v_add_u32_e32 v60, 0, v117
	v_add_u32_e32 v61, 0x11400, v60
	v_mfma_f32_16x16x32_bf16 v[68:71], v[36:39], v[20:23], v[68:71]
	v_add_u32_e32 v56, 0x11000, v60
	v_add_u32_e32 v60, 0x11800, v60
	v_mfma_f32_16x16x32_bf16 v[48:51], v[36:39], v[28:31], v[44:47]
	v_lshlrev_b64 v[36:37], 7, v[180:181]
	v_lshl_add_u64 v[36:37], v[94:95], 0, v[36:37]
	s_nop 0
	global_load_dwordx4 v[44:47], v[36:37], off
	s_nop 0
	global_load_dwordx4 v[36:39], v[36:37], off offset:64
	ds_read_b128 v[64:67], v61
	ds_read_b64 v[118:119], v103
	ds_read_b128 v[56:59], v56
	ds_read_b128 v[60:63], v60
	s_waitcnt lgkmcnt(3)
	v_add_f32_e32 v88, v88, v64
	v_mul_f32_e32 v88, 0xbfb8aa3b, v88
	v_exp_f32_e32 v88, v88
	s_waitcnt lgkmcnt(0)
	v_add_f32_e32 v84, v84, v60
	v_mul_f32_e32 v84, 0xbfb8aa3b, v84
	v_exp_f32_e32 v84, v84
	v_add_f32_e32 v88, 1.0, v88
	v_rcp_f32_e32 v88, v88
	v_add_f32_e32 v89, v89, v65
	v_mul_f32_e32 v89, 0xbfb8aa3b, v89
	v_exp_f32_e32 v89, v89
	v_mul_f32_e32 v88, 0xc1000000, v88
	v_mul_f32_e32 v88, v56, v88
	v_mul_f32_e32 v88, 0x3fb8aa3b, v88
	v_exp_f32_e32 v88, v88
	v_add_f32_e32 v84, 1.0, v84
	v_rcp_f32_e32 v84, v84
	v_add_f32_e32 v89, 1.0, v89
	v_fma_f32 v122, -v88, v88, 1.0
	v_sqrt_f32_e32 v122, v122
	v_rcp_f32_e32 v89, v89
	v_lshlrev_b32_e32 v120, 16, v118
	v_mul_f32_e32 v84, v84, v120
	v_mul_f32_e32 v84, v84, v122
	v_add_f32_e32 v85, v85, v61
	v_mul_f32_e32 v89, 0xc1000000, v89
	v_fmac_f32_dpp v84, v84, v88 row_shr:1 row_mask:0xf bank_mask:0xf bound_ctrl:1
	v_mul_f32_dpp v88, v88, v88 row_shr:1 row_mask:0xf bank_mask:0xf
	v_mul_f32_e32 v85, 0xbfb8aa3b, v85
	v_mul_f32_e32 v89, v57, v89
	v_exp_f32_e32 v85, v85
	v_mul_f32_e32 v89, 0x3fb8aa3b, v89
	v_add_f32_e32 v90, v90, v66
	v_fmac_f32_dpp v84, v84, v88 row_shr:2 row_mask:0xf bank_mask:0xf bound_ctrl:1
	v_mul_f32_dpp v88, v88, v88 row_shr:2 row_mask:0xf bank_mask:0xf
	v_exp_f32_e32 v89, v89
	v_mul_f32_e32 v90, 0xbfb8aa3b, v90
	v_exp_f32_e32 v90, v90
	v_fmac_f32_dpp v84, v84, v88 row_shr:4 row_mask:0xf bank_mask:0xf bound_ctrl:1
	v_mul_f32_dpp v88, v88, v88 row_shr:4 row_mask:0xf bank_mask:0xf
	v_add_f32_e32 v85, 1.0, v85
	v_fmac_f32_dpp v84, v84, v88 row_shr:8 row_mask:0xf bank_mask:0xf bound_ctrl:1
	v_mul_f32_dpp v88, v88, v88 row_shr:8 row_mask:0xf bank_mask:0xf
	v_rcp_f32_e32 v85, v85
	v_fma_f32 v120, -v89, v89, 1.0
	v_sqrt_f32_e32 v120, v120
	v_add_f32_e32 v90, 1.0, v90
	v_rcp_f32_e32 v90, v90
	v_and_b32_e32 v118, 0xffff0000, v118
	v_mul_f32_e32 v85, v85, v118
	v_mul_f32_e32 v85, v85, v120
	v_add_f32_e32 v86, v86, v62
	v_mul_f32_e32 v90, 0xc1000000, v90
	v_fmac_f32_dpp v85, v85, v89 row_shr:1 row_mask:0xf bank_mask:0xf bound_ctrl:1
	v_mul_f32_dpp v89, v89, v89 row_shr:1 row_mask:0xf bank_mask:0xf
	v_mul_f32_e32 v86, 0xbfb8aa3b, v86
	v_mul_f32_e32 v90, v58, v90
	v_exp_f32_e32 v86, v86
	v_mul_f32_e32 v90, 0x3fb8aa3b, v90
	v_add_f32_e32 v91, v91, v67
	v_fmac_f32_dpp v85, v85, v89 row_shr:2 row_mask:0xf bank_mask:0xf bound_ctrl:1
	v_mul_f32_dpp v89, v89, v89 row_shr:2 row_mask:0xf bank_mask:0xf
	v_exp_f32_e32 v90, v90
	v_mul_f32_e32 v91, 0xbfb8aa3b, v91
	v_exp_f32_e32 v91, v91
	v_fmac_f32_dpp v85, v85, v89 row_shr:4 row_mask:0xf bank_mask:0xf bound_ctrl:1
	v_mul_f32_dpp v89, v89, v89 row_shr:4 row_mask:0xf bank_mask:0xf
	v_add_f32_e32 v86, 1.0, v86
	v_fmac_f32_dpp v85, v85, v89 row_shr:8 row_mask:0xf bank_mask:0xf bound_ctrl:1
	v_mul_f32_dpp v89, v89, v89 row_shr:8 row_mask:0xf bank_mask:0xf
	v_rcp_f32_e32 v86, v86
	v_fma_f32 v118, -v90, v90, 1.0
	v_sqrt_f32_e32 v118, v118
	v_add_f32_e32 v91, 1.0, v91
	v_rcp_f32_e32 v91, v91
	v_lshlrev_b32_e32 v121, 16, v119
	v_mul_f32_e32 v86, v86, v121
	v_mul_f32_e32 v86, v86, v118
	v_add_f32_e32 v87, v87, v63
	v_mul_f32_e32 v91, 0xc1000000, v91
	v_fmac_f32_dpp v86, v86, v90 row_shr:1 row_mask:0xf bank_mask:0xf bound_ctrl:1
	v_mul_f32_dpp v90, v90, v90 row_shr:1 row_mask:0xf bank_mask:0xf
	v_mul_f32_e32 v87, 0xbfb8aa3b, v87
	v_mul_f32_e32 v91, v59, v91
	v_exp_f32_e32 v87, v87
	v_mul_f32_e32 v91, 0x3fb8aa3b, v91
	v_fmac_f32_dpp v86, v86, v90 row_shr:2 row_mask:0xf bank_mask:0xf bound_ctrl:1
	v_mul_f32_dpp v90, v90, v90 row_shr:2 row_mask:0xf bank_mask:0xf
	v_exp_f32_e32 v91, v91
	v_add_f32_e32 v80, v80, v64
	v_fmac_f32_dpp v86, v86, v90 row_shr:4 row_mask:0xf bank_mask:0xf bound_ctrl:1
; #define LAS __attribute__((address_space(3)))
; __device__ __forceinline__ float fsigmoid(float x) { return __builtin_amdgcn_rcpf(1.0f + __expf(-x)); }
; template <int PASS, bool REV> ...
;     ...
;         for (int tg = 0; tg < 4; ++tg) { const v2u uw = *(const LAS v2u*)(UB + (tg * 16 + fr) * 264 + ch); const float uv[4] = {bflo(uw.x), bfhi(uw.x), bflo(uw.y), bfhi(uw.y)};
; #pragma unroll
;             for (int j = 0; j < 4; ++j) { const float r = fsigmoid(aa[tg][j] + bav[j]), ig = fsigmoid(ax[tg][j] + bxv[j]); const float la = -8.0f * r * sp[j];
;                 float Av = __expf(la); const float om = __builtin_fmaf(-Av, Av, 1.0f);
;                 float Bv = __builtin_amdgcn_sqrtf(om) * (ig * uv[j]);
;                 rg_scan_step<REV, 1>(Av, Bv); rg_scan_step<REV, 2>(Av, Bv); rg_scan_step<REV, 4>(Av, Bv); rg_scan_step<REV, 8>(Av, Bv);
;                 aa[tg][j] = Av; ax[tg][j] = Bv; } }
	v_mul_f32_dpp v90, v90, v90 row_shr:4 row_mask:0xf bank_mask:0xf
	v_mul_f32_e32 v80, 0xbfb8aa3b, v80
	v_add_f32_e32 v87, 1.0, v87
	v_exp_f32_e32 v80, v80
	v_fmac_f32_dpp v86, v86, v90 row_shr:8 row_mask:0xf bank_mask:0xf bound_ctrl:1
	v_mul_f32_dpp v90, v90, v90 row_shr:8 row_mask:0xf bank_mask:0xf
	v_rcp_f32_e32 v87, v87
	v_fma_f32 v118, -v91, v91, 1.0
	v_sqrt_f32_e32 v118, v118
	v_and_b32_e32 v119, 0xffff0000, v119
	v_add_f32_e32 v80, 1.0, v80
	v_mul_f32_e32 v87, v87, v119
	v_rcp_f32_e32 v80, v80
	v_mul_f32_e32 v87, v87, v118
	v_add_f32_e32 v76, v76, v60
	s_nop 0
	v_fmac_f32_dpp v87, v87, v91 row_shr:1 row_mask:0xf bank_mask:0xf bound_ctrl:1
	v_mul_f32_dpp v91, v91, v91 row_shr:1 row_mask:0xf bank_mask:0xf
	v_mul_f32_e32 v80, 0xc1000000, v80
	v_fmac_f32_dpp v87, v87, v91 row_shr:2 row_mask:0xf bank_mask:0xf bound_ctrl:1
	v_mul_f32_dpp v91, v91, v91 row_shr:2 row_mask:0xf bank_mask:0xf
	v_mul_f32_e32 v76, 0xbfb8aa3b, v76
	v_mul_f32_e32 v80, v56, v80
	v_exp_f32_e32 v76, v76
	v_mul_f32_e32 v80, 0x3fb8aa3b, v80
	v_add_f32_e32 v81, v81, v65
	v_fmac_f32_dpp v87, v87, v91 row_shr:4 row_mask:0xf bank_mask:0xf bound_ctrl:1
	v_mul_f32_dpp v91, v91, v91 row_shr:4 row_mask:0xf bank_mask:0xf
	v_exp_f32_e32 v80, v80
	v_mul_f32_e32 v81, 0xbfb8aa3b, v81
	v_exp_f32_e32 v81, v81
	v_fmac_f32_dpp v87, v87, v91 row_shr:8 row_mask:0xf bank_mask:0xf bound_ctrl:1
	v_mul_f32_dpp v91, v91, v91 row_shr:8 row_mask:0xf bank_mask:0xf
	ds_read_b64 v[118:119], v103 offset:8448
	v_add_f32_e32 v76, 1.0, v76
	v_rcp_f32_e32 v76, v76
	v_fma_f32 v122, -v80, v80, 1.0
	v_sqrt_f32_e32 v122, v122
	v_add_f32_e32 v81, 1.0, v81
	v_rcp_f32_e32 v81, v81
	s_waitcnt lgkmcnt(0)
	v_lshlrev_b32_e32 v120, 16, v118
	v_mul_f32_e32 v76, v76, v120
	v_mul_f32_e32 v76, v122, v76
	v_add_f32_e32 v77, v77, v61
	v_mul_f32_e32 v81, 0xc1000000, v81
	v_fmac_f32_dpp v76, v76, v80 row_shr:1 row_mask:0xf bank_mask:0xf bound_ctrl:1
	v_mul_f32_dpp v80, v80, v80 row_shr:1 row_mask:0xf bank_mask:0xf
	v_mul_f32_e32 v77, 0xbfb8aa3b, v77
	v_mul_f32_e32 v81, v57, v81
	v_exp_f32_e32 v77, v77
	v_mul_f32_e32 v81, 0x3fb8aa3b, v81
	v_add_f32_e32 v82, v82, v66
	v_fmac_f32_dpp v76, v76, v80 row_shr:2 row_mask:0xf bank_mask:0xf bound_ctrl:1
	v_mul_f32_dpp v80, v80, v80 row_shr:2 row_mask:0xf bank_mask:0xf
	v_exp_f32_e32 v81, v81
	v_mul_f32_e32 v82, 0xbfb8aa3b, v82
	v_exp_f32_e32 v82, v82
	v_fmac_f32_dpp v76, v76, v80 row_shr:4 row_mask:0xf bank_mask:0xf bound_ctrl:1
	v_mul_f32_dpp v80, v80, v80 row_shr:4 row_mask:0xf bank_mask:0xf
	v_add_f32_e32 v77, 1.0, v77
	v_fmac_f32_dpp v76, v76, v80 row_shr:8 row_mask:0xf bank_mask:0xf bound_ctrl:1
	v_mul_f32_dpp v80, v80, v80 row_shr:8 row_mask:0xf bank_mask:0xf
	v_rcp_f32_e32 v77, v77
	v_fma_f32 v120, -v81, v81, 1.0
	v_sqrt_f32_e32 v120, v120
	v_add_f32_e32 v82, 1.0, v82
	v_rcp_f32_e32 v82, v82
	v_and_b32_e32 v118, 0xffff0000, v118
	v_mul_f32_e32 v77, v77, v118
	v_mul_f32_e32 v77, v120, v77
	v_add_f32_e32 v78, v78, v62
	v_mul_f32_e32 v82, 0xc1000000, v82
	v_fmac_f32_dpp v77, v77, v81 row_shr:1 row_mask:0xf bank_mask:0xf bound_ctrl:1
	v_mul_f32_dpp v81, v81, v81 row_shr:1 row_mask:0xf bank_mask:0xf
	v_mul_f32_e32 v78, 0xbfb8aa3b, v78
	v_mul_f32_e32 v82, v58, v82
	v_exp_f32_e32 v78, v78
	v_mul_f32_e32 v82, 0x3fb8aa3b, v82
	v_add_f32_e32 v83, v83, v67
	v_fmac_f32_dpp v77, v77, v81 row_shr:2 row_mask:0xf bank_mask:0xf bound_ctrl:1
	v_mul_f32_dpp v81, v81, v81 row_shr:2 row_mask:0xf bank_mask:0xf
	v_exp_f32_e32 v82, v82
	v_mul_f32_e32 v83, 0xbfb8aa3b, v83
	v_exp_f32_e32 v83, v83
	v_fmac_f32_dpp v77, v77, v81 row_shr:4 row_mask:0xf bank_mask:0xf bound_ctrl:1
	v_mul_f32_dpp v81, v81, v81 row_shr:4 row_mask:0xf bank_mask:0xf
	v_add_f32_e32 v78, 1.0, v78
	v_fmac_f32_dpp v77, v77, v81 row_shr:8 row_mask:0xf bank_mask:0xf bound_ctrl:1
	v_mul_f32_dpp v81, v81, v81 row_shr:8 row_mask:0xf bank_mask:0xf
	v_rcp_f32_e32 v78, v78
	v_fma_f32 v118, -v82, v82, 1.0
	v_sqrt_f32_e32 v118, v118
	v_add_f32_e32 v83, 1.0, v83
	v_rcp_f32_e32 v83, v83
	v_lshlrev_b32_e32 v121, 16, v119
	v_mul_f32_e32 v78, v78, v121
	v_mul_f32_e32 v78, v118, v78
	v_add_f32_e32 v79, v79, v63
	v_mul_f32_e32 v83, 0xc1000000, v83
	v_fmac_f32_dpp v78, v78, v82 row_shr:1 row_mask:0xf bank_mask:0xf bound_ctrl:1
	v_mul_f32_dpp v82, v82, v82 row_shr:1 row_mask:0xf bank_mask:0xf
	v_mul_f32_e32 v79, 0xbfb8aa3b, v79
	v_mul_f32_e32 v83, v59, v83
	v_exp_f32_e32 v79, v79
	v_mul_f32_e32 v83, 0x3fb8aa3b, v83
	v_fmac_f32_dpp v78, v78, v82 row_shr:2 row_mask:0xf bank_mask:0xf bound_ctrl:1
	v_mul_f32_dpp v82, v82, v82 row_shr:2 row_mask:0xf bank_mask:0xf
	v_exp_f32_e32 v83, v83
	v_add_f32_e32 v72, v72, v64
	v_fmac_f32_dpp v78, v78, v82 row_shr:4 row_mask:0xf bank_mask:0xf bound_ctrl:1
	v_mul_f32_dpp v82, v82, v82 row_shr:4 row_mask:0xf bank_mask:0xf
	v_mul_f32_e32 v72, 0xbfb8aa3b, v72
	v_add_f32_e32 v79, 1.0, v79
	v_exp_f32_e32 v72, v72
	v_fmac_f32_dpp v78, v78, v82 row_shr:8 row_mask:0xf bank_mask:0xf bound_ctrl:1
	v_mul_f32_dpp v82, v82, v82 row_shr:8 row_mask:0xf bank_mask:0xf
	v_rcp_f32_e32 v79, v79
	v_fma_f32 v118, -v83, v83, 1.0
	v_sqrt_f32_e32 v118, v118
	v_and_b32_e32 v119, 0xffff0000, v119
	v_add_f32_e32 v72, 1.0, v72
	v_mul_f32_e32 v79, v79, v119
	v_rcp_f32_e32 v72, v72
	v_mul_f32_e32 v79, v118, v79
	v_add_f32_e32 v68, v68, v60
	s_nop 0
	v_fmac_f32_dpp v79, v79, v83 row_shr:1 row_mask:0xf bank_mask:0xf bound_ctrl:1
	v_mul_f32_dpp v83, v83, v83 row_shr:1 row_mask:0xf bank_mask:0xf
	v_mul_f32_e32 v72, 0xc1000000, v72
	v_fmac_f32_dpp v79, v79, v83 row_shr:2 row_mask:0xf bank_mask:0xf bound_ctrl:1
	v_mul_f32_dpp v83, v83, v83 row_shr:2 row_mask:0xf bank_mask:0xf
	v_mul_f32_e32 v68, 0xbfb8aa3b, v68
	v_mul_f32_e32 v72, v56, v72
	v_exp_f32_e32 v68, v68
	v_mul_f32_e32 v72, 0x3fb8aa3b, v72
	v_add_f32_e32 v73, v73, v65
	v_fmac_f32_dpp v79, v79, v83 row_shr:4 row_mask:0xf bank_mask:0xf bound_ctrl:1
	v_mul_f32_dpp v83, v83, v83 row_shr:4 row_mask:0xf bank_mask:0xf
	v_exp_f32_e32 v72, v72
	v_mul_f32_e32 v73, 0xbfb8aa3b, v73
	v_exp_f32_e32 v73, v73
	v_fmac_f32_dpp v79, v79, v83 row_shr:8 row_mask:0xf bank_mask:0xf bound_ctrl:1
	v_mul_f32_dpp v83, v83, v83 row_shr:8 row_mask:0xf bank_mask:0xf
	ds_read_b64 v[118:119], v103 offset:16896
	v_add_f32_e32 v68, 1.0, v68
	v_rcp_f32_e32 v68, v68
	v_fma_f32 v122, -v72, v72, 1.0
	v_sqrt_f32_e32 v122, v122
	v_add_f32_e32 v73, 1.0, v73
	v_rcp_f32_e32 v73, v73
	s_waitcnt lgkmcnt(0)
; #define LAS __attribute__((address_space(3)))
; __device__ __forceinline__ float fsigmoid(float x) { return __builtin_amdgcn_rcpf(1.0f + __expf(-x)); }
; template <int PASS, bool REV> ...
;     ...
;         for (int tg = 0; tg < 4; ++tg) { const v2u uw = *(const LAS v2u*)(UB + (tg * 16 + fr) * 264 + ch); const float uv[4] = {bflo(uw.x), bfhi(uw.x), bflo(uw.y), bfhi(uw.y)};
; #pragma unroll
;             for (int j = 0; j < 4; ++j) { const float r = fsigmoid(aa[tg][j] + bav[j]), ig = fsigmoid(ax[tg][j] + bxv[j]); const float la = -8.0f * r * sp[j];
;                 float Av = __expf(la); const float om = __builtin_fmaf(-Av, Av, 1.0f);
;                 float Bv = __builtin_amdgcn_sqrtf(om) * (ig * uv[j]);
;                 rg_scan_step<REV, 1>(Av, Bv); rg_scan_step<REV, 2>(Av, Bv); rg_scan_step<REV, 4>(Av, Bv); rg_scan_step<REV, 8>(Av, Bv);
;                 aa[tg][j] = Av; ax[tg][j] = Bv; } }
	v_lshlrev_b32_e32 v120, 16, v118
	v_mul_f32_e32 v68, v68, v120
	v_mul_f32_e32 v68, v122, v68
	v_add_f32_e32 v69, v69, v61
	v_mul_f32_e32 v73, 0xc1000000, v73
	v_fmac_f32_dpp v68, v68, v72 row_shr:1 row_mask:0xf bank_mask:0xf bound_ctrl:1
	v_mul_f32_dpp v72, v72, v72 row_shr:1 row_mask:0xf bank_mask:0xf
	v_mul_f32_e32 v69, 0xbfb8aa3b, v69
	v_mul_f32_e32 v73, v57, v73
	v_exp_f32_e32 v69, v69
	v_mul_f32_e32 v73, 0x3fb8aa3b, v73
	v_add_f32_e32 v74, v74, v66
	v_fmac_f32_dpp v68, v68, v72 row_shr:2 row_mask:0xf bank_mask:0xf bound_ctrl:1
	v_mul_f32_dpp v72, v72, v72 row_shr:2 row_mask:0xf bank_mask:0xf
	v_exp_f32_e32 v73, v73
	v_mul_f32_e32 v74, 0xbfb8aa3b, v74
	v_exp_f32_e32 v74, v74
	v_fmac_f32_dpp v68, v68, v72 row_shr:4 row_mask:0xf bank_mask:0xf bound_ctrl:1
	v_mul_f32_dpp v72, v72, v72 row_shr:4 row_mask:0xf bank_mask:0xf
	v_add_f32_e32 v69, 1.0, v69
	v_fmac_f32_dpp v68, v68, v72 row_shr:8 row_mask:0xf bank_mask:0xf bound_ctrl:1
	v_mul_f32_dpp v72, v72, v72 row_shr:8 row_mask:0xf bank_mask:0xf
	v_rcp_f32_e32 v69, v69
	v_fma_f32 v120, -v73, v73, 1.0
	v_sqrt_f32_e32 v120, v120
	v_add_f32_e32 v74, 1.0, v74
	v_rcp_f32_e32 v74, v74
	v_and_b32_e32 v118, 0xffff0000, v118
	v_mul_f32_e32 v69, v69, v118
	v_mul_f32_e32 v69, v120, v69
	v_add_f32_e32 v52, v52, v64
	v_add_f32_e32 v70, v70, v62
	v_mul_f32_e32 v74, 0xc1000000, v74
	v_mul_f32_e32 v52, 0xbfb8aa3b, v52
	v_fmac_f32_dpp v69, v69, v73 row_shr:1 row_mask:0xf bank_mask:0xf bound_ctrl:1
	v_mul_f32_dpp v73, v73, v73 row_shr:1 row_mask:0xf bank_mask:0xf
	v_mul_f32_e32 v70, 0xbfb8aa3b, v70
	v_mul_f32_e32 v74, v58, v74
	v_exp_f32_e32 v52, v52
	v_exp_f32_e32 v70, v70
	v_mul_f32_e32 v74, 0x3fb8aa3b, v74
	v_fmac_f32_dpp v69, v69, v73 row_shr:2 row_mask:0xf bank_mask:0xf bound_ctrl:1
	v_mul_f32_dpp v73, v73, v73 row_shr:2 row_mask:0xf bank_mask:0xf
	v_exp_f32_e32 v74, v74
	v_fmac_f32_dpp v69, v69, v73 row_shr:4 row_mask:0xf bank_mask:0xf bound_ctrl:1
	v_mul_f32_dpp v73, v73, v73 row_shr:4 row_mask:0xf bank_mask:0xf
	v_add_f32_e32 v52, 1.0, v52
	v_add_f32_e32 v70, 1.0, v70
	v_rcp_f32_e32 v52, v52
	v_fmac_f32_dpp v69, v69, v73 row_shr:8 row_mask:0xf bank_mask:0xf bound_ctrl:1
	v_mul_f32_dpp v73, v73, v73 row_shr:8 row_mask:0xf bank_mask:0xf
	v_rcp_f32_e32 v70, v70
	v_fma_f32 v118, -v74, v74, 1.0
	v_sqrt_f32_e32 v118, v118
	v_lshlrev_b32_e32 v121, 16, v119
	v_add_f32_e32 v48, v48, v60
	v_mul_f32_e32 v52, 0xc1000000, v52
	v_mul_f32_e32 v70, v70, v121
	v_mul_f32_e32 v48, 0xbfb8aa3b, v48
	v_mul_f32_e32 v52, v56, v52
	v_mul_f32_e32 v70, v118, v70
	v_exp_f32_e32 v48, v48
	v_mul_f32_e32 v52, 0x3fb8aa3b, v52
	v_exp_f32_e32 v52, v52
	v_fmac_f32_dpp v70, v70, v74 row_shr:1 row_mask:0xf bank_mask:0xf bound_ctrl:1
	v_mul_f32_dpp v74, v74, v74 row_shr:1 row_mask:0xf bank_mask:0xf
	ds_read_b64 v[122:123], v103 offset:25344
	v_fmac_f32_dpp v70, v70, v74 row_shr:2 row_mask:0xf bank_mask:0xf bound_ctrl:1
	v_add_f32_e32 v48, 1.0, v48
	v_mul_f32_dpp v74, v74, v74 row_shr:2 row_mask:0xf bank_mask:0xf
	v_rcp_f32_e32 v48, v48
	v_fma_f32 v56, -v52, v52, 1.0
	v_fmac_f32_dpp v70, v70, v74 row_shr:4 row_mask:0xf bank_mask:0xf bound_ctrl:1
	v_sqrt_f32_e32 v56, v56
	v_mul_f32_dpp v74, v74, v74 row_shr:4 row_mask:0xf bank_mask:0xf
	v_fmac_f32_dpp v70, v70, v74 row_shr:8 row_mask:0xf bank_mask:0xf bound_ctrl:1
	v_add_f32_e32 v75, v75, v67
	s_waitcnt lgkmcnt(0)
	v_lshlrev_b32_e32 v120, 16, v122
	v_mul_f32_e32 v75, 0xbfb8aa3b, v75
	v_mul_f32_e32 v48, v48, v120
	v_exp_f32_e32 v75, v75
	v_mul_f32_e32 v120, v56, v48
	v_add_f32_e32 v75, 1.0, v75
	v_mov_b32_e32 v48, v52
	v_fmac_f32_dpp v120, v120, v52 row_shr:1 row_mask:0xf bank_mask:0xf bound_ctrl:1
	v_mul_f32_dpp v48, v52, v52 row_shr:1 row_mask:0xf bank_mask:0xf
	v_rcp_f32_e32 v75, v75
	v_fmac_f32_dpp v120, v120, v48 row_shr:2 row_mask:0xf bank_mask:0xf bound_ctrl:1
	v_mul_f32_dpp v48, v48, v48 row_shr:2 row_mask:0xf bank_mask:0xf
	v_add_f32_e32 v71, v71, v63
	v_fmac_f32_dpp v120, v120, v48 row_shr:4 row_mask:0xf bank_mask:0xf bound_ctrl:1
	v_mul_f32_dpp v48, v48, v48 row_shr:4 row_mask:0xf bank_mask:0xf
	v_mul_f32_e32 v75, 0xc1000000, v75
	v_fmac_f32_dpp v120, v120, v48 row_shr:8 row_mask:0xf bank_mask:0xf bound_ctrl:1
	v_mov_b32_e32 v121, v48
	v_mul_f32_dpp v121, v48, v48 row_shr:8 row_mask:0xf bank_mask:0xf
	v_add_f32_e32 v48, v53, v65
	v_mul_f32_e32 v48, 0xbfb8aa3b, v48
	v_mul_f32_e32 v71, 0xbfb8aa3b, v71
	v_mul_f32_e32 v75, v59, v75
	v_exp_f32_e32 v48, v48
	v_exp_f32_e32 v71, v71
	v_mul_f32_e32 v75, 0x3fb8aa3b, v75
	v_exp_f32_e32 v75, v75
	v_add_f32_e32 v48, 1.0, v48
	v_add_f32_e32 v71, 1.0, v71
	v_rcp_f32_e32 v48, v48
	v_mul_f32_dpp v74, v74, v74 row_shr:8 row_mask:0xf bank_mask:0xf
	v_rcp_f32_e32 v71, v71
	v_fma_f32 v118, -v75, v75, 1.0
	v_sqrt_f32_e32 v118, v118
	v_and_b32_e32 v119, 0xffff0000, v119
	v_add_f32_e32 v49, v49, v61
	v_mul_f32_e32 v48, 0xc1000000, v48
	v_mul_f32_e32 v71, v71, v119
	v_mul_f32_e32 v49, 0xbfb8aa3b, v49
	v_mul_f32_e32 v48, v57, v48
	v_mul_f32_e32 v71, v118, v71
	v_exp_f32_e32 v49, v49
	v_mul_f32_e32 v48, 0x3fb8aa3b, v48
	v_exp_f32_e32 v48, v48
	v_fmac_f32_dpp v71, v71, v75 row_shr:1 row_mask:0xf bank_mask:0xf bound_ctrl:1
	v_mul_f32_dpp v75, v75, v75 row_shr:1 row_mask:0xf bank_mask:0xf
	s_nop 0
	v_fmac_f32_dpp v71, v71, v75 row_shr:2 row_mask:0xf bank_mask:0xf bound_ctrl:1
	v_add_f32_e32 v49, 1.0, v49
	v_mul_f32_dpp v75, v75, v75 row_shr:2 row_mask:0xf bank_mask:0xf
	v_rcp_f32_e32 v49, v49
	v_fma_f32 v52, -v48, v48, 1.0
	v_fmac_f32_dpp v71, v71, v75 row_shr:4 row_mask:0xf bank_mask:0xf bound_ctrl:1
	v_sqrt_f32_e32 v52, v52
	v_mul_f32_dpp v75, v75, v75 row_shr:4 row_mask:0xf bank_mask:0xf
; #define LAS __attribute__((address_space(3)))
; __device__ __forceinline__ float fsigmoid(float x) { return __builtin_amdgcn_rcpf(1.0f + __expf(-x)); }
; __device__ __forceinline__ float bperm_f(int idx4, float x) { return __builtin_bit_cast(float, __builtin_amdgcn_ds_bpermute(idx4, __builtin_bit_cast(int, x))); }
; template <int PASS, bool REV> ...
;     ...
;         for (int tg = 0; tg < 4; ++tg) { const v2u uw = *(const LAS v2u*)(UB + (tg * 16 + fr) * 264 + ch); const float uv[4] = {bflo(uw.x), bfhi(uw.x), bflo(uw.y), bfhi(uw.y)};
; #pragma unroll
;             for (int j = 0; j < 4; ++j) { const float r = fsigmoid(aa[tg][j] + bav[j]), ig = fsigmoid(ax[tg][j] + bxv[j]); const float la = -8.0f * r * sp[j];
;                 float Av = __expf(la); const float om = __builtin_fmaf(-Av, Av, 1.0f);
;                 float Bv = __builtin_amdgcn_sqrtf(om) * (ig * uv[j]);
;                 rg_scan_step<REV, 1>(Av, Bv); rg_scan_step<REV, 2>(Av, Bv); rg_scan_step<REV, 4>(Av, Bv); rg_scan_step<REV, 8>(Av, Bv);
;                 aa[tg][j] = Av; ax[tg][j] = Bv; } }
;         const int lastl4 = ((lane & 48) | (REV ? 0 : 15)) << 2;
;         if (PASS == 1) {
;             f32x4 At = (f32x4){1.f, 1.f, 1.f, 1.f}, Bt = (f32x4){0.f, 0.f, 0.f, 0.f};
; #pragma unroll
;             for (int t4 = 0; t4 < 4; ++t4) { const int tg = REV ? 3 - t4 : t4;
; #pragma unroll
;                 for (int j = 0; j < 4; ++j) { const float ta = bperm_f(lastl4, aa[tg][j]), tb = bperm_f(lastl4, ax[tg][j]); Bt[j] = ta * Bt[j] + tb; At[j] = At[j] * ta; } }
;             if (fr == 0) { f32x4* cp = (f32x4*)(CAR + ((size_t)u * 2 + d) * 256 + ch); cp[0] = (f32x4){At[0], Bt[0], At[1], Bt[1]}; cp[1] = (f32x4){At[2], Bt[2], At[3], Bt[3]}; }
	v_fmac_f32_dpp v71, v71, v75 row_shr:8 row_mask:0xf bank_mask:0xf bound_ctrl:1
	v_and_b32_e32 v119, 0xffff0000, v122
	v_mul_f32_e32 v49, v49, v119
	v_mul_f32_e32 v119, v52, v49
	s_nop 1
	v_fmac_f32_dpp v119, v119, v48 row_shr:1 row_mask:0xf bank_mask:0xf bound_ctrl:1
	v_mul_f32_dpp v48, v48, v48 row_shr:1 row_mask:0xf bank_mask:0xf
	s_nop 0
	v_fmac_f32_dpp v119, v119, v48 row_shr:2 row_mask:0xf bank_mask:0xf bound_ctrl:1
	v_mul_f32_dpp v48, v48, v48 row_shr:2 row_mask:0xf bank_mask:0xf
	v_mul_f32_dpp v75, v75, v75 row_shr:8 row_mask:0xf bank_mask:0xf
	v_fmac_f32_dpp v119, v119, v48 row_shr:4 row_mask:0xf bank_mask:0xf bound_ctrl:1
	v_mul_f32_dpp v48, v48, v48 row_shr:4 row_mask:0xf bank_mask:0xf
	v_lshlrev_b32_e32 v118, 16, v123
	v_fmac_f32_dpp v119, v119, v48 row_shr:8 row_mask:0xf bank_mask:0xf bound_ctrl:1
	v_mov_b32_e32 v122, v48
	v_mul_f32_dpp v122, v48, v48 row_shr:8 row_mask:0xf bank_mask:0xf
	v_add_f32_e32 v48, v54, v66
	v_mul_f32_e32 v48, 0xbfb8aa3b, v48
	v_exp_f32_e32 v48, v48
	v_add_f32_e32 v49, v50, v62
	v_mul_f32_e32 v49, 0xbfb8aa3b, v49
	v_exp_f32_e32 v49, v49
	v_add_f32_e32 v48, 1.0, v48
	v_rcp_f32_e32 v48, v48
	v_and_b32_e32 v103, 0xffff0000, v123
	v_add_f32_e32 v49, 1.0, v49
	v_rcp_f32_e32 v49, v49
	v_mul_f32_e32 v48, 0xc1000000, v48
	v_mul_f32_e32 v48, v58, v48
	v_mul_f32_e32 v48, 0x3fb8aa3b, v48
	v_exp_f32_e32 v48, v48
	v_mul_f32_e32 v49, v49, v118
	ds_bpermute_b32 v52, v106, v84
	ds_bpermute_b32 v53, v106, v85
	v_fma_f32 v50, -v48, v48, 1.0
	v_sqrt_f32_e32 v50, v50
	ds_bpermute_b32 v54, v106, v86
	ds_bpermute_b32 v56, v106, v80
	ds_bpermute_b32 v60, v106, v76
	v_mul_f32_e32 v118, v50, v49
	ds_bpermute_b32 v57, v106, v81
	s_nop 0
	v_fmac_f32_dpp v118, v118, v48 row_shr:1 row_mask:0xf bank_mask:0xf bound_ctrl:1
	v_mul_f32_dpp v48, v48, v48 row_shr:1 row_mask:0xf bank_mask:0xf
	ds_bpermute_b32 v61, v106, v77
	v_fmac_f32_dpp v118, v118, v48 row_shr:2 row_mask:0xf bank_mask:0xf bound_ctrl:1
	v_mul_f32_dpp v48, v48, v48 row_shr:2 row_mask:0xf bank_mask:0xf
	ds_bpermute_b32 v58, v106, v82
	v_fmac_f32_dpp v118, v118, v48 row_shr:4 row_mask:0xf bank_mask:0xf bound_ctrl:1
	v_mul_f32_dpp v48, v48, v48 row_shr:4 row_mask:0xf bank_mask:0xf
	ds_bpermute_b32 v62, v106, v78
	v_fmac_f32_dpp v118, v118, v48 row_shr:8 row_mask:0xf bank_mask:0xf bound_ctrl:1
	v_mov_b32_e32 v123, v48
	v_mul_f32_dpp v123, v48, v48 row_shr:8 row_mask:0xf bank_mask:0xf
	v_add_f32_e32 v48, v55, v67
	v_mul_f32_e32 v48, 0xbfb8aa3b, v48
	v_exp_f32_e32 v48, v48
	v_add_f32_e32 v49, v51, v63
	v_mul_f32_e32 v49, 0xbfb8aa3b, v49
	v_exp_f32_e32 v49, v49
	v_add_f32_e32 v48, 1.0, v48
	v_rcp_f32_e32 v48, v48
	ds_bpermute_b32 v51, v106, v91
	v_add_f32_e32 v49, 1.0, v49
	v_rcp_f32_e32 v49, v49
	v_mul_f32_e32 v48, 0xc1000000, v48
	v_mul_f32_e32 v48, v59, v48
	v_mul_f32_e32 v48, 0x3fb8aa3b, v48
	v_exp_f32_e32 v48, v48
	v_mul_f32_e32 v49, v49, v103
	ds_bpermute_b32 v55, v106, v87
	ds_bpermute_b32 v59, v106, v83
	v_fma_f32 v50, -v48, v48, 1.0
	v_sqrt_f32_e32 v50, v50
	ds_bpermute_b32 v63, v106, v79
	ds_bpermute_b32 v64, v106, v72
	ds_bpermute_b32 v68, v106, v68
	v_mul_f32_e32 v103, v50, v49
	ds_bpermute_b32 v65, v106, v73
	s_nop 0
	v_fmac_f32_dpp v103, v103, v48 row_shr:1 row_mask:0xf bank_mask:0xf bound_ctrl:1
	v_mul_f32_dpp v48, v48, v48 row_shr:1 row_mask:0xf bank_mask:0xf
	ds_bpermute_b32 v69, v106, v69
	v_fmac_f32_dpp v103, v103, v48 row_shr:2 row_mask:0xf bank_mask:0xf bound_ctrl:1
	v_mul_f32_dpp v48, v48, v48 row_shr:2 row_mask:0xf bank_mask:0xf
	ds_bpermute_b32 v66, v106, v74
	v_fmac_f32_dpp v103, v103, v48 row_shr:4 row_mask:0xf bank_mask:0xf bound_ctrl:1
	v_mul_f32_dpp v48, v48, v48 row_shr:4 row_mask:0xf bank_mask:0xf
	ds_bpermute_b32 v70, v106, v70
	v_fmac_f32_dpp v103, v103, v48 row_shr:8 row_mask:0xf bank_mask:0xf bound_ctrl:1
	v_mov_b32_e32 v124, v48
	v_mul_f32_dpp v124, v48, v48 row_shr:8 row_mask:0xf bank_mask:0xf
	ds_bpermute_b32 v48, v106, v88
	ds_bpermute_b32 v49, v106, v89
	ds_bpermute_b32 v50, v106, v90
	ds_bpermute_b32 v67, v106, v75
	ds_bpermute_b32 v71, v106, v71
	ds_bpermute_b32 v72, v106, v121
	ds_bpermute_b32 v76, v106, v120
	ds_bpermute_b32 v73, v106, v122
	ds_bpermute_b32 v77, v106, v119
	ds_bpermute_b32 v74, v106, v123
	ds_bpermute_b32 v78, v106, v118
	ds_bpermute_b32 v75, v106, v124
	ds_bpermute_b32 v79, v106, v103
	s_and_saveexec_b64 s[0:1], s[36:37]
	s_cbranch_execz .LBB0_567
	s_waitcnt lgkmcnt(11)
	v_pk_mul_f32 v[80:81], v[48:49], v[56:57]
	v_pk_fma_f32 v[48:49], v[48:49], 0, v[52:53] op_sel_hi:[1,0,1]
	v_pk_mul_f32 v[80:81], v[80:81], v[64:65]
	v_pk_fma_f32 v[48:49], v[48:49], v[56:57], v[60:61]
	s_waitcnt lgkmcnt(10)
	v_pk_mul_f32 v[82:83], v[50:51], v[58:59]
	v_pk_fma_f32 v[48:49], v[48:49], v[64:65], v[68:69]
	s_waitcnt lgkmcnt(5)
	v_pk_mul_f32 v[80:81], v[80:81], v[72:73]
	s_waitcnt lgkmcnt(4)
	v_pk_fma_f32 v[52:53], v[48:49], v[72:73], v[76:77]
	v_pk_fma_f32 v[48:49], v[50:51], 0, v[54:55] op_sel_hi:[1,0,1]
	v_pk_mul_f32 v[82:83], v[82:83], v[66:67]
	v_pk_fma_f32 v[48:49], v[48:49], v[58:59], v[62:63]
	v_ashrrev_i32_e32 v103, 31, v102
	v_pk_fma_f32 v[48:49], v[48:49], v[66:67], v[70:71]
	s_waitcnt lgkmcnt(1)
	v_pk_mul_f32 v[82:83], v[82:83], v[74:75]
	s_waitcnt lgkmcnt(0)
	v_pk_fma_f32 v[54:55], v[48:49], v[74:75], v[78:79]
	v_lshl_add_u64 v[48:49], v[102:103], 3, s[22:23]
	v_mov_b32_e32 v50, v80
	v_mov_b32_e32 v51, v52
	v_mov_b32_e32 v52, v81
	global_store_dwordx4 v[48:49], v[50:53], off
	s_nop 1
	v_mov_b32_e32 v52, v82
	v_mov_b32_e32 v53, v54
	v_mov_b32_e32 v54, v83
	global_store_dwordx4 v[48:49], v[52:55], off offset:16
	s_branch .LBB0_567

; #define LAS __attribute__((address_space(3)))
; template <int PASS, bool REV> ...
;     ...
;     for (int ng = ng_lo; ng < ng_hi; ++ng) {
;         f32x4 aa[4], ax[4];
;         v2u gwv[4];
; #pragma unroll
;         for (int tg = 0; tg < 4; ++tg) { aa[tg] = (f32x4){0.f, 0.f, 0.f, 0.f}; ax[tg] = (f32x4){0.f, 0.f, 0.f, 0.f}; }
; #pragma unroll
;         for (int kk = 0; kk < 2; ++kk) { const bf16x8 wa = wcur[0][kk], wx = wcur[1][kk]; bf16x8 uf[4][2];
; #pragma unroll
;             for (int tg = 0; tg < 4; ++tg) uf[tg][kk] = *(const LAS bf16x8*)(UB + (tg * 16 + fr) * 264 + blk * 64 + kk * 32 + fq * 8);
; #pragma unroll
;             for (int tg = 0; tg < 4; ++tg) { aa[tg] = __builtin_amdgcn_mfma_f32_16x16x32_bf16(wa, uf[tg][kk], aa[tg], 0, 0, 0); ax[tg] = __builtin_amdgcn_mfma_f32_16x16x32_bf16(wx, uf[tg][kk], ax[tg], 0, 0, 0); } }
;         { const int ng1 = (ng + 1 < ng_hi) ? ng + 1 : ng_lo;
; #pragma unroll
;             for (int gt = 0; gt < 2; ++gt)
; #pragma unroll
;                 for (int kk = 0; kk < 2; ++kk) wcur[gt][kk] = *(const bf16x8*)(Wg + ((size_t)(gt * 4 + blk) * 64 + ng1 * 16 + fr) * 64 + kk * 32 + fq * 8); }
;         if (PASS == 2 && REV && emit) {
; #pragma unroll
;             for (int tg = 0; tg < 4; ++tg) gwv[tg] = *(const v2u*)(P + (size_t)(R0 + tg * 16 + fr) * PROJ + C_RGG + blk * 64 + ng * 16 + fq * 4); }
;         const int ch = blk * 64 + ng * 16 + fq * 4; const f32x4 sp = *(const LAS f32x4*)(cst + ch), bav = *(const LAS f32x4*)(cst + 256 + ch), bxv = *(const LAS f32x4*)(cst + 512 + ch);
.LBB0_766:
	ds_read_b128 v[16:19], v188
	ds_read_b128 v[20:23], v188 offset:8448
	ds_read_b128 v[24:27], v188 offset:16896
	ds_read_b128 v[28:31], v188 offset:25344
	s_add_i32 s1, s1, 1
	s_waitcnt vmcnt(0) lgkmcnt(3)
	v_mfma_f32_16x16x32_bf16 v[32:35], v[8:11], v[16:19], 0
	s_cmp_lt_u32 s1, s2
	s_cselect_b64 s[20:21], -1, 0
	s_and_b64 s[12:13], s[20:21], exec
	v_mfma_f32_16x16x32_bf16 v[16:19], v[12:15], v[16:19], 0
	s_cselect_b32 s5, s1, s3
	v_lshl_add_u32 v180, s5, 4, v150
	v_add_u32_e32 v98, 0, v191
	s_waitcnt lgkmcnt(2)
	v_mfma_f32_16x16x32_bf16 v[36:39], v[8:11], v[20:23], 0
	s_nop 2
	v_mfma_f32_16x16x32_bf16 v[20:23], v[12:15], v[20:23], 0
	s_waitcnt lgkmcnt(1)
	s_nop 2
	v_mfma_f32_16x16x32_bf16 v[40:43], v[8:11], v[24:27], 0
	s_nop 2
	v_mfma_f32_16x16x32_bf16 v[24:27], v[12:15], v[24:27], 0
	s_waitcnt lgkmcnt(0)
	s_nop 2
	v_mfma_f32_16x16x32_bf16 v[8:11], v[8:11], v[28:31], 0
	s_and_b32 s5, s0, 0x1000
	s_addk_i32 s0, 0x1000
	s_nop 0
	v_mfma_f32_16x16x32_bf16 v[12:15], v[12:15], v[28:31], 0
	ds_read_b128 v[28:31], v188 offset:64
	ds_read_b128 v[44:47], v188 offset:8512
	ds_read_b128 v[82:85], v188 offset:16960
	ds_read_b128 v[86:89], v188 offset:25408
	v_add_u32_e32 v191, 32, v191
	s_and_b64 vcc, s[20:21], exec
	s_waitcnt lgkmcnt(3)
	v_mfma_f32_16x16x32_bf16 v[56:59], v[0:3], v[28:31], v[32:35]
	s_waitcnt lgkmcnt(2)
	v_mfma_f32_16x16x32_bf16 v[48:51], v[0:3], v[44:47], v[36:39]
	v_mfma_f32_16x16x32_bf16 v[44:47], v[4:7], v[44:47], v[20:23]
	s_waitcnt lgkmcnt(1)
	v_mfma_f32_16x16x32_bf16 v[40:43], v[0:3], v[82:85], v[40:43]
	s_waitcnt lgkmcnt(0)
	v_mfma_f32_16x16x32_bf16 v[20:23], v[0:3], v[86:89], v[8:11]
	v_lshlrev_b64 v[0:1], 7, v[180:181]
	v_add_u32_e32 v180, 0x100, v180
	v_lshl_add_u64 v[0:1], v[62:63], 0, v[0:1]
	v_mfma_f32_16x16x32_bf16 v[52:55], v[4:7], v[28:31], v[16:19]
	global_load_dwordx4 v[8:11], v[0:1], off
	s_nop 0
	global_load_dwordx4 v[0:3], v[0:1], off offset:64
	v_mfma_f32_16x16x32_bf16 v[36:39], v[4:7], v[82:85], v[24:27]
	v_mfma_f32_16x16x32_bf16 v[16:19], v[4:7], v[86:89], v[12:15]
	v_lshlrev_b64 v[4:5], 7, v[180:181]
	v_lshl_add_u64 v[4:5], v[62:63], 0, v[4:5]
	v_lshl_add_u64 v[24:25], v[80:81], 0, s[46:47]
	global_load_dwordx4 v[12:15], v[4:5], off
	s_nop 0
	global_load_dwordx4 v[4:7], v[4:5], off offset:64
	v_add_u32_e32 v180, 0, v190
	global_load_dwordx2 v[88:89], v[24:25], off
	v_lshl_add_u64 v[24:25], v[78:79], 0, s[46:47]
	global_load_dwordx2 v[86:87], v[24:25], off
	v_lshl_add_u64 v[24:25], v[76:77], 0, s[46:47]
	global_load_dwordx2 v[84:85], v[24:25], off
	v_lshl_add_u64 v[24:25], v[74:75], 0, s[46:47]
	global_load_dwordx2 v[82:83], v[24:25], off
	v_add_u32_e32 v24, 0x11c00, v180
	v_add_u32_e32 v28, 0x12000, v180
	ds_read_b128 v[24:27], v24
	ds_read_b128 v[32:35], v28
	v_add_u32_e32 v28, 0x12400, v180
	ds_read_b128 v[28:31], v28
	ds_read_b64 v[90:91], v98
	v_add_u32_e32 v190, 64, v190
	s_waitcnt lgkmcnt(2)
	v_add_f32_e32 v56, v56, v32
	v_mul_f32_e32 v56, 0xbfb8aa3b, v56
	v_exp_f32_e32 v56, v56
	s_waitcnt lgkmcnt(1)
	v_add_f32_e32 v52, v52, v28
	v_mul_f32_e32 v52, 0xbfb8aa3b, v52
	v_exp_f32_e32 v52, v52
	v_add_f32_e32 v56, 1.0, v56
	v_rcp_f32_e32 v56, v56
	v_add_f32_e32 v48, v48, v32
	v_add_f32_e32 v52, 1.0, v52
	v_rcp_f32_e32 v112, v52
	v_mul_f32_e32 v52, 0xc1000000, v56
	v_mul_f32_e32 v52, v24, v52
	v_mul_f32_e32 v52, 0x3fb8aa3b, v52
	v_exp_f32_e32 v108, v52
	v_add_f32_e32 v40, v40, v32
	v_mul_f32_e32 v48, 0xbfb8aa3b, v48
	v_mul_f32_e32 v40, 0xbfb8aa3b, v40
	v_fma_f32 v52, -v108, v108, 1.0
	v_sqrt_f32_e32 v114, v52
	v_add_f32_e32 v52, v57, v33
	v_mul_f32_e32 v52, 0xbfb8aa3b, v52
	v_exp_f32_e32 v52, v52
	v_exp_f32_e32 v48, v48
	v_exp_f32_e32 v40, v40
	v_add_f32_e32 v44, v44, v28
	v_add_f32_e32 v36, v36, v28
	v_mul_f32_e32 v44, 0xbfb8aa3b, v44
	v_mul_f32_e32 v36, 0xbfb8aa3b, v36
	v_add_f32_e32 v52, 1.0, v52
	v_add_f32_e32 v48, 1.0, v48
	v_exp_f32_e32 v44, v44
	v_add_f32_e32 v40, 1.0, v40
	v_exp_f32_e32 v36, v36
	v_rcp_f32_e32 v52, v52
	v_rcp_f32_e32 v48, v48
	v_rcp_f32_e32 v40, v40
	v_add_f32_e32 v44, 1.0, v44
	v_add_f32_e32 v36, 1.0, v36
	v_mul_f32_e32 v52, 0xc1000000, v52
	v_rcp_f32_e32 v140, v44
	v_mul_f32_e32 v44, 0xc1000000, v48
	v_rcp_f32_e32 v56, v36
	v_mul_f32_e32 v36, 0xc1000000, v40
	v_mul_f32_e32 v52, v25, v52
	v_mul_f32_e32 v44, v24, v44
	v_mul_f32_e32 v36, v24, v36
	v_mul_f32_e32 v52, 0x3fb8aa3b, v52
	v_mul_f32_e32 v44, 0x3fb8aa3b, v44
	v_mul_f32_e32 v36, 0x3fb8aa3b, v36
	v_exp_f32_e32 v109, v52
	v_exp_f32_e32 v132, v44
	v_exp_f32_e32 v36, v36
	v_add_f32_e32 v53, v53, v29
	v_fma_f32 v52, -v109, v109, 1.0
	v_fma_f32 v44, -v132, v132, 1.0
	v_fma_f32 v40, -v36, v36, 1.0
	v_sqrt_f32_e32 v115, v52
	v_add_f32_e32 v52, v58, v34
	v_sqrt_f32_e32 v142, v44
	v_add_f32_e32 v44, v49, v33
	v_sqrt_f32_e32 v58, v40
	v_add_f32_e32 v40, v41, v33
	v_mul_f32_e32 v52, 0xbfb8aa3b, v52
	v_mul_f32_e32 v44, 0xbfb8aa3b, v44
	v_mul_f32_e32 v40, 0xbfb8aa3b, v40
	v_exp_f32_e32 v52, v52
	v_exp_f32_e32 v44, v44
	v_exp_f32_e32 v40, v40
	v_add_f32_e32 v37, v37, v29
	v_mul_f32_e32 v53, 0xbfb8aa3b, v53
	v_mul_f32_e32 v37, 0xbfb8aa3b, v37
	v_exp_f32_e32 v53, v53
	v_add_f32_e32 v52, 1.0, v52
	v_add_f32_e32 v44, 1.0, v44
	v_add_f32_e32 v40, 1.0, v40
	v_exp_f32_e32 v37, v37
	v_rcp_f32_e32 v52, v52
	v_rcp_f32_e32 v44, v44
	v_rcp_f32_e32 v40, v40
	v_add_f32_e32 v53, 1.0, v53
	v_add_f32_e32 v37, 1.0, v37
	v_rcp_f32_e32 v113, v53
	v_add_f32_e32 v53, v54, v30
	v_mul_f32_e32 v52, 0xc1000000, v52
	v_mul_f32_e32 v44, 0xc1000000, v44
	v_rcp_f32_e32 v57, v37
	v_mul_f32_e32 v37, 0xc1000000, v40
	v_mul_f32_e32 v53, 0xbfb8aa3b, v53
	v_mul_f32_e32 v52, v26, v52
	v_mul_f32_e32 v44, v25, v44
	v_mul_f32_e32 v37, v25, v37
	v_exp_f32_e32 v53, v53
; #define LAS __attribute__((address_space(3)))
; __device__ __forceinline__ float fsigmoid(float x) { return __builtin_amdgcn_rcpf(1.0f + __expf(-x)); }
; template <int PASS, bool REV> ...
;     ...
;         const int ch = blk * 64 + ng * 16 + fq * 4; const f32x4 sp = *(const LAS f32x4*)(cst + ch), bav = *(const LAS f32x4*)(cst + 256 + ch), bxv = *(const LAS f32x4*)(cst + 512 + ch);
; #pragma unroll
;         for (int tg = 0; tg < 4; ++tg) { const v2u uw = *(const LAS v2u*)(UB + (tg * 16 + fr) * 264 + ch); const float uv[4] = {bflo(uw.x), bfhi(uw.x), bflo(uw.y), bfhi(uw.y)};
; #pragma unroll
;             for (int j = 0; j < 4; ++j) { const float r = fsigmoid(aa[tg][j] + bav[j]), ig = fsigmoid(ax[tg][j] + bxv[j]); const float la = -8.0f * r * sp[j];
;                 float Av = __expf(la); const float om = __builtin_fmaf(-Av, Av, 1.0f);
;                 float Bv = __builtin_amdgcn_sqrtf(om) * (ig * uv[j]);
;                 rg_scan_step<REV, 1>(Av, Bv); rg_scan_step<REV, 2>(Av, Bv); rg_scan_step<REV, 4>(Av, Bv); rg_scan_step<REV, 8>(Av, Bv);
;                 aa[tg][j] = Av; ax[tg][j] = Bv; } }
	v_mul_f32_e32 v52, 0x3fb8aa3b, v52
	v_mul_f32_e32 v44, 0x3fb8aa3b, v44
	v_mul_f32_e32 v37, 0x3fb8aa3b, v37
	v_exp_f32_e32 v52, v52
	v_exp_f32_e32 v133, v44
	v_exp_f32_e32 v37, v37
	v_add_f32_e32 v53, 1.0, v53
	v_rcp_f32_e32 v92, v53
	v_fma_f32 v53, -v52, v52, 1.0
	v_fma_f32 v44, -v133, v133, 1.0
	v_fma_f32 v40, -v37, v37, 1.0
	v_sqrt_f32_e32 v94, v53
	v_add_f32_e32 v53, v59, v35
	v_sqrt_f32_e32 v143, v44
	v_add_f32_e32 v44, v50, v34
	v_sqrt_f32_e32 v59, v40
	v_add_f32_e32 v40, v42, v34
	v_mul_f32_e32 v44, 0xbfb8aa3b, v44
	v_mul_f32_e32 v40, 0xbfb8aa3b, v40
	v_exp_f32_e32 v44, v44
	v_exp_f32_e32 v40, v40
	v_add_f32_e32 v38, v38, v30
	v_mul_f32_e32 v38, 0xbfb8aa3b, v38
	v_add_f32_e32 v44, 1.0, v44
	v_add_f32_e32 v40, 1.0, v40
	v_exp_f32_e32 v38, v38
	v_rcp_f32_e32 v44, v44
	v_rcp_f32_e32 v40, v40
	v_add_f32_e32 v45, v45, v29
	v_add_f32_e32 v38, 1.0, v38
	v_mul_f32_e32 v44, 0xc1000000, v44
	v_rcp_f32_e32 v42, v38
	v_mul_f32_e32 v38, 0xc1000000, v40
	v_mul_f32_e32 v44, v26, v44
	v_mul_f32_e32 v38, v26, v38
	v_mul_f32_e32 v45, 0xbfb8aa3b, v45
	v_mul_f32_e32 v44, 0x3fb8aa3b, v44
	v_mul_f32_e32 v38, 0x3fb8aa3b, v38
	v_exp_f32_e32 v45, v45
	v_exp_f32_e32 v118, v44
	v_exp_f32_e32 v40, v38
	v_mul_f32_e32 v53, 0xbfb8aa3b, v53
	v_add_f32_e32 v45, 1.0, v45
	v_fma_f32 v44, -v118, v118, 1.0
	v_fma_f32 v38, -v40, v40, 1.0
	v_rcp_f32_e32 v141, v45
	v_add_f32_e32 v45, v46, v30
	v_sqrt_f32_e32 v138, v44
	v_add_f32_e32 v44, v51, v35
	v_sqrt_f32_e32 v46, v38
	v_add_f32_e32 v38, v43, v35
	v_mul_f32_e32 v44, 0xbfb8aa3b, v44
	v_mul_f32_e32 v38, 0xbfb8aa3b, v38
	v_exp_f32_e32 v53, v53
	v_exp_f32_e32 v44, v44
	v_exp_f32_e32 v38, v38
	v_mul_f32_e32 v45, 0xbfb8aa3b, v45
	v_add_f32_e32 v53, 1.0, v53
	v_add_f32_e32 v44, 1.0, v44
	v_add_f32_e32 v38, 1.0, v38
	v_rcp_f32_e32 v53, v53
	v_exp_f32_e32 v45, v45
	v_rcp_f32_e32 v44, v44
	v_rcp_f32_e32 v38, v38
	v_add_f32_e32 v20, v20, v32
	v_add_f32_e32 v54, v55, v31
	v_mul_f32_e32 v53, 0xc1000000, v53
	v_add_f32_e32 v45, 1.0, v45
	v_mul_f32_e32 v44, 0xc1000000, v44
	v_mul_f32_e32 v38, 0xc1000000, v38
	v_mul_f32_e32 v20, 0xbfb8aa3b, v20
	v_mul_f32_e32 v54, 0xbfb8aa3b, v54
	v_mul_f32_e32 v53, v27, v53
	v_rcp_f32_e32 v136, v45
	v_add_f32_e32 v45, v47, v31
	v_mul_f32_e32 v44, v27, v44
	v_add_f32_e32 v39, v39, v31
	v_mul_f32_e32 v38, v27, v38
	v_exp_f32_e32 v20, v20
	v_exp_f32_e32 v54, v54
	v_mul_f32_e32 v53, 0x3fb8aa3b, v53
	v_mul_f32_e32 v45, 0xbfb8aa3b, v45
	v_mul_f32_e32 v44, 0x3fb8aa3b, v44
	v_mul_f32_e32 v39, 0xbfb8aa3b, v39
	v_mul_f32_e32 v38, 0x3fb8aa3b, v38
	v_exp_f32_e32 v53, v53
	v_exp_f32_e32 v45, v45
	v_exp_f32_e32 v119, v44
	v_exp_f32_e32 v39, v39
	v_exp_f32_e32 v41, v38
	v_add_f32_e32 v16, v16, v28
	v_mul_f32_e32 v16, 0xbfb8aa3b, v16
	v_add_f32_e32 v20, 1.0, v20
	v_exp_f32_e32 v16, v16
	v_add_f32_e32 v54, 1.0, v54
	v_rcp_f32_e32 v20, v20
	v_rcp_f32_e32 v93, v54
	v_fma_f32 v54, -v53, v53, 1.0
	v_add_f32_e32 v45, 1.0, v45
	v_fma_f32 v44, -v119, v119, 1.0
	v_add_f32_e32 v39, 1.0, v39
	v_fma_f32 v38, -v41, v41, 1.0
	v_sqrt_f32_e32 v95, v54
	ds_read_b64 v[54:55], v98 offset:8448
	v_rcp_f32_e32 v137, v45
	v_sqrt_f32_e32 v139, v44
	ds_read_b64 v[44:45], v98 offset:16896
	v_rcp_f32_e32 v43, v39
	v_sqrt_f32_e32 v47, v38
	ds_read_b64 v[38:39], v98 offset:25344
	v_add_f32_e32 v16, 1.0, v16
	v_rcp_f32_e32 v124, v16
	v_mul_f32_e32 v16, 0xc1000000, v20
	v_mul_f32_e32 v16, v24, v16
	v_mul_f32_e32 v16, 0x3fb8aa3b, v16
	s_waitcnt lgkmcnt(0)
	v_lshlrev_b32_e32 v122, 16, v38
	v_and_b32_e32 v123, 0xffff0000, v38
	v_exp_f32_e32 v38, v16
	v_lshlrev_b32_e32 v102, 16, v39
	v_and_b32_e32 v103, 0xffff0000, v39
	v_add_f32_e32 v17, v17, v29
	v_fma_f32 v16, -v38, v38, 1.0
	v_sqrt_f32_e32 v126, v16
	v_add_f32_e32 v16, v21, v33
	v_mul_f32_e32 v16, 0xbfb8aa3b, v16
	v_exp_f32_e32 v16, v16
	v_mul_f32_e32 v17, 0xbfb8aa3b, v17
	v_exp_f32_e32 v17, v17
	v_lshlrev_b32_e32 v134, 16, v54
	v_add_f32_e32 v16, 1.0, v16
	v_rcp_f32_e32 v16, v16
	v_add_f32_e32 v17, 1.0, v17
	v_rcp_f32_e32 v125, v17
	v_add_f32_e32 v17, v18, v30
	v_mul_f32_e32 v16, 0xc1000000, v16
	v_mul_f32_e32 v16, v25, v16
	v_mul_f32_e32 v16, 0x3fb8aa3b, v16
	v_exp_f32_e32 v39, v16
	v_mul_f32_e32 v17, 0xbfb8aa3b, v17
	v_exp_f32_e32 v17, v17
	v_and_b32_e32 v135, 0xffff0000, v54
	v_fma_f32 v16, -v39, v39, 1.0
	v_sqrt_f32_e32 v127, v16
	v_add_f32_e32 v16, v22, v34
	v_mul_f32_e32 v16, 0xbfb8aa3b, v16
	v_exp_f32_e32 v16, v16
	v_add_f32_e32 v17, 1.0, v17
	v_rcp_f32_e32 v104, v17
	v_add_f32_e32 v17, v19, v31
	v_add_f32_e32 v16, 1.0, v16
	v_rcp_f32_e32 v16, v16
	v_pk_mul_f32 v[30:31], v[140:141], v[134:135]
	v_pk_mul_f32 v[30:31], v[142:143], v[30:31]
	v_mul_f32_e32 v16, 0xc1000000, v16
	v_mul_f32_e32 v16, v26, v16
	v_mul_f32_e32 v16, 0x3fb8aa3b, v16
	v_exp_f32_e32 v50, v16
	s_nop 0
	v_fma_f32 v16, -v50, v50, 1.0
	v_fmac_f32_dpp v30, v30, v132 row_shl:1 row_mask:0xf bank_mask:0xf bound_ctrl:1
	v_fmac_f32_dpp v31, v31, v133 row_shl:1 row_mask:0xf bank_mask:0xf bound_ctrl:1
	v_sqrt_f32_e32 v106, v16
	v_add_f32_e32 v16, v23, v35
	v_mov_b32_e32 v34, v132
	v_mul_f32_dpp v34, v132, v132 row_shl:1 row_mask:0xf bank_mask:0xf
	v_mov_b32_e32 v35, v133
	v_mul_f32_dpp v35, v133, v133 row_shl:1 row_mask:0xf bank_mask:0xf
	v_fmac_f32_dpp v30, v30, v34 row_shl:2 row_mask:0xf bank_mask:0xf bound_ctrl:1
	v_fmac_f32_dpp v31, v31, v35 row_shl:2 row_mask:0xf bank_mask:0xf bound_ctrl:1
	v_mov_b32_e32 v132, v34
	v_mul_f32_dpp v132, v34, v34 row_shl:2 row_mask:0xf bank_mask:0xf
	v_mov_b32_e32 v133, v35
	v_mul_f32_dpp v133, v35, v35 row_shl:2 row_mask:0xf bank_mask:0xf
	v_fmac_f32_dpp v30, v30, v132 row_shl:4 row_mask:0xf bank_mask:0xf bound_ctrl:1
	v_fmac_f32_dpp v31, v31, v133 row_shl:4 row_mask:0xf bank_mask:0xf bound_ctrl:1
; #define LAS __attribute__((address_space(3)))
; __device__ __forceinline__ float fsigmoid(float x) { return __builtin_amdgcn_rcpf(1.0f + __expf(-x)); }
; template <int PASS, bool REV> ...
;     ...
;         for (int tg = 0; tg < 4; ++tg) { const v2u uw = *(const LAS v2u*)(UB + (tg * 16 + fr) * 264 + ch); const float uv[4] = {bflo(uw.x), bfhi(uw.x), bflo(uw.y), bfhi(uw.y)};
; #pragma unroll
;             for (int j = 0; j < 4; ++j) { const float r = fsigmoid(aa[tg][j] + bav[j]), ig = fsigmoid(ax[tg][j] + bxv[j]); const float la = -8.0f * r * sp[j];
;                 float Av = __expf(la); const float om = __builtin_fmaf(-Av, Av, 1.0f);
;                 float Bv = __builtin_amdgcn_sqrtf(om) * (ig * uv[j]);
;                 rg_scan_step<REV, 1>(Av, Bv); rg_scan_step<REV, 2>(Av, Bv); rg_scan_step<REV, 4>(Av, Bv); rg_scan_step<REV, 8>(Av, Bv);
;                 aa[tg][j] = Av; ax[tg][j] = Bv; } }
;     ...
;                         const v2u gw = gwv[tg]; const float g[4] = {bflo(gw.x), bfhi(gw.x), bflo(gw.y), bfhi(gw.y)}; float y[4];
; #pragma unroll
;                         for (int j = 0; j < 4; ++j) { const float x = g[j]; const float u2 = 1.5957691216057308f * (x + 0.044715f * x * x * x); y[j] = (hf[j] + ax[tg][j]) * x * fsigmoid(u2); }
	v_lshlrev_b32_e32 v110, 16, v90
	v_and_b32_e32 v111, 0xffff0000, v90
	v_mov_b32_e32 v34, v132
	v_mul_f32_dpp v34, v132, v132 row_shl:4 row_mask:0xf bank_mask:0xf
	v_mov_b32_e32 v35, v133
	v_mul_f32_dpp v35, v133, v133 row_shl:4 row_mask:0xf bank_mask:0xf
	v_mov_b32_e32 v132, v30
	v_fmac_f32_dpp v132, v30, v34 row_shl:8 row_mask:0xf bank_mask:0xf bound_ctrl:1
	v_mov_b32_e32 v133, v31
	v_fmac_f32_dpp v133, v31, v35 row_shl:8 row_mask:0xf bank_mask:0xf bound_ctrl:1
	v_pk_mul_f32 v[30:31], v[112:113], v[110:111]
	v_pk_mul_f32 v[30:31], v[30:31], v[114:115]
	s_nop 1
	v_fmac_f32_dpp v30, v30, v108 row_shl:1 row_mask:0xf bank_mask:0xf bound_ctrl:1
	v_fmac_f32_dpp v31, v31, v109 row_shl:1 row_mask:0xf bank_mask:0xf bound_ctrl:1
	v_mov_b32_e32 v134, v34
	v_mul_f32_dpp v134, v34, v34 row_shl:8 row_mask:0xf bank_mask:0xf
	v_mov_b32_e32 v135, v35
	v_mul_f32_dpp v135, v35, v35 row_shl:8 row_mask:0xf bank_mask:0xf
	v_mov_b32_e32 v34, v108
	v_mul_f32_dpp v34, v108, v108 row_shl:1 row_mask:0xf bank_mask:0xf
	v_mov_b32_e32 v35, v109
	v_mul_f32_dpp v35, v109, v109 row_shl:1 row_mask:0xf bank_mask:0xf
	v_fmac_f32_dpp v30, v30, v34 row_shl:2 row_mask:0xf bank_mask:0xf bound_ctrl:1
	v_fmac_f32_dpp v31, v31, v35 row_shl:2 row_mask:0xf bank_mask:0xf bound_ctrl:1
	v_mov_b32_e32 v108, v34
	v_mul_f32_dpp v108, v34, v34 row_shl:2 row_mask:0xf bank_mask:0xf
	v_mov_b32_e32 v109, v35
	v_mul_f32_dpp v109, v35, v35 row_shl:2 row_mask:0xf bank_mask:0xf
	v_fmac_f32_dpp v30, v30, v108 row_shl:4 row_mask:0xf bank_mask:0xf bound_ctrl:1
	v_fmac_f32_dpp v31, v31, v109 row_shl:4 row_mask:0xf bank_mask:0xf bound_ctrl:1
	s_waitcnt vmcnt(3)
	v_lshlrev_b32_e32 v114, 16, v88
	v_mov_b32_e32 v34, v108
	v_mul_f32_dpp v34, v108, v108 row_shl:4 row_mask:0xf bank_mask:0xf
	v_mov_b32_e32 v35, v109
	v_mul_f32_dpp v35, v109, v109 row_shl:4 row_mask:0xf bank_mask:0xf
	v_mul_f32_e32 v29, 0x3d372713, v114
	v_mov_b32_e32 v112, v30
	v_fmac_f32_dpp v112, v30, v34 row_shl:8 row_mask:0xf bank_mask:0xf bound_ctrl:1
	v_mov_b32_e32 v113, v31
	v_fmac_f32_dpp v113, v31, v35 row_shl:8 row_mask:0xf bank_mask:0xf bound_ctrl:1
	v_mul_f32_e32 v29, v29, v114
	v_mov_b32_e32 v30, v114
	v_fmac_f32_e32 v30, v29, v30
	v_mul_f32_e32 v29, 0x3fcc422a, v30
	v_mul_f32_e32 v29, 0xbfb8aa3b, v29
	v_exp_f32_e32 v29, v29
	v_and_b32_e32 v115, 0xffff0000, v88
	v_mov_b32_e32 v30, v115
	s_waitcnt vmcnt(2)
	v_lshlrev_b32_e32 v142, 16, v86
	v_add_f32_e32 v29, 1.0, v29
	v_rcp_f32_e32 v140, v29
	v_mul_f32_e32 v29, 0x3d372713, v115
	v_mul_f32_e32 v29, v29, v115
	v_fmac_f32_e32 v30, v29, v30
	v_mul_f32_e32 v29, 0x3fcc422a, v30
	v_mul_f32_e32 v29, 0xbfb8aa3b, v29
	v_exp_f32_e32 v29, v29
	v_mov_b32_e32 v30, v142
	v_and_b32_e32 v143, 0xffff0000, v86
	v_lshlrev_b32_e32 v120, 16, v55
	v_add_f32_e32 v29, 1.0, v29
	v_rcp_f32_e32 v141, v29
	v_mul_f32_e32 v29, 0x3d372713, v142
	v_mul_f32_e32 v29, v29, v142
	v_fmac_f32_e32 v30, v29, v30
	v_mul_f32_e32 v29, 0x3fcc422a, v30
	v_mul_f32_e32 v29, 0xbfb8aa3b, v29
	v_exp_f32_e32 v29, v29
	v_mov_b32_e32 v30, v143
	v_and_b32_e32 v121, 0xffff0000, v55
	v_add_f32_e32 v29, 1.0, v29
	v_rcp_f32_e32 v144, v29
	v_mul_f32_e32 v29, 0x3d372713, v143
	v_mul_f32_e32 v29, v29, v143
	v_fmac_f32_e32 v30, v29, v30
	v_mul_f32_e32 v29, 0x3fcc422a, v30
	v_pk_mul_f32 v[30:31], v[136:137], v[120:121]
	v_pk_mul_f32 v[30:31], v[138:139], v[30:31]
	s_nop 1
	v_fmac_f32_dpp v30, v30, v118 row_shl:1 row_mask:0xf bank_mask:0xf bound_ctrl:1
	v_fmac_f32_dpp v31, v31, v119 row_shl:1 row_mask:0xf bank_mask:0xf bound_ctrl:1
	v_mov_b32_e32 v116, v34
	v_mul_f32_dpp v116, v34, v34 row_shl:8 row_mask:0xf bank_mask:0xf
	v_mov_b32_e32 v117, v35
	v_mul_f32_dpp v117, v35, v35 row_shl:8 row_mask:0xf bank_mask:0xf
	v_mov_b32_e32 v34, v118
	v_mul_f32_dpp v34, v118, v118 row_shl:1 row_mask:0xf bank_mask:0xf
	v_mov_b32_e32 v35, v119
	v_mul_f32_dpp v35, v119, v119 row_shl:1 row_mask:0xf bank_mask:0xf
	v_fmac_f32_dpp v30, v30, v34 row_shl:2 row_mask:0xf bank_mask:0xf bound_ctrl:1
	v_fmac_f32_dpp v31, v31, v35 row_shl:2 row_mask:0xf bank_mask:0xf bound_ctrl:1
	v_mov_b32_e32 v108, v34
	v_mul_f32_dpp v108, v34, v34 row_shl:2 row_mask:0xf bank_mask:0xf
	v_mov_b32_e32 v109, v35
	v_mul_f32_dpp v109, v35, v35 row_shl:2 row_mask:0xf bank_mask:0xf
	v_fmac_f32_dpp v30, v30, v108 row_shl:4 row_mask:0xf bank_mask:0xf bound_ctrl:1
	v_fmac_f32_dpp v31, v31, v109 row_shl:4 row_mask:0xf bank_mask:0xf bound_ctrl:1
	v_lshlrev_b32_e32 v90, 16, v91
	v_and_b32_e32 v91, 0xffff0000, v91
	v_mov_b32_e32 v34, v108
	v_mul_f32_dpp v34, v108, v108 row_shl:4 row_mask:0xf bank_mask:0xf
	v_mov_b32_e32 v35, v109
	v_mul_f32_dpp v35, v109, v109 row_shl:4 row_mask:0xf bank_mask:0xf
	v_mov_b32_e32 v108, v30
	v_fmac_f32_dpp v108, v30, v34 row_shl:8 row_mask:0xf bank_mask:0xf bound_ctrl:1
	v_mov_b32_e32 v109, v31
	v_fmac_f32_dpp v109, v31, v35 row_shl:8 row_mask:0xf bank_mask:0xf bound_ctrl:1
	v_pk_mul_f32 v[30:31], v[92:93], v[90:91]
	v_pk_mul_f32 v[30:31], v[30:31], v[94:95]
	v_mul_f32_e32 v29, 0xbfb8aa3b, v29
	v_exp_f32_e32 v29, v29
	v_fmac_f32_dpp v30, v30, v52 row_shl:1 row_mask:0xf bank_mask:0xf bound_ctrl:1
	v_fmac_f32_dpp v31, v31, v53 row_shl:1 row_mask:0xf bank_mask:0xf bound_ctrl:1
	v_mov_b32_e32 v110, v34
	v_mul_f32_dpp v110, v34, v34 row_shl:8 row_mask:0xf bank_mask:0xf
	v_mov_b32_e32 v111, v35
	v_mul_f32_dpp v111, v35, v35 row_shl:8 row_mask:0xf bank_mask:0xf
	v_mov_b32_e32 v34, v52
	v_mul_f32_dpp v34, v52, v52 row_shl:1 row_mask:0xf bank_mask:0xf
	v_mov_b32_e32 v35, v53
	v_mul_f32_dpp v35, v53, v53 row_shl:1 row_mask:0xf bank_mask:0xf
	v_fmac_f32_dpp v30, v30, v34 row_shl:2 row_mask:0xf bank_mask:0xf bound_ctrl:1
	v_fmac_f32_dpp v31, v31, v35 row_shl:2 row_mask:0xf bank_mask:0xf bound_ctrl:1
; #define LAS __attribute__((address_space(3)))
; __device__ __forceinline__ float fsigmoid(float x) { return __builtin_amdgcn_rcpf(1.0f + __expf(-x)); }
; __device__ __forceinline__ float bperm_f(int idx4, float x) { return __builtin_bit_cast(float, __builtin_amdgcn_ds_bpermute(idx4, __builtin_bit_cast(int, x))); }
; template <int PASS, bool REV> ...
;     ...
;         for (int tg = 0; tg < 4; ++tg) { const v2u uw = *(const LAS v2u*)(UB + (tg * 16 + fr) * 264 + ch); const float uv[4] = {bflo(uw.x), bfhi(uw.x), bflo(uw.y), bfhi(uw.y)};
; #pragma unroll
;             for (int j = 0; j < 4; ++j) { const float r = fsigmoid(aa[tg][j] + bav[j]), ig = fsigmoid(ax[tg][j] + bxv[j]); const float la = -8.0f * r * sp[j];
;                 float Av = __expf(la); const float om = __builtin_fmaf(-Av, Av, 1.0f);
;                 float Bv = __builtin_amdgcn_sqrtf(om) * (ig * uv[j]);
;                 rg_scan_step<REV, 1>(Av, Bv); rg_scan_step<REV, 2>(Av, Bv); rg_scan_step<REV, 4>(Av, Bv); rg_scan_step<REV, 8>(Av, Bv);
;                 aa[tg][j] = Av; ax[tg][j] = Bv; } }
;         const int lastl4 = ((lane & 48) | (REV ? 0 : 15)) << 2;
;         if (PASS == 1) {
;             f32x4 At = (f32x4){1.f, 1.f, 1.f, 1.f}, Bt = (f32x4){0.f, 0.f, 0.f, 0.f};
; #pragma unroll
;             for (int t4 = 0; t4 < 4; ++t4) { const int tg = REV ? 3 - t4 : t4;
; #pragma unroll
;                 for (int j = 0; j < 4; ++j) { const float ta = bperm_f(lastl4, aa[tg][j]), tb = bperm_f(lastl4, ax[tg][j]); Bt[j] = ta * Bt[j] + tb; At[j] = At[j] * ta; } }
;             if (fr == 0) { f32x4* cp = (f32x4*)(CAR + ((size_t)u * 2 + d) * 256 + ch); cp[0] = (f32x4){At[0], Bt[0], At[1], Bt[1]}; cp[1] = (f32x4){At[2], Bt[2], At[3], Bt[3]}; }
;         } else {
;             f32x4 hin = *(const LAS f32x4*)(CIN + d * 256 + ch);
; #pragma unroll
;             for (int t4 = 0; t4 < 4; ++t4) { const int tg = REV ? 3 - t4 : t4;
; #pragma unroll
;                 for (int j = 0; j < 4; ++j) { const float h = aa[tg][j] * hin[j] + ax[tg][j]; ax[tg][j] = h; hin[j] = bperm_f(lastl4, h); } }
	v_mov_b32_e32 v52, v34
	v_mul_f32_dpp v52, v34, v34 row_shl:2 row_mask:0xf bank_mask:0xf
	v_mov_b32_e32 v53, v35
	v_mul_f32_dpp v53, v35, v35 row_shl:2 row_mask:0xf bank_mask:0xf
	v_mul_f32_e32 v16, 0xbfb8aa3b, v16
	v_add_f32_e32 v29, 1.0, v29
	v_fmac_f32_dpp v30, v30, v52 row_shl:4 row_mask:0xf bank_mask:0xf bound_ctrl:1
	v_fmac_f32_dpp v31, v31, v53 row_shl:4 row_mask:0xf bank_mask:0xf bound_ctrl:1
	v_lshlrev_b32_e32 v88, 16, v89
	v_exp_f32_e32 v16, v16
	v_rcp_f32_e32 v145, v29
	v_mov_b32_e32 v34, v52
	v_mul_f32_dpp v34, v52, v52 row_shl:4 row_mask:0xf bank_mask:0xf
	v_mov_b32_e32 v35, v53
	v_mul_f32_dpp v35, v53, v53 row_shl:4 row_mask:0xf bank_mask:0xf
	v_mul_f32_e32 v29, 0x3d372713, v88
	v_mov_b32_e32 v52, v30
	v_fmac_f32_dpp v52, v30, v34 row_shl:8 row_mask:0xf bank_mask:0xf bound_ctrl:1
	v_mov_b32_e32 v53, v31
	v_fmac_f32_dpp v53, v31, v35 row_shl:8 row_mask:0xf bank_mask:0xf bound_ctrl:1
	v_mul_f32_e32 v29, v29, v88
	v_mov_b32_e32 v30, v88
	v_fmac_f32_e32 v30, v29, v30
	v_mul_f32_e32 v29, 0x3fcc422a, v30
	v_add_f32_e32 v16, 1.0, v16
	v_mul_f32_e32 v29, 0xbfb8aa3b, v29
	v_rcp_f32_e32 v16, v16
	v_exp_f32_e32 v29, v29
	v_pk_mul_f32 v[118:119], v[124:125], v[122:123]
	v_pk_mul_f32 v[118:119], v[126:127], v[118:119]
	v_mul_f32_e32 v16, 0xc1000000, v16
	v_and_b32_e32 v89, 0xffff0000, v89
	v_add_f32_e32 v29, 1.0, v29
	v_mov_b32_e32 v122, v38
	v_mul_f32_dpp v122, v38, v38 row_shl:1 row_mask:0xf bank_mask:0xf
	v_mov_b32_e32 v123, v39
	v_mul_f32_dpp v123, v39, v39 row_shl:1 row_mask:0xf bank_mask:0xf
	v_fmac_f32_dpp v118, v118, v38 row_shl:1 row_mask:0xf bank_mask:0xf bound_ctrl:1
	v_mov_b32_e32 v38, v118
	v_fmac_f32_dpp v119, v119, v39 row_shl:1 row_mask:0xf bank_mask:0xf bound_ctrl:1
	v_mov_b32_e32 v39, v119
	v_mul_f32_e32 v16, v27, v16
	ds_read_b128 v[24:27], v180 offset:35840
	v_rcp_f32_e32 v92, v29
	v_mul_f32_e32 v29, 0x3d372713, v89
	v_mul_f32_e32 v29, v29, v89
	v_mov_b32_e32 v30, v89
	v_mov_b32_e32 v120, v122
	v_mul_f32_dpp v120, v122, v122 row_shl:2 row_mask:0xf bank_mask:0xf
	v_mov_b32_e32 v121, v123
	v_mul_f32_dpp v121, v123, v123 row_shl:2 row_mask:0xf bank_mask:0xf
	v_fmac_f32_dpp v38, v38, v122 row_shl:2 row_mask:0xf bank_mask:0xf bound_ctrl:1
	v_fmac_f32_dpp v39, v39, v123 row_shl:2 row_mask:0xf bank_mask:0xf bound_ctrl:1
	v_fmac_f32_e32 v30, v29, v30
	v_mov_b32_e32 v124, v120
	v_lshlrev_b32_e32 v54, 16, v44
	v_and_b32_e32 v55, 0xffff0000, v44
	v_mul_f32_e32 v29, 0x3fcc422a, v30
	v_fmac_f32_dpp v38, v38, v120 row_shl:4 row_mask:0xf bank_mask:0xf bound_ctrl:1
	v_fmac_f32_dpp v39, v39, v121 row_shl:4 row_mask:0xf bank_mask:0xf bound_ctrl:1
	v_mul_f32_dpp v124, v120, v120 row_shl:4 row_mask:0xf bank_mask:0xf
	v_mul_f32_e32 v29, 0xbfb8aa3b, v29
	v_pk_mul_f32 v[54:55], v[56:57], v[54:55]
	v_exp_f32_e32 v29, v29
	v_mov_b32_e32 v125, v124
	v_mul_f32_dpp v125, v124, v124 row_shl:8 row_mask:0xf bank_mask:0xf
	s_waitcnt lgkmcnt(0)
	v_mov_b32_e32 v119, v24
	v_mov_b32_e32 v120, v121
	v_mul_f32_dpp v120, v121, v121 row_shl:4 row_mask:0xf bank_mask:0xf
	v_pk_mul_f32 v[54:55], v[58:59], v[54:55]
	v_mov_b32_e32 v118, v181
	v_mov_b32_e32 v122, v181
	s_nop 0
	v_mov_b32_dpp v118, v38 row_shl:8 row_mask:0xf bank_mask:0xf
	v_mov_b32_dpp v122, v39 row_shl:8 row_mask:0xf bank_mask:0xf
	v_mov_b32_e32 v121, v120
	v_mul_f32_dpp v121, v120, v120 row_shl:8 row_mask:0xf bank_mask:0xf
	v_mov_b32_e32 v123, v25
	v_mov_b32_e32 v58, v36
	v_mul_f32_dpp v58, v36, v36 row_shl:1 row_mask:0xf bank_mask:0xf
	v_mov_b32_e32 v59, v37
	v_mul_f32_dpp v59, v37, v37 row_shl:1 row_mask:0xf bank_mask:0xf
	v_fmac_f32_dpp v54, v54, v36 row_shl:1 row_mask:0xf bank_mask:0xf bound_ctrl:1
	v_mov_b32_e32 v36, v54
	v_fmac_f32_dpp v55, v55, v37 row_shl:1 row_mask:0xf bank_mask:0xf bound_ctrl:1
	v_mov_b32_e32 v37, v55
	v_pk_mul_f32 v[118:119], v[124:125], v[118:119]
	v_pk_mul_f32 v[24:25], v[120:121], v[122:123]
	v_add_f32_e32 v29, 1.0, v29
	v_lshlrev_b32_e32 v86, 16, v87
	v_mov_b32_e32 v120, v118
	v_mov_b32_e32 v121, v24
	v_mov_b32_e32 v56, v58
	v_mul_f32_dpp v56, v58, v58 row_shl:2 row_mask:0xf bank_mask:0xf
	v_mov_b32_e32 v57, v59
	v_mul_f32_dpp v57, v59, v59 row_shl:2 row_mask:0xf bank_mask:0xf
	v_fmac_f32_dpp v36, v36, v58 row_shl:2 row_mask:0xf bank_mask:0xf bound_ctrl:1
	v_fmac_f32_dpp v37, v37, v59 row_shl:2 row_mask:0xf bank_mask:0xf bound_ctrl:1
	v_rcp_f32_e32 v93, v29
	v_mul_f32_e32 v29, 0x3d372713, v86
	v_pk_add_f32 v[38:39], v[38:39], v[120:121]
	v_mov_b32_e32 v24, v119
	v_mul_f32_e32 v29, v29, v86
	v_mov_b32_e32 v30, v86
	v_pk_add_f32 v[24:25], v[38:39], v[24:25]
	v_fmac_f32_dpp v36, v36, v56 row_shl:4 row_mask:0xf bank_mask:0xf bound_ctrl:1
	v_fmac_f32_dpp v37, v37, v57 row_shl:4 row_mask:0xf bank_mask:0xf bound_ctrl:1
	v_mov_b32_e32 v54, v56
	v_mul_f32_dpp v54, v56, v56 row_shl:4 row_mask:0xf bank_mask:0xf
	v_mov_b32_e32 v56, v57
	v_mul_f32_dpp v56, v57, v57 row_shl:4 row_mask:0xf bank_mask:0xf
	s_waitcnt vmcnt(1)
	v_lshlrev_b32_e32 v58, 16, v84
	v_fmac_f32_e32 v30, v29, v30
	ds_bpermute_b32 v39, v151, v24
	ds_bpermute_b32 v119, v151, v25
	v_and_b32_e32 v59, 0xffff0000, v84
	v_mul_f32_e32 v84, 0x3d372713, v58
	v_mul_f32_e32 v29, 0x3fcc422a, v30
	v_mul_f32_e32 v84, v84, v58
	v_mov_b32_e32 v96, v58
	v_mul_f32_e32 v29, 0xbfb8aa3b, v29
	v_fmac_f32_e32 v96, v84, v96
	v_exp_f32_e32 v29, v29
	v_mov_b32_e32 v38, v181
	v_mov_b32_e32 v118, v181
	v_mov_b32_e32 v55, v54
	v_mov_b32_e32 v57, v56
	v_mul_f32_e32 v84, 0x3fcc422a, v96
	v_mov_b32_dpp v38, v36 row_shl:8 row_mask:0xf bank_mask:0xf
	v_mov_b32_dpp v118, v37 row_shl:8 row_mask:0xf bank_mask:0xf
	v_mul_f32_dpp v55, v54, v54 row_shl:8 row_mask:0xf bank_mask:0xf
	v_mul_f32_dpp v57, v56, v56 row_shl:8 row_mask:0xf bank_mask:0xf
	v_mul_f32_e32 v84, 0xbfb8aa3b, v84
	v_exp_f32_e32 v84, v84
	s_waitcnt lgkmcnt(1)
	v_pk_mul_f32 v[38:39], v[54:55], v[38:39]
	s_waitcnt lgkmcnt(0)
	v_pk_mul_f32 v[54:55], v[56:57], v[118:119]
	v_mov_b32_e32 v56, v38
	v_mov_b32_e32 v57, v54
	v_and_b32_e32 v87, 0xffff0000, v87
	v_add_f32_e32 v29, 1.0, v29
	v_pk_add_f32 v[36:37], v[36:37], v[56:57]
	v_mov_b32_e32 v54, v39
	v_mul_f32_e32 v17, 0xbfb8aa3b, v17
	v_mul_f32_e32 v16, 0x3fb8aa3b, v16
	v_rcp_f32_e32 v94, v29
	v_mul_f32_e32 v29, 0x3d372713, v87
	v_pk_add_f32 v[54:55], v[36:37], v[54:55]
	v_exp_f32_e32 v17, v17
	v_exp_f32_e32 v51, v16
	v_mul_f32_e32 v29, v29, v87
	v_mov_b32_e32 v30, v87
	v_add_f32_e32 v84, 1.0, v84
	ds_bpermute_b32 v36, v151, v54
	ds_bpermute_b32 v37, v151, v55
	v_fmac_f32_e32 v30, v29, v30
	v_rcp_f32_e32 v96, v84
	v_mul_f32_e32 v84, 0x3d372713, v59
	v_mul_f32_e32 v29, 0x3fcc422a, v30
	v_mul_f32_e32 v84, v84, v59
	v_mov_b32_e32 v97, v59
	v_mul_f32_e32 v29, 0xbfb8aa3b, v29
	v_fmac_f32_e32 v97, v84, v97
	v_add_f32_e32 v17, 1.0, v17
	v_fma_f32 v16, -v51, v51, 1.0
	s_waitcnt lgkmcnt(0)
	s_barrier
; #define LAS __attribute__((address_space(3)))
; __device__ __forceinline__ unsigned pk2(float lo, float hi) { const f32x2cv v = {lo, hi}; return __builtin_bit_cast(unsigned, __builtin_convertvector(v, bf16x2cv)); }
; __device__ __forceinline__ void lds_barrier() { asm volatile("s_waitcnt lgkmcnt(0)" ::: "memory"); __builtin_amdgcn_s_barrier(); asm volatile("" ::: "memory"); }
; __device__ __forceinline__ float fsigmoid(float x) { return __builtin_amdgcn_rcpf(1.0f + __expf(-x)); }
; __device__ __forceinline__ float bperm_f(int idx4, float x) { return __builtin_bit_cast(float, __builtin_amdgcn_ds_bpermute(idx4, __builtin_bit_cast(int, x))); }
; template <int PASS, bool REV> ...
;     ...
;             f32x4 hin = *(const LAS f32x4*)(CIN + d * 256 + ch);
; #pragma unroll
;             for (int t4 = 0; t4 < 4; ++t4) { const int tg = REV ? 3 - t4 : t4;
; #pragma unroll
;                 for (int j = 0; j < 4; ++j) { const float h = aa[tg][j] * hin[j] + ax[tg][j]; ax[tg][j] = h; hin[j] = bperm_f(lastl4, h); } }
;             LAS float* hs = HS + (ng & 1) * 4096;
;             if (!REV) {
; #pragma unroll
;                 for (int tg = 0; tg < 4; ++tg) *(LAS f32x4*)(hs + (tg * 16 + fr) * 64 + blk * 16 + fq * 4) = ax[tg];
;             }
;             lds_barrier();
;             if (REV && emit) {
; #pragma unroll
;                 for (int tp = 0; tp < 4; tp += 2) { unsigned pkk[2][2];
; #pragma unroll
;                     for (int dm = 0; dm < 2; ++dm) { const int tg = tp + dm; const int tok = tg * 16 + fr; const f32x4 hf = *(const LAS f32x4*)(hs + tok * 64 + blk * 16 + fq * 4);
;                         const v2u gw = gwv[tg]; const float g[4] = {bflo(gw.x), bfhi(gw.x), bflo(gw.y), bfhi(gw.y)}; float y[4];
; #pragma unroll
;                         for (int j = 0; j < 4; ++j) { const float x = g[j]; const float u2 = 1.5957691216057308f * (x + 0.044715f * x * x * x); y[j] = (hf[j] + ax[tg][j]) * x * fsigmoid(u2); }
;                         pkk[dm][0] = pk2(y[0], y[1]); pkk[dm][1] = pk2(y[2], y[3]); }
	v_lshl_add_u32 v28, s5, 2, v152
	v_exp_f32_e32 v29, v29
	v_mul_f32_e32 v84, 0x3fcc422a, v97
	v_rcp_f32_e32 v105, v17
	v_sqrt_f32_e32 v107, v16
	ds_read_b128 v[20:23], v28 offset:36864
	ds_read_b128 v[16:19], v28 offset:40960
	v_mul_f32_e32 v84, 0xbfb8aa3b, v84
	s_waitcnt lgkmcnt(2)
	v_pk_fma_f32 v[38:39], v[134:135], v[36:37], v[132:133]
	v_exp_f32_e32 v84, v84
	ds_bpermute_b32 v36, v151, v38
	ds_bpermute_b32 v37, v151, v39
	v_add_f32_e32 v29, 1.0, v29
	v_mov_b32_e32 v90, v34
	v_mul_f32_dpp v90, v34, v34 row_shl:8 row_mask:0xf bank_mask:0xf
	v_mov_b32_e32 v91, v35
	v_mul_f32_dpp v91, v35, v35 row_shl:8 row_mask:0xf bank_mask:0xf
	v_rcp_f32_e32 v95, v29
	ds_read_b128 v[32:35], v28 offset:45056
	ds_read_b128 v[28:31], v28 offset:49152
	v_add_f32_e32 v84, 1.0, v84
	s_waitcnt lgkmcnt(4)
	v_pk_add_f32 v[16:17], v[38:39], v[16:17]
	v_rcp_f32_e32 v97, v84
	s_waitcnt lgkmcnt(2)
	v_pk_fma_f32 v[36:37], v[116:117], v[36:37], v[112:113]
	v_pk_mul_f32 v[16:17], v[16:17], v[142:143]
	v_pk_add_f32 v[20:21], v[36:37], v[20:21]
	v_pk_mul_f32 v[16:17], v[144:145], v[16:17]
	v_pk_mul_f32 v[20:21], v[20:21], v[114:115]
	v_cvt_pk_bf16_f32 v38, v16, v17
	s_waitcnt lgkmcnt(1)
	v_pk_add_f32 v[16:17], v[54:55], v[32:33]
	v_pk_mul_f32 v[20:21], v[140:141], v[20:21]
	v_pk_mul_f32 v[16:17], v[16:17], v[58:59]
	v_cvt_pk_bf16_f32 v36, v20, v21
	v_pk_mul_f32 v[16:17], v[96:97], v[16:17]
	s_waitcnt vmcnt(0)
	v_lshlrev_b32_e32 v20, 16, v82
	v_cvt_pk_bf16_f32 v16, v16, v17
	v_mul_f32_e32 v17, 0x3d372713, v20
	v_mul_f32_e32 v17, v17, v20
	v_mov_b32_e32 v32, v20
	v_fmac_f32_e32 v32, v17, v32
	v_mul_f32_e32 v17, 0x3fcc422a, v32
	v_mul_f32_e32 v17, 0xbfb8aa3b, v17
	v_exp_f32_e32 v17, v17
	v_and_b32_e32 v21, 0xffff0000, v82
	v_mov_b32_e32 v33, v21
	v_add_f32_e32 v17, 1.0, v17
	v_rcp_f32_e32 v32, v17
	v_mul_f32_e32 v17, 0x3d372713, v21
	v_mul_f32_e32 v17, v17, v21
	v_fmac_f32_e32 v33, v17, v33
	v_mul_f32_e32 v17, 0x3fcc422a, v33
	v_mul_f32_e32 v17, 0xbfb8aa3b, v17
	v_exp_f32_e32 v17, v17
	s_waitcnt lgkmcnt(0)
	v_pk_add_f32 v[24:25], v[24:25], v[28:29]
	v_add_f32_e32 v17, 1.0, v17
	v_rcp_f32_e32 v33, v17
	v_pk_mul_f32 v[20:21], v[24:25], v[20:21]
	v_pk_mul_f32 v[24:25], v[104:105], v[102:103]
	v_pk_mul_f32 v[20:21], v[32:33], v[20:21]
	v_pk_mul_f32 v[24:25], v[106:107], v[24:25]
	v_mov_b32_e32 v32, v50
	v_mul_f32_dpp v32, v50, v50 row_shl:1 row_mask:0xf bank_mask:0xf
	v_mov_b32_e32 v33, v51
	v_mul_f32_dpp v33, v51, v51 row_shl:1 row_mask:0xf bank_mask:0xf
	v_fmac_f32_dpp v24, v24, v50 row_shl:1 row_mask:0xf bank_mask:0xf bound_ctrl:1
	v_fmac_f32_dpp v25, v25, v51 row_shl:1 row_mask:0xf bank_mask:0xf bound_ctrl:1
	v_mov_b32_e32 v50, v32
	v_mul_f32_dpp v50, v32, v32 row_shl:2 row_mask:0xf bank_mask:0xf
	v_mov_b32_e32 v51, v33
	v_mul_f32_dpp v51, v33, v33 row_shl:2 row_mask:0xf bank_mask:0xf
	v_fmac_f32_dpp v24, v24, v32 row_shl:2 row_mask:0xf bank_mask:0xf bound_ctrl:1
	v_fmac_f32_dpp v25, v25, v33 row_shl:2 row_mask:0xf bank_mask:0xf bound_ctrl:1
	v_mov_b32_e32 v54, v50
	v_mul_f32_dpp v54, v50, v50 row_shl:4 row_mask:0xf bank_mask:0xf
	v_fmac_f32_dpp v24, v24, v50 row_shl:4 row_mask:0xf bank_mask:0xf bound_ctrl:1
	v_fmac_f32_dpp v25, v25, v51 row_shl:4 row_mask:0xf bank_mask:0xf bound_ctrl:1
	v_mov_b32_e32 v55, v54
	v_mul_f32_dpp v55, v54, v54 row_shl:8 row_mask:0xf bank_mask:0xf
	v_mov_b32_e32 v50, v51
	v_mul_f32_dpp v50, v51, v51 row_shl:4 row_mask:0xf bank_mask:0xf
	v_mov_b32_e32 v28, v181
	v_mov_b32_e32 v32, v181
	s_nop 0
	v_mov_b32_dpp v28, v24 row_shl:8 row_mask:0xf bank_mask:0xf
	v_mov_b32_dpp v32, v25 row_shl:8 row_mask:0xf bank_mask:0xf
	v_mov_b32_e32 v29, v26
	v_mov_b32_e32 v51, v50
	v_mul_f32_dpp v51, v50, v50 row_shl:8 row_mask:0xf bank_mask:0xf
	v_mov_b32_e32 v33, v27
	v_pk_mul_f32 v[28:29], v[54:55], v[28:29]
	v_pk_mul_f32 v[26:27], v[50:51], v[32:33]
	v_lshlrev_b32_e32 v44, 16, v45
	v_and_b32_e32 v45, 0xffff0000, v45
	v_mov_b32_e32 v32, v28
	v_mov_b32_e32 v33, v26
	v_pk_add_f32 v[24:25], v[24:25], v[32:33]
	v_pk_mul_f32 v[32:33], v[42:43], v[44:45]
	v_pk_mul_f32 v[32:33], v[46:47], v[32:33]
	v_mov_b32_e32 v44, v40
	v_mul_f32_dpp v44, v40, v40 row_shl:1 row_mask:0xf bank_mask:0xf
	v_mov_b32_e32 v45, v41
	v_mul_f32_dpp v45, v41, v41 row_shl:1 row_mask:0xf bank_mask:0xf
	v_fmac_f32_dpp v32, v32, v40 row_shl:1 row_mask:0xf bank_mask:0xf bound_ctrl:1
	v_fmac_f32_dpp v33, v33, v41 row_shl:1 row_mask:0xf bank_mask:0xf bound_ctrl:1
	v_mov_b32_e32 v42, v44
	v_mul_f32_dpp v42, v44, v44 row_shl:2 row_mask:0xf bank_mask:0xf
	v_mov_b32_e32 v43, v45
	v_mul_f32_dpp v43, v45, v45 row_shl:2 row_mask:0xf bank_mask:0xf
	v_fmac_f32_dpp v32, v32, v44 row_shl:2 row_mask:0xf bank_mask:0xf bound_ctrl:1
	v_fmac_f32_dpp v33, v33, v45 row_shl:2 row_mask:0xf bank_mask:0xf bound_ctrl:1
	s_nop 1
	v_fmac_f32_dpp v32, v32, v42 row_shl:4 row_mask:0xf bank_mask:0xf bound_ctrl:1
	v_fmac_f32_dpp v33, v33, v43 row_shl:4 row_mask:0xf bank_mask:0xf bound_ctrl:1
	v_mov_b32_e32 v40, v42
	v_mul_f32_dpp v40, v42, v42 row_shl:4 row_mask:0xf bank_mask:0xf
	v_mov_b32_e32 v42, v43
	v_mul_f32_dpp v42, v43, v43 row_shl:4 row_mask:0xf bank_mask:0xf
	v_mov_b32_e32 v41, v40
	v_mul_f32_dpp v41, v40, v40 row_shl:8 row_mask:0xf bank_mask:0xf
	v_lshlrev_b32_e32 v44, 16, v85
	v_mov_b32_e32 v26, v29
	v_mov_b32_e32 v43, v42
	v_mul_f32_dpp v43, v42, v42 row_shl:8 row_mask:0xf bank_mask:0xf
	v_mul_f32_e32 v17, 0x3d372713, v44
	v_pk_add_f32 v[24:25], v[24:25], v[26:27]
	v_mul_f32_e32 v17, v17, v44
	v_mov_b32_e32 v37, v44
	ds_bpermute_b32 v27, v151, v24
	ds_bpermute_b32 v29, v151, v25
	v_fmac_f32_e32 v37, v17, v37
	v_mul_f32_e32 v17, 0x3fcc422a, v37
	v_mul_f32_e32 v17, 0xbfb8aa3b, v17
	v_mov_b32_e32 v26, v181
	v_mov_b32_e32 v28, v181
	v_exp_f32_e32 v17, v17
	v_mov_b32_dpp v26, v32 row_shl:8 row_mask:0xf bank_mask:0xf
	v_mov_b32_dpp v28, v33 row_shl:8 row_mask:0xf bank_mask:0xf
	s_waitcnt lgkmcnt(1)
; #define LAS __attribute__((address_space(3)))
; __device__ __forceinline__ unsigned pk2(float lo, float hi) { const f32x2cv v = {lo, hi}; return __builtin_bit_cast(unsigned, __builtin_convertvector(v, bf16x2cv)); }
; __device__ __forceinline__ void lds_barrier() { asm volatile("s_waitcnt lgkmcnt(0)" ::: "memory"); __builtin_amdgcn_s_barrier(); asm volatile("" ::: "memory"); }
; __device__ __forceinline__ float fsigmoid(float x) { return __builtin_amdgcn_rcpf(1.0f + __expf(-x)); }
; template <int PASS, bool REV> ...
;     ...
;             for (int t4 = 0; t4 < 4; ++t4) { const int tg = REV ? 3 - t4 : t4;
; #pragma unroll
;                 for (int j = 0; j < 4; ++j) { const float h = aa[tg][j] * hin[j] + ax[tg][j]; ax[tg][j] = h; hin[j] = bperm_f(lastl4, h); } }
;             LAS float* hs = HS + (ng & 1) * 4096;
;             if (!REV) {
; #pragma unroll
;                 for (int tg = 0; tg < 4; ++tg) *(LAS f32x4*)(hs + (tg * 16 + fr) * 64 + blk * 16 + fq * 4) = ax[tg];
;             }
;             lds_barrier();
;             if (REV && emit) {
; #pragma unroll
;                 for (int tp = 0; tp < 4; tp += 2) { unsigned pkk[2][2];
; #pragma unroll
;                     for (int dm = 0; dm < 2; ++dm) { const int tg = tp + dm; const int tok = tg * 16 + fr; const f32x4 hf = *(const LAS f32x4*)(hs + tok * 64 + blk * 16 + fq * 4);
;                         const v2u gw = gwv[tg]; const float g[4] = {bflo(gw.x), bfhi(gw.x), bflo(gw.y), bfhi(gw.y)}; float y[4];
; #pragma unroll
;                         for (int j = 0; j < 4; ++j) { const float x = g[j]; const float u2 = 1.5957691216057308f * (x + 0.044715f * x * x * x); y[j] = (hf[j] + ax[tg][j]) * x * fsigmoid(u2); }
;                         pkk[dm][0] = pk2(y[0], y[1]); pkk[dm][1] = pk2(y[2], y[3]); }
;                     { auto r = __builtin_amdgcn_permlane16_swap(pkk[0][0], pkk[1][0], false, false); pkk[0][0] = r[0]; pkk[1][0] = r[1]; }
;                     { auto r = __builtin_amdgcn_permlane16_swap(pkk[0][1], pkk[1][1], false, false); pkk[0][1] = r[0]; pkk[1][1] = r[1]; }
;                     v4u o; o.x = pkk[0][0]; o.y = pkk[0][1]; o.z = pkk[1][0]; o.w = pkk[1][1];
;                     const int tok = (tp + (fq & 1)) * 16 + fr;
;                     *(v4u*)(MIX + (size_t)(R0 + tok) * 1024 + 768 + ch - (fq & 1) * 4) = o; }
	v_pk_mul_f32 v[26:27], v[40:41], v[26:27]
	s_waitcnt lgkmcnt(0)
	v_pk_mul_f32 v[28:29], v[42:43], v[28:29]
	v_mov_b32_e32 v40, v26
	v_mov_b32_e32 v41, v28
	v_and_b32_e32 v45, 0xffff0000, v85
	v_add_f32_e32 v17, 1.0, v17
	v_pk_add_f32 v[32:33], v[32:33], v[40:41]
	v_mov_b32_e32 v28, v27
	v_rcp_f32_e32 v46, v17
	v_mul_f32_e32 v17, 0x3d372713, v45
	v_pk_add_f32 v[26:27], v[32:33], v[28:29]
	v_mul_f32_e32 v17, v17, v45
	v_mov_b32_e32 v37, v45
	ds_bpermute_b32 v28, v151, v26
	ds_bpermute_b32 v29, v151, v27
	v_fmac_f32_e32 v37, v17, v37
	v_mul_f32_e32 v17, 0x3fcc422a, v37
	v_mul_f32_e32 v17, 0xbfb8aa3b, v17
	v_exp_f32_e32 v17, v17
	s_waitcnt lgkmcnt(0)
	v_pk_fma_f32 v[28:29], v[110:111], v[28:29], v[108:109]
	ds_bpermute_b32 v32, v151, v28
	ds_bpermute_b32 v33, v151, v29
	v_add_f32_e32 v17, 1.0, v17
	v_pk_add_f32 v[18:19], v[28:29], v[18:19]
	v_rcp_f32_e32 v47, v17
	v_pk_mul_f32 v[18:19], v[18:19], v[86:87]
	s_waitcnt lgkmcnt(0)
	v_pk_fma_f32 v[32:33], v[90:91], v[32:33], v[52:53]
	v_pk_mul_f32 v[18:19], v[94:95], v[18:19]
	v_pk_add_f32 v[22:23], v[32:33], v[22:23]
	v_cvt_pk_bf16_f32 v39, v18, v19
	v_pk_add_f32 v[18:19], v[26:27], v[34:35]
	v_pk_mul_f32 v[22:23], v[22:23], v[88:89]
	v_pk_mul_f32 v[18:19], v[18:19], v[44:45]
	v_pk_mul_f32 v[22:23], v[92:93], v[22:23]
	v_pk_mul_f32 v[18:19], v[46:47], v[18:19]
	v_cvt_pk_bf16_f32 v37, v22, v23
	v_cvt_pk_bf16_f32 v17, v18, v19
	v_lshlrev_b32_e32 v18, 16, v83
	v_mul_f32_e32 v22, 0x3d372713, v18
	v_mul_f32_e32 v22, v22, v18
	v_mov_b32_e32 v23, v18
	v_and_b32_e32 v19, 0xffff0000, v83
	v_fmac_f32_e32 v23, v22, v23
	v_mul_f32_e32 v22, 0x3fcc422a, v23
	v_mul_f32_e32 v23, 0x3d372713, v19
	v_mul_f32_e32 v23, v23, v19
	v_mov_b32_e32 v26, v19
	v_fmac_f32_e32 v26, v23, v26
	v_mul_f32_e32 v23, 0x3fcc422a, v26
	v_mul_f32_e32 v22, 0xbfb8aa3b, v22
	v_mul_f32_e32 v23, 0xbfb8aa3b, v23
	v_exp_f32_e32 v22, v22
	v_exp_f32_e32 v23, v23
	v_pk_add_f32 v[24:25], v[24:25], v[30:31]
	v_lshl_add_u64 v[100:101], v[72:73], 0, s[46:47]
	v_add_f32_e32 v22, 1.0, v22
	v_add_f32_e32 v23, 1.0, v23
	v_rcp_f32_e32 v22, v22
	v_rcp_f32_e32 v23, v23
	v_pk_mul_f32 v[18:19], v[24:25], v[18:19]
	v_permlane16_swap_b32_e32 v36, v38
	v_pk_mul_f32 v[22:23], v[22:23], v[18:19]
	v_cvt_pk_bf16_f32 v18, v20, v21
	v_cvt_pk_bf16_f32 v19, v22, v23
	v_permlane16_swap_b32_e32 v37, v39
	v_permlane16_swap_b32_e32 v16, v18
	v_permlane16_swap_b32_e32 v17, v19
	v_lshl_add_u64 v[20:21], v[70:71], 0, s[46:47]
	v_lshl_add_u64 v[70:71], v[70:71], 0, 32
	v_lshl_add_u64 v[72:73], v[72:73], 0, 32
	v_lshl_add_u64 v[74:75], v[74:75], 0, 32
	v_lshl_add_u64 v[76:77], v[76:77], 0, 32
	v_lshl_add_u64 v[78:79], v[78:79], 0, 32
	v_lshl_add_u64 v[80:81], v[80:81], 0, 32
	global_store_dwordx4 v[100:101], v[36:39], off
	global_store_dwordx4 v[20:21], v[16:19], off
	s_cbranch_vccnz .LBB0_766
	s_mov_b64 s[0:1], 0

; #define LAS __attribute__((address_space(3)))
; __device__ __forceinline__ float fsigmoid(float x) { return __builtin_amdgcn_rcpf(1.0f + __expf(-x)); }
; template <int PASS, bool REV> ...
;     ...
;     for (int ng = ng_lo; ng < ng_hi; ++ng) {
;         f32x4 aa[4], ax[4];
;         v2u gwv[4];
; #pragma unroll
;         for (int tg = 0; tg < 4; ++tg) { aa[tg] = (f32x4){0.f, 0.f, 0.f, 0.f}; ax[tg] = (f32x4){0.f, 0.f, 0.f, 0.f}; }
; #pragma unroll
;         for (int kk = 0; kk < 2; ++kk) { const bf16x8 wa = wcur[0][kk], wx = wcur[1][kk]; bf16x8 uf[4][2];
; #pragma unroll
;             for (int tg = 0; tg < 4; ++tg) uf[tg][kk] = *(const LAS bf16x8*)(UB + (tg * 16 + fr) * 264 + blk * 64 + kk * 32 + fq * 8);
; #pragma unroll
;             for (int tg = 0; tg < 4; ++tg) { aa[tg] = __builtin_amdgcn_mfma_f32_16x16x32_bf16(wa, uf[tg][kk], aa[tg], 0, 0, 0); ax[tg] = __builtin_amdgcn_mfma_f32_16x16x32_bf16(wx, uf[tg][kk], ax[tg], 0, 0, 0); } }
;         { const int ng1 = (ng + 1 < ng_hi) ? ng + 1 : ng_lo;
; #pragma unroll
;             for (int gt = 0; gt < 2; ++gt)
; #pragma unroll
;                 for (int kk = 0; kk < 2; ++kk) wcur[gt][kk] = *(const bf16x8*)(Wg + ((size_t)(gt * 4 + blk) * 64 + ng1 * 16 + fr) * 64 + kk * 32 + fq * 8); }
;         if (PASS == 2 && REV && emit) {
; #pragma unroll
;             for (int tg = 0; tg < 4; ++tg) gwv[tg] = *(const v2u*)(P + (size_t)(R0 + tg * 16 + fr) * PROJ + C_RGG + blk * 64 + ng * 16 + fq * 4); }
;         const int ch = blk * 64 + ng * 16 + fq * 4; const f32x4 sp = *(const LAS f32x4*)(cst + ch), bav = *(const LAS f32x4*)(cst + 256 + ch), bxv = *(const LAS f32x4*)(cst + 512 + ch);
; #pragma unroll
;         for (int tg = 0; tg < 4; ++tg) { const v2u uw = *(const LAS v2u*)(UB + (tg * 16 + fr) * 264 + ch); const float uv[4] = {bflo(uw.x), bfhi(uw.x), bflo(uw.y), bfhi(uw.y)};
; #pragma unroll
;             for (int j = 0; j < 4; ++j) { const float r = fsigmoid(aa[tg][j] + bav[j]), ig = fsigmoid(ax[tg][j] + bxv[j]); const float la = -8.0f * r * sp[j];
.LBB0_770:
	ds_read_b128 v[16:19], v189
	ds_read_b128 v[20:23], v189 offset:8448
	ds_read_b128 v[24:27], v189 offset:16896
	ds_read_b128 v[28:31], v189 offset:25344
	s_add_i32 s1, s1, 1
	s_waitcnt vmcnt(0) lgkmcnt(3)
	v_mfma_f32_16x16x32_bf16 v[32:35], v[8:11], v[16:19], 0
	s_cmp_lt_u32 s1, s2
	s_cselect_b32 s5, s1, s3
	v_lshl_add_u32 v180, s5, 4, v154
	v_mfma_f32_16x16x32_bf16 v[16:19], v[12:15], v[16:19], 0
	v_add_u32_e32 v112, 0, v110
	s_waitcnt lgkmcnt(2)
	s_nop 1
	v_mfma_f32_16x16x32_bf16 v[36:39], v[8:11], v[20:23], 0
	s_nop 2
	v_mfma_f32_16x16x32_bf16 v[20:23], v[12:15], v[20:23], 0
	s_waitcnt lgkmcnt(1)
	s_nop 2
	v_mfma_f32_16x16x32_bf16 v[40:43], v[8:11], v[24:27], 0
	s_nop 2
	v_mfma_f32_16x16x32_bf16 v[24:27], v[12:15], v[24:27], 0
	s_waitcnt lgkmcnt(0)
	s_nop 2
	v_mfma_f32_16x16x32_bf16 v[8:11], v[8:11], v[28:31], 0
	s_and_b32 s4, s0, 0x1000
	s_addk_i32 s0, 0x1000
	s_cmp_ge_u32 s1, s2
	v_mfma_f32_16x16x32_bf16 v[12:15], v[12:15], v[28:31], 0
	ds_read_b128 v[28:31], v189 offset:64
	ds_read_b128 v[44:47], v189 offset:8512
	ds_read_b128 v[70:73], v189 offset:16960
	ds_read_b128 v[74:77], v189 offset:25408
	v_add_u32_e32 v110, 64, v110
	s_waitcnt lgkmcnt(3)
	v_mfma_f32_16x16x32_bf16 v[56:59], v[0:3], v[28:31], v[32:35]
	s_waitcnt lgkmcnt(2)
	v_mfma_f32_16x16x32_bf16 v[48:51], v[0:3], v[44:47], v[36:39]
	v_mfma_f32_16x16x32_bf16 v[44:47], v[4:7], v[44:47], v[20:23]
	s_waitcnt lgkmcnt(1)
	v_mfma_f32_16x16x32_bf16 v[40:43], v[0:3], v[70:73], v[40:43]
	s_waitcnt lgkmcnt(0)
	v_mfma_f32_16x16x32_bf16 v[20:23], v[0:3], v[74:77], v[8:11]
	v_lshlrev_b64 v[0:1], 7, v[180:181]
	v_add_u32_e32 v180, 0x100, v180
	v_lshl_add_u64 v[0:1], v[62:63], 0, v[0:1]
	v_mfma_f32_16x16x32_bf16 v[52:55], v[4:7], v[28:31], v[16:19]
	v_add_u32_e32 v28, 0x11400, v112
	global_load_dwordx4 v[8:11], v[0:1], off
	s_nop 0
	global_load_dwordx4 v[0:3], v[0:1], off offset:64
	v_mfma_f32_16x16x32_bf16 v[36:39], v[4:7], v[70:73], v[24:27]
	v_mfma_f32_16x16x32_bf16 v[16:19], v[4:7], v[74:77], v[12:15]
	v_lshlrev_b64 v[4:5], 7, v[180:181]
	v_lshl_add_u64 v[4:5], v[62:63], 0, v[4:5]
	v_add_u32_e32 v24, 0x11000, v112
	global_load_dwordx4 v[12:15], v[4:5], off
	s_nop 0
	global_load_dwordx4 v[4:7], v[4:5], off offset:64
	ds_read_b128 v[24:27], v24
	ds_read_b128 v[32:35], v28
	v_add_u32_e32 v28, 0x11800, v112
	ds_read_b128 v[28:31], v28
	v_add_u32_e32 v76, 0, v111
	ds_read_b64 v[70:71], v76
	s_waitcnt lgkmcnt(2)
	v_add_f32_e32 v40, v40, v32
	v_mul_f32_e32 v40, 0xbfb8aa3b, v40
	v_exp_f32_e32 v40, v40
	s_waitcnt lgkmcnt(1)
	v_add_f32_e32 v36, v36, v28
	v_mul_f32_e32 v36, 0xbfb8aa3b, v36
	v_exp_f32_e32 v36, v36
	v_add_f32_e32 v40, 1.0, v40
	v_rcp_f32_e32 v40, v40
	v_add_f32_e32 v48, v48, v32
	v_mul_f32_e32 v48, 0xbfb8aa3b, v48
	v_exp_f32_e32 v48, v48
	v_add_f32_e32 v36, 1.0, v36
	v_rcp_f32_e32 v74, v36
	v_mul_f32_e32 v36, 0xc1000000, v40
	v_add_f32_e32 v44, v44, v28
	v_mul_f32_e32 v36, v24, v36
	v_mul_f32_e32 v44, 0xbfb8aa3b, v44
	v_mul_f32_e32 v36, 0x3fb8aa3b, v36
	v_add_f32_e32 v48, 1.0, v48
	v_exp_f32_e32 v44, v44
	v_exp_f32_e32 v40, v36
	v_rcp_f32_e32 v48, v48
	v_add_f32_e32 v20, v20, v32
	v_add_f32_e32 v44, 1.0, v44
	v_fma_f32 v36, -v40, v40, 1.0
	v_rcp_f32_e32 v86, v44
	v_mul_f32_e32 v44, 0xc1000000, v48
	v_sqrt_f32_e32 v78, v36
	v_add_f32_e32 v36, v41, v33
	v_mul_f32_e32 v44, v24, v44
	v_mul_f32_e32 v36, 0xbfb8aa3b, v36
	v_mul_f32_e32 v44, 0x3fb8aa3b, v44
	v_exp_f32_e32 v36, v36
	v_exp_f32_e32 v48, v44
	v_mul_f32_e32 v20, 0xbfb8aa3b, v20
	v_exp_f32_e32 v20, v20
	v_add_f32_e32 v36, 1.0, v36
	v_fma_f32 v44, -v48, v48, 1.0
	v_rcp_f32_e32 v36, v36
	v_sqrt_f32_e32 v94, v44
	v_add_f32_e32 v44, v49, v33
	v_mul_f32_e32 v44, 0xbfb8aa3b, v44
	v_exp_f32_e32 v44, v44
	v_add_f32_e32 v56, v56, v32
	v_mul_f32_e32 v36, 0xc1000000, v36
	v_mul_f32_e32 v56, 0xbfb8aa3b, v56
	v_mul_f32_e32 v36, v25, v36
	v_add_f32_e32 v16, v16, v28
	v_exp_f32_e32 v56, v56
	v_mul_f32_e32 v36, 0x3fb8aa3b, v36
	v_mul_f32_e32 v16, 0xbfb8aa3b, v16
	v_add_f32_e32 v44, 1.0, v44
	v_exp_f32_e32 v41, v36
	v_add_f32_e32 v20, 1.0, v20
	v_exp_f32_e32 v16, v16
	v_add_f32_e32 v52, v52, v28
	v_rcp_f32_e32 v44, v44
	v_rcp_f32_e32 v20, v20
	v_mul_f32_e32 v52, 0xbfb8aa3b, v52
	v_add_f32_e32 v56, 1.0, v56
	v_exp_f32_e32 v52, v52
	v_rcp_f32_e32 v56, v56
	v_fma_f32 v36, -v41, v41, 1.0
	v_add_f32_e32 v16, 1.0, v16
	v_mul_f32_e32 v44, 0xc1000000, v44
	v_sqrt_f32_e32 v79, v36
	v_add_f32_e32 v36, v42, v34
	v_rcp_f32_e32 v42, v16
	v_mul_f32_e32 v16, 0xc1000000, v20
	v_mul_f32_e32 v44, v25, v44
	v_mul_f32_e32 v16, v24, v16
	v_add_f32_e32 v52, 1.0, v52
	v_mul_f32_e32 v44, 0x3fb8aa3b, v44
	v_mul_f32_e32 v16, 0x3fb8aa3b, v16
	v_rcp_f32_e32 v90, v52
	v_mul_f32_e32 v52, 0xc1000000, v56
	v_exp_f32_e32 v49, v44
	v_exp_f32_e32 v28, v16
	v_mul_f32_e32 v52, v24, v52
	v_mul_f32_e32 v52, 0x3fb8aa3b, v52
	v_exp_f32_e32 v56, v52
	v_fma_f32 v44, -v49, v49, 1.0
	v_fma_f32 v16, -v28, v28, 1.0
	v_sqrt_f32_e32 v95, v44
	v_add_f32_e32 v44, v50, v34
	v_sqrt_f32_e32 v50, v16
	v_add_f32_e32 v16, v21, v33
	v_mul_f32_e32 v44, 0xbfb8aa3b, v44
	v_mul_f32_e32 v16, 0xbfb8aa3b, v16
	v_fma_f32 v52, -v56, v56, 1.0
	v_exp_f32_e32 v44, v44
	v_exp_f32_e32 v16, v16
	v_sqrt_f32_e32 v96, v52
	v_add_f32_e32 v52, v57, v33
	v_mul_f32_e32 v52, 0xbfb8aa3b, v52
	v_exp_f32_e32 v52, v52
	v_add_f32_e32 v44, 1.0, v44
	v_add_f32_e32 v16, 1.0, v16
	v_add_f32_e32 v45, v45, v29
	v_rcp_f32_e32 v44, v44
	v_rcp_f32_e32 v16, v16
	v_mul_f32_e32 v45, 0xbfb8aa3b, v45
	v_add_f32_e32 v52, 1.0, v52
	v_exp_f32_e32 v45, v45
	v_rcp_f32_e32 v52, v52
	v_mul_f32_e32 v44, 0xc1000000, v44
	v_mul_f32_e32 v16, 0xc1000000, v16
	v_mul_f32_e32 v44, v26, v44
	v_mul_f32_e32 v16, v25, v16
	v_add_f32_e32 v45, 1.0, v45
; #define LAS __attribute__((address_space(3)))
; __device__ __forceinline__ float fsigmoid(float x) { return __builtin_amdgcn_rcpf(1.0f + __expf(-x)); }
; __device__ __forceinline__ float bperm_f(int idx4, float x) { return __builtin_bit_cast(float, __builtin_amdgcn_ds_bpermute(idx4, __builtin_bit_cast(int, x))); }
; template <int PASS, bool REV> ...
;     ...
;         for (int tg = 0; tg < 4; ++tg) { const v2u uw = *(const LAS v2u*)(UB + (tg * 16 + fr) * 264 + ch); const float uv[4] = {bflo(uw.x), bfhi(uw.x), bflo(uw.y), bfhi(uw.y)};
; #pragma unroll
;             for (int j = 0; j < 4; ++j) { const float r = fsigmoid(aa[tg][j] + bav[j]), ig = fsigmoid(ax[tg][j] + bxv[j]); const float la = -8.0f * r * sp[j];
;                 float Av = __expf(la); const float om = __builtin_fmaf(-Av, Av, 1.0f);
;                 float Bv = __builtin_amdgcn_sqrtf(om) * (ig * uv[j]);
;                 rg_scan_step<REV, 1>(Av, Bv); rg_scan_step<REV, 2>(Av, Bv); rg_scan_step<REV, 4>(Av, Bv); rg_scan_step<REV, 8>(Av, Bv);
;                 aa[tg][j] = Av; ax[tg][j] = Bv; } }
;         const int lastl4 = ((lane & 48) | (REV ? 0 : 15)) << 2;
;         if (PASS == 1) {
;             f32x4 At = (f32x4){1.f, 1.f, 1.f, 1.f}, Bt = (f32x4){0.f, 0.f, 0.f, 0.f};
; #pragma unroll
;             for (int t4 = 0; t4 < 4; ++t4) { const int tg = REV ? 3 - t4 : t4;
; #pragma unroll
;                 for (int j = 0; j < 4; ++j) { const float ta = bperm_f(lastl4, aa[tg][j]), tb = bperm_f(lastl4, ax[tg][j]); Bt[j] = ta * Bt[j] + tb; At[j] = At[j] * ta; } }
;             if (fr == 0) { f32x4* cp = (f32x4*)(CAR + ((size_t)u * 2 + d) * 256 + ch); cp[0] = (f32x4){At[0], Bt[0], At[1], Bt[1]}; cp[1] = (f32x4){At[2], Bt[2], At[3], Bt[3]}; }
;         } else {
;             f32x4 hin = *(const LAS f32x4*)(CIN + d * 256 + ch);
; #pragma unroll
;             for (int t4 = 0; t4 < 4; ++t4) { const int tg = REV ? 3 - t4 : t4;
; #pragma unroll
;                 for (int j = 0; j < 4; ++j) { const float h = aa[tg][j] * hin[j] + ax[tg][j]; ax[tg][j] = h; hin[j] = bperm_f(lastl4, h); } }
	v_mul_f32_e32 v44, 0x3fb8aa3b, v44
	v_mul_f32_e32 v16, 0x3fb8aa3b, v16
	v_add_f32_e32 v53, v53, v29
	v_mul_f32_e32 v52, 0xc1000000, v52
	v_rcp_f32_e32 v87, v45
	v_add_f32_e32 v45, v46, v30
	v_exp_f32_e32 v46, v44
	v_add_f32_e32 v37, v37, v29
	v_add_f32_e32 v17, v17, v29
	v_exp_f32_e32 v29, v16
	v_mul_f32_e32 v52, v25, v52
	v_mul_f32_e32 v36, 0xbfb8aa3b, v36
	v_mul_f32_e32 v52, 0x3fb8aa3b, v52
	v_exp_f32_e32 v36, v36
	v_exp_f32_e32 v57, v52
	v_fma_f32 v44, -v46, v46, 1.0
	v_fma_f32 v16, -v29, v29, 1.0
	v_sqrt_f32_e32 v84, v44
	v_add_f32_e32 v44, v51, v35
	v_sqrt_f32_e32 v51, v16
	v_add_f32_e32 v16, v22, v34
	v_add_f32_e32 v36, 1.0, v36
	v_mul_f32_e32 v16, 0xbfb8aa3b, v16
	v_fma_f32 v52, -v57, v57, 1.0
	v_rcp_f32_e32 v36, v36
	v_exp_f32_e32 v16, v16
	v_sqrt_f32_e32 v97, v52
	v_add_f32_e32 v52, v58, v34
	v_mul_f32_e32 v37, 0xbfb8aa3b, v37
	v_mul_f32_e32 v52, 0xbfb8aa3b, v52
	v_exp_f32_e32 v37, v37
	v_exp_f32_e32 v52, v52
	v_mul_f32_e32 v36, 0xc1000000, v36
	v_add_f32_e32 v16, 1.0, v16
	v_mul_f32_e32 v36, v26, v36
	v_rcp_f32_e32 v16, v16
	v_mul_f32_e32 v53, 0xbfb8aa3b, v53
	v_add_f32_e32 v37, 1.0, v37
	v_mul_f32_e32 v36, 0x3fb8aa3b, v36
	v_mul_f32_e32 v17, 0xbfb8aa3b, v17
	v_exp_f32_e32 v53, v53
	v_add_f32_e32 v52, 1.0, v52
	v_rcp_f32_e32 v75, v37
	v_add_f32_e32 v37, v38, v30
	v_exp_f32_e32 v38, v36
	v_exp_f32_e32 v17, v17
	v_rcp_f32_e32 v52, v52
	v_mul_f32_e32 v16, 0xc1000000, v16
	v_mul_f32_e32 v16, v26, v16
	v_add_f32_e32 v53, 1.0, v53
	v_fma_f32 v36, -v38, v38, 1.0
	v_add_f32_e32 v17, 1.0, v17
	v_mul_f32_e32 v16, 0x3fb8aa3b, v16
	v_rcp_f32_e32 v91, v53
	v_add_f32_e32 v53, v54, v30
	v_mul_f32_e32 v52, 0xc1000000, v52
	v_sqrt_f32_e32 v72, v36
	v_add_f32_e32 v36, v43, v35
	v_rcp_f32_e32 v43, v17
	v_add_f32_e32 v17, v18, v30
	v_exp_f32_e32 v30, v16
	v_mul_f32_e32 v52, v26, v52
	v_mul_f32_e32 v52, 0x3fb8aa3b, v52
	v_exp_f32_e32 v54, v52
	v_fma_f32 v16, -v30, v30, 1.0
	v_sqrt_f32_e32 v34, v16
	v_add_f32_e32 v16, v23, v35
	v_mul_f32_e32 v16, 0xbfb8aa3b, v16
	v_fma_f32 v52, -v54, v54, 1.0
	v_exp_f32_e32 v16, v16
	v_sqrt_f32_e32 v102, v52
	v_add_f32_e32 v52, v59, v35
	v_mul_f32_e32 v52, 0xbfb8aa3b, v52
	v_exp_f32_e32 v52, v52
	v_mul_f32_e32 v44, 0xbfb8aa3b, v44
	v_mul_f32_e32 v36, 0xbfb8aa3b, v36
	v_mul_f32_e32 v17, 0xbfb8aa3b, v17
	v_add_f32_e32 v16, 1.0, v16
	v_exp_f32_e32 v44, v44
	v_exp_f32_e32 v36, v36
	v_exp_f32_e32 v17, v17
	v_rcp_f32_e32 v16, v16
	v_mul_f32_e32 v53, 0xbfb8aa3b, v53
	v_mul_f32_e32 v45, 0xbfb8aa3b, v45
	v_mul_f32_e32 v37, 0xbfb8aa3b, v37
	v_exp_f32_e32 v53, v53
	v_add_f32_e32 v52, 1.0, v52
	v_exp_f32_e32 v45, v45
	v_exp_f32_e32 v37, v37
	v_rcp_f32_e32 v52, v52
	v_add_f32_e32 v44, 1.0, v44
	v_add_f32_e32 v36, 1.0, v36
	v_add_f32_e32 v17, 1.0, v17
	v_mul_f32_e32 v16, 0xc1000000, v16
	v_rcp_f32_e32 v44, v44
	v_rcp_f32_e32 v36, v36
	v_rcp_f32_e32 v32, v17
	v_add_f32_e32 v17, v19, v31
	v_mul_f32_e32 v16, v27, v16
	v_add_f32_e32 v53, 1.0, v53
	v_add_f32_e32 v45, 1.0, v45
	v_add_f32_e32 v37, 1.0, v37
	v_mul_f32_e32 v17, 0xbfb8aa3b, v17
	v_mul_f32_e32 v16, 0x3fb8aa3b, v16
	s_waitcnt lgkmcnt(0)
	v_lshlrev_b32_e32 v20, 16, v70
	v_and_b32_e32 v21, 0xffff0000, v70
	v_rcp_f32_e32 v98, v53
	v_add_f32_e32 v53, v55, v31
	v_mul_f32_e32 v52, 0xc1000000, v52
	v_rcp_f32_e32 v82, v45
	v_add_f32_e32 v45, v47, v31
	v_rcp_f32_e32 v58, v37
	v_add_f32_e32 v37, v39, v31
	v_exp_f32_e32 v17, v17
	v_exp_f32_e32 v31, v16
	v_pk_mul_f32 v[20:21], v[90:91], v[20:21]
	v_mul_f32_e32 v53, 0xbfb8aa3b, v53
	v_mul_f32_e32 v52, v27, v52
	v_pk_mul_f32 v[20:21], v[20:21], v[96:97]
	v_exp_f32_e32 v53, v53
	v_mul_f32_e32 v52, 0x3fb8aa3b, v52
	v_mul_f32_e32 v44, 0xc1000000, v44
	v_mul_f32_e32 v36, 0xc1000000, v36
	v_exp_f32_e32 v55, v52
	v_mul_f32_e32 v44, v27, v44
	v_mul_f32_e32 v36, v27, v36
	v_mov_b32_e32 v24, v56
	v_mul_f32_dpp v24, v56, v56 row_shr:1 row_mask:0xf bank_mask:0xf
	v_mov_b32_e32 v25, v57
	v_mul_f32_dpp v25, v57, v57 row_shr:1 row_mask:0xf bank_mask:0xf
	v_fmac_f32_dpp v20, v20, v56 row_shr:1 row_mask:0xf bank_mask:0xf bound_ctrl:1
	v_fmac_f32_dpp v21, v21, v57 row_shr:1 row_mask:0xf bank_mask:0xf bound_ctrl:1
	v_add_f32_e32 v17, 1.0, v17
	v_fma_f32 v16, -v31, v31, 1.0
	v_rcp_f32_e32 v33, v17
	v_sqrt_f32_e32 v35, v16
	ds_read_b128 v[16:19], v112 offset:34816
	v_mov_b32_e32 v26, v24
	v_mul_f32_dpp v26, v24, v24 row_shr:2 row_mask:0xf bank_mask:0xf
	v_mov_b32_e32 v27, v25
	v_mul_f32_dpp v27, v25, v25 row_shr:2 row_mask:0xf bank_mask:0xf
	v_fmac_f32_dpp v20, v20, v24 row_shr:2 row_mask:0xf bank_mask:0xf bound_ctrl:1
	v_fmac_f32_dpp v21, v21, v25 row_shr:2 row_mask:0xf bank_mask:0xf bound_ctrl:1
	v_add_f32_e32 v53, 1.0, v53
	v_rcp_f32_e32 v99, v53
	v_fma_f32 v52, -v55, v55, 1.0
	v_mov_b32_e32 v24, v26
	v_mul_f32_dpp v24, v26, v26 row_shr:4 row_mask:0xf bank_mask:0xf
	v_mov_b32_e32 v25, v27
	v_mul_f32_dpp v25, v27, v27 row_shr:4 row_mask:0xf bank_mask:0xf
	v_fmac_f32_dpp v20, v20, v26 row_shr:4 row_mask:0xf bank_mask:0xf bound_ctrl:1
	v_fmac_f32_dpp v21, v21, v27 row_shr:4 row_mask:0xf bank_mask:0xf bound_ctrl:1
	v_sqrt_f32_e32 v103, v52
	s_nop 0
	v_fmac_f32_dpp v20, v20, v24 row_shr:8 row_mask:0xf bank_mask:0xf bound_ctrl:1
	v_fmac_f32_dpp v21, v21, v25 row_shr:8 row_mask:0xf bank_mask:0xf bound_ctrl:1
	v_mov_b32_e32 v22, v24
	v_mul_f32_dpp v22, v24, v24 row_shr:8 row_mask:0xf bank_mask:0xf
	v_mov_b32_e32 v23, v25
	v_mul_f32_dpp v23, v25, v25 row_shr:8 row_mask:0xf bank_mask:0xf
	s_waitcnt lgkmcnt(0)
; #define LAS __attribute__((address_space(3)))
; __device__ __forceinline__ float fsigmoid(float x) { return __builtin_amdgcn_rcpf(1.0f + __expf(-x)); }
; __device__ __forceinline__ float bperm_f(int idx4, float x) { return __builtin_bit_cast(float, __builtin_amdgcn_ds_bpermute(idx4, __builtin_bit_cast(int, x))); }
; template <int PASS, bool REV> ...
;     ...
;         for (int tg = 0; tg < 4; ++tg) { const v2u uw = *(const LAS v2u*)(UB + (tg * 16 + fr) * 264 + ch); const float uv[4] = {bflo(uw.x), bfhi(uw.x), bflo(uw.y), bfhi(uw.y)};
; #pragma unroll
;             for (int j = 0; j < 4; ++j) { const float r = fsigmoid(aa[tg][j] + bav[j]), ig = fsigmoid(ax[tg][j] + bxv[j]); const float la = -8.0f * r * sp[j];
;                 float Av = __expf(la); const float om = __builtin_fmaf(-Av, Av, 1.0f);
;                 float Bv = __builtin_amdgcn_sqrtf(om) * (ig * uv[j]);
;                 rg_scan_step<REV, 1>(Av, Bv); rg_scan_step<REV, 2>(Av, Bv); rg_scan_step<REV, 4>(Av, Bv); rg_scan_step<REV, 8>(Av, Bv);
;                 aa[tg][j] = Av; ax[tg][j] = Bv; } }
;         const int lastl4 = ((lane & 48) | (REV ? 0 : 15)) << 2;
;         if (PASS == 1) {
;             f32x4 At = (f32x4){1.f, 1.f, 1.f, 1.f}, Bt = (f32x4){0.f, 0.f, 0.f, 0.f};
; #pragma unroll
;             for (int t4 = 0; t4 < 4; ++t4) { const int tg = REV ? 3 - t4 : t4;
; #pragma unroll
;                 for (int j = 0; j < 4; ++j) { const float ta = bperm_f(lastl4, aa[tg][j]), tb = bperm_f(lastl4, ax[tg][j]); Bt[j] = ta * Bt[j] + tb; At[j] = At[j] * ta; } }
;             if (fr == 0) { f32x4* cp = (f32x4*)(CAR + ((size_t)u * 2 + d) * 256 + ch); cp[0] = (f32x4){At[0], Bt[0], At[1], Bt[1]}; cp[1] = (f32x4){At[2], Bt[2], At[3], Bt[3]}; }
;         } else {
;             f32x4 hin = *(const LAS f32x4*)(CIN + d * 256 + ch);
; #pragma unroll
;             for (int t4 = 0; t4 < 4; ++t4) { const int tg = REV ? 3 - t4 : t4;
; #pragma unroll
;                 for (int j = 0; j < 4; ++j) { const float h = aa[tg][j] * hin[j] + ax[tg][j]; ax[tg][j] = h; hin[j] = bperm_f(lastl4, h); } }
	v_pk_fma_f32 v[16:17], v[22:23], v[16:17], v[20:21]
	v_lshlrev_b32_e32 v22, 16, v71
	v_and_b32_e32 v23, 0xffff0000, v71
	v_pk_mul_f32 v[22:23], v[98:99], v[22:23]
	v_pk_mul_f32 v[22:23], v[22:23], v[102:103]
	v_mov_b32_e32 v26, v54
	v_mul_f32_dpp v26, v54, v54 row_shr:1 row_mask:0xf bank_mask:0xf
	v_mov_b32_e32 v27, v55
	v_mul_f32_dpp v27, v55, v55 row_shr:1 row_mask:0xf bank_mask:0xf
	v_fmac_f32_dpp v22, v22, v54 row_shr:1 row_mask:0xf bank_mask:0xf bound_ctrl:1
	v_fmac_f32_dpp v23, v23, v55 row_shr:1 row_mask:0xf bank_mask:0xf bound_ctrl:1
	v_mul_f32_e32 v45, 0xbfb8aa3b, v45
	v_mul_f32_e32 v44, 0x3fb8aa3b, v44
	v_mul_f32_e32 v37, 0xbfb8aa3b, v37
	v_mul_f32_e32 v36, 0x3fb8aa3b, v36
	ds_read_b64 v[52:53], v76 offset:8448
	v_exp_f32_e32 v45, v45
	v_exp_f32_e32 v47, v44
	v_exp_f32_e32 v37, v37
	v_exp_f32_e32 v39, v36
	v_mov_b32_e32 v54, v26
	v_mul_f32_dpp v54, v26, v26 row_shr:2 row_mask:0xf bank_mask:0xf
	v_mov_b32_e32 v55, v27
	v_mul_f32_dpp v55, v27, v27 row_shr:2 row_mask:0xf bank_mask:0xf
	v_fmac_f32_dpp v22, v22, v26 row_shr:2 row_mask:0xf bank_mask:0xf bound_ctrl:1
	v_fmac_f32_dpp v23, v23, v27 row_shr:2 row_mask:0xf bank_mask:0xf bound_ctrl:1
	v_mov_b32_e32 v26, v54
	v_mul_f32_dpp v26, v54, v54 row_shr:4 row_mask:0xf bank_mask:0xf
	v_mov_b32_e32 v27, v55
	v_mul_f32_dpp v27, v55, v55 row_shr:4 row_mask:0xf bank_mask:0xf
	v_fmac_f32_dpp v22, v22, v54 row_shr:4 row_mask:0xf bank_mask:0xf bound_ctrl:1
	v_fmac_f32_dpp v23, v23, v55 row_shr:4 row_mask:0xf bank_mask:0xf bound_ctrl:1
	v_add_f32_e32 v45, 1.0, v45
	v_fma_f32 v44, -v47, v47, 1.0
	v_add_f32_e32 v37, 1.0, v37
	v_fma_f32 v36, -v39, v39, 1.0
	v_fmac_f32_dpp v22, v22, v26 row_shr:8 row_mask:0xf bank_mask:0xf bound_ctrl:1
	v_fmac_f32_dpp v23, v23, v27 row_shr:8 row_mask:0xf bank_mask:0xf bound_ctrl:1
	v_mov_b32_e32 v24, v26
	v_mul_f32_dpp v24, v26, v26 row_shr:8 row_mask:0xf bank_mask:0xf
	v_mov_b32_e32 v25, v27
	v_mul_f32_dpp v25, v27, v27 row_shr:8 row_mask:0xf bank_mask:0xf
	v_rcp_f32_e32 v83, v45
	v_sqrt_f32_e32 v85, v44
	ds_read_b64 v[44:45], v76 offset:16896
	v_rcp_f32_e32 v59, v37
	v_sqrt_f32_e32 v73, v36
	ds_read_b64 v[36:37], v76 offset:25344
	v_pk_fma_f32 v[18:19], v[24:25], v[18:19], v[22:23]
	s_waitcnt lgkmcnt(2)
	v_lshlrev_b32_e32 v24, 16, v52
	v_and_b32_e32 v25, 0xffff0000, v52
	v_pk_mul_f32 v[24:25], v[86:87], v[24:25]
	v_pk_mul_f32 v[24:25], v[94:95], v[24:25]
	v_mov_b32_e32 v54, v48
	v_mul_f32_dpp v54, v48, v48 row_shr:1 row_mask:0xf bank_mask:0xf
	v_mov_b32_e32 v55, v49
	v_mul_f32_dpp v55, v49, v49 row_shr:1 row_mask:0xf bank_mask:0xf
	v_fmac_f32_dpp v24, v24, v48 row_shr:1 row_mask:0xf bank_mask:0xf bound_ctrl:1
	v_fmac_f32_dpp v25, v25, v49 row_shr:1 row_mask:0xf bank_mask:0xf bound_ctrl:1
	ds_bpermute_b32 v20, v155, v16
	ds_bpermute_b32 v21, v155, v17
	v_mov_b32_e32 v48, v54
	v_mul_f32_dpp v48, v54, v54 row_shr:2 row_mask:0xf bank_mask:0xf
	v_mov_b32_e32 v49, v55
	v_mul_f32_dpp v49, v55, v55 row_shr:2 row_mask:0xf bank_mask:0xf
	v_fmac_f32_dpp v24, v24, v54 row_shr:2 row_mask:0xf bank_mask:0xf bound_ctrl:1
	v_fmac_f32_dpp v25, v25, v55 row_shr:2 row_mask:0xf bank_mask:0xf bound_ctrl:1
	v_mov_b32_e32 v54, v48
	v_mul_f32_dpp v54, v48, v48 row_shr:4 row_mask:0xf bank_mask:0xf
	v_mov_b32_e32 v55, v49
	v_mul_f32_dpp v55, v49, v49 row_shr:4 row_mask:0xf bank_mask:0xf
	v_fmac_f32_dpp v24, v24, v48 row_shr:4 row_mask:0xf bank_mask:0xf bound_ctrl:1
	v_fmac_f32_dpp v25, v25, v49 row_shr:4 row_mask:0xf bank_mask:0xf bound_ctrl:1
	s_nop 1
	v_fmac_f32_dpp v24, v24, v54 row_shr:8 row_mask:0xf bank_mask:0xf bound_ctrl:1
	v_fmac_f32_dpp v25, v25, v55 row_shr:8 row_mask:0xf bank_mask:0xf bound_ctrl:1
	v_mov_b32_e32 v26, v54
	v_mul_f32_dpp v26, v54, v54 row_shr:8 row_mask:0xf bank_mask:0xf
	v_mov_b32_e32 v27, v55
	v_mul_f32_dpp v27, v55, v55 row_shr:8 row_mask:0xf bank_mask:0xf
	s_waitcnt lgkmcnt(0)
	v_pk_fma_f32 v[20:21], v[26:27], v[20:21], v[24:25]
	v_lshlrev_b32_e32 v26, 16, v53
	v_and_b32_e32 v27, 0xffff0000, v53
	v_pk_mul_f32 v[26:27], v[82:83], v[26:27]
	v_pk_mul_f32 v[26:27], v[84:85], v[26:27]
	v_mov_b32_e32 v52, v46
	v_mul_f32_dpp v52, v46, v46 row_shr:1 row_mask:0xf bank_mask:0xf
	v_mov_b32_e32 v53, v47
	v_mul_f32_dpp v53, v47, v47 row_shr:1 row_mask:0xf bank_mask:0xf
	v_fmac_f32_dpp v26, v26, v46 row_shr:1 row_mask:0xf bank_mask:0xf bound_ctrl:1
	v_fmac_f32_dpp v27, v27, v47 row_shr:1 row_mask:0xf bank_mask:0xf bound_ctrl:1
	ds_bpermute_b32 v22, v155, v18
	ds_bpermute_b32 v23, v155, v19
	v_mov_b32_e32 v48, v52
	v_mul_f32_dpp v48, v52, v52 row_shr:2 row_mask:0xf bank_mask:0xf
	v_mov_b32_e32 v49, v53
	v_mul_f32_dpp v49, v53, v53 row_shr:2 row_mask:0xf bank_mask:0xf
	v_fmac_f32_dpp v26, v26, v52 row_shr:2 row_mask:0xf bank_mask:0xf bound_ctrl:1
	v_fmac_f32_dpp v27, v27, v53 row_shr:2 row_mask:0xf bank_mask:0xf bound_ctrl:1
	v_mov_b32_e32 v52, v48
	v_mul_f32_dpp v52, v48, v48 row_shr:4 row_mask:0xf bank_mask:0xf
	v_mov_b32_e32 v53, v49
	v_mul_f32_dpp v53, v49, v49 row_shr:4 row_mask:0xf bank_mask:0xf
	v_fmac_f32_dpp v26, v26, v48 row_shr:4 row_mask:0xf bank_mask:0xf bound_ctrl:1
	v_fmac_f32_dpp v27, v27, v49 row_shr:4 row_mask:0xf bank_mask:0xf bound_ctrl:1
	s_nop 1
	v_fmac_f32_dpp v26, v26, v52 row_shr:8 row_mask:0xf bank_mask:0xf bound_ctrl:1
	v_fmac_f32_dpp v27, v27, v53 row_shr:8 row_mask:0xf bank_mask:0xf bound_ctrl:1
	v_mov_b32_e32 v46, v52
	v_mul_f32_dpp v46, v52, v52 row_shr:8 row_mask:0xf bank_mask:0xf
	v_mov_b32_e32 v47, v53
	v_mul_f32_dpp v47, v53, v53 row_shr:8 row_mask:0xf bank_mask:0xf
	s_waitcnt lgkmcnt(0)
; #define LAS __attribute__((address_space(3)))
; __device__ __forceinline__ float fsigmoid(float x) { return __builtin_amdgcn_rcpf(1.0f + __expf(-x)); }
; __device__ __forceinline__ float bperm_f(int idx4, float x) { return __builtin_bit_cast(float, __builtin_amdgcn_ds_bpermute(idx4, __builtin_bit_cast(int, x))); }
; template <int PASS, bool REV> ...
;     ...
;         for (int tg = 0; tg < 4; ++tg) { const v2u uw = *(const LAS v2u*)(UB + (tg * 16 + fr) * 264 + ch); const float uv[4] = {bflo(uw.x), bfhi(uw.x), bflo(uw.y), bfhi(uw.y)};
; #pragma unroll
;             for (int j = 0; j < 4; ++j) { const float r = fsigmoid(aa[tg][j] + bav[j]), ig = fsigmoid(ax[tg][j] + bxv[j]); const float la = -8.0f * r * sp[j];
;                 float Av = __expf(la); const float om = __builtin_fmaf(-Av, Av, 1.0f);
;                 float Bv = __builtin_amdgcn_sqrtf(om) * (ig * uv[j]);
;                 rg_scan_step<REV, 1>(Av, Bv); rg_scan_step<REV, 2>(Av, Bv); rg_scan_step<REV, 4>(Av, Bv); rg_scan_step<REV, 8>(Av, Bv);
;                 aa[tg][j] = Av; ax[tg][j] = Bv; } }
;         const int lastl4 = ((lane & 48) | (REV ? 0 : 15)) << 2;
;         if (PASS == 1) {
;             f32x4 At = (f32x4){1.f, 1.f, 1.f, 1.f}, Bt = (f32x4){0.f, 0.f, 0.f, 0.f};
; #pragma unroll
;             for (int t4 = 0; t4 < 4; ++t4) { const int tg = REV ? 3 - t4 : t4;
; #pragma unroll
;                 for (int j = 0; j < 4; ++j) { const float ta = bperm_f(lastl4, aa[tg][j]), tb = bperm_f(lastl4, ax[tg][j]); Bt[j] = ta * Bt[j] + tb; At[j] = At[j] * ta; } }
;             if (fr == 0) { f32x4* cp = (f32x4*)(CAR + ((size_t)u * 2 + d) * 256 + ch); cp[0] = (f32x4){At[0], Bt[0], At[1], Bt[1]}; cp[1] = (f32x4){At[2], Bt[2], At[3], Bt[3]}; }
;         } else {
;             f32x4 hin = *(const LAS f32x4*)(CIN + d * 256 + ch);
; #pragma unroll
;             for (int t4 = 0; t4 < 4; ++t4) { const int tg = REV ? 3 - t4 : t4;
; #pragma unroll
;                 for (int j = 0; j < 4; ++j) { const float h = aa[tg][j] * hin[j] + ax[tg][j]; ax[tg][j] = h; hin[j] = bperm_f(lastl4, h); } }
	v_pk_fma_f32 v[22:23], v[46:47], v[22:23], v[26:27]
	v_lshlrev_b32_e32 v46, 16, v44
	v_and_b32_e32 v47, 0xffff0000, v44
	v_pk_mul_f32 v[46:47], v[74:75], v[46:47]
	v_pk_mul_f32 v[46:47], v[78:79], v[46:47]
	v_mov_b32_e32 v52, v40
	v_mul_f32_dpp v52, v40, v40 row_shr:1 row_mask:0xf bank_mask:0xf
	v_mov_b32_e32 v53, v41
	v_mul_f32_dpp v53, v41, v41 row_shr:1 row_mask:0xf bank_mask:0xf
	v_fmac_f32_dpp v46, v46, v40 row_shr:1 row_mask:0xf bank_mask:0xf bound_ctrl:1
	v_mov_b32_e32 v40, v46
	v_fmac_f32_dpp v47, v47, v41 row_shr:1 row_mask:0xf bank_mask:0xf bound_ctrl:1
	v_mov_b32_e32 v41, v47
	ds_bpermute_b32 v24, v155, v20
	ds_bpermute_b32 v25, v155, v21
	v_mov_b32_e32 v48, v52
	v_mul_f32_dpp v48, v52, v52 row_shr:2 row_mask:0xf bank_mask:0xf
	v_mov_b32_e32 v49, v53
	v_mul_f32_dpp v49, v53, v53 row_shr:2 row_mask:0xf bank_mask:0xf
	v_fmac_f32_dpp v40, v40, v52 row_shr:2 row_mask:0xf bank_mask:0xf bound_ctrl:1
	v_fmac_f32_dpp v41, v41, v53 row_shr:2 row_mask:0xf bank_mask:0xf bound_ctrl:1
	v_mov_b32_e32 v52, v48
	v_mul_f32_dpp v52, v48, v48 row_shr:4 row_mask:0xf bank_mask:0xf
	v_mov_b32_e32 v53, v49
	v_mul_f32_dpp v53, v49, v49 row_shr:4 row_mask:0xf bank_mask:0xf
	v_fmac_f32_dpp v40, v40, v48 row_shr:4 row_mask:0xf bank_mask:0xf bound_ctrl:1
	v_fmac_f32_dpp v41, v41, v49 row_shr:4 row_mask:0xf bank_mask:0xf bound_ctrl:1
	v_lshlrev_b32_e32 v44, 16, v45
	v_and_b32_e32 v45, 0xffff0000, v45
	v_fmac_f32_dpp v40, v40, v52 row_shr:8 row_mask:0xf bank_mask:0xf bound_ctrl:1
	v_fmac_f32_dpp v41, v41, v53 row_shr:8 row_mask:0xf bank_mask:0xf bound_ctrl:1
	v_mov_b32_e32 v46, v52
	v_mul_f32_dpp v46, v52, v52 row_shr:8 row_mask:0xf bank_mask:0xf
	v_mov_b32_e32 v47, v53
	v_mul_f32_dpp v47, v53, v53 row_shr:8 row_mask:0xf bank_mask:0xf
	v_pk_mul_f32 v[44:45], v[58:59], v[44:45]
	s_waitcnt lgkmcnt(0)
	v_pk_fma_f32 v[24:25], v[46:47], v[24:25], v[40:41]
	v_pk_mul_f32 v[44:45], v[72:73], v[44:45]
	v_mov_b32_e32 v48, v38
	v_mul_f32_dpp v48, v38, v38 row_shr:1 row_mask:0xf bank_mask:0xf
	v_mov_b32_e32 v49, v39
	v_mul_f32_dpp v49, v39, v39 row_shr:1 row_mask:0xf bank_mask:0xf
	v_fmac_f32_dpp v44, v44, v38 row_shr:1 row_mask:0xf bank_mask:0xf bound_ctrl:1
	v_mov_b32_e32 v38, v44
	v_fmac_f32_dpp v45, v45, v39 row_shr:1 row_mask:0xf bank_mask:0xf bound_ctrl:1
	v_mov_b32_e32 v39, v45
	ds_bpermute_b32 v26, v155, v22
	ds_bpermute_b32 v27, v155, v23
	v_mov_b32_e32 v46, v48
	v_mul_f32_dpp v46, v48, v48 row_shr:2 row_mask:0xf bank_mask:0xf
	v_mov_b32_e32 v47, v49
	v_mul_f32_dpp v47, v49, v49 row_shr:2 row_mask:0xf bank_mask:0xf
	v_fmac_f32_dpp v38, v38, v48 row_shr:2 row_mask:0xf bank_mask:0xf bound_ctrl:1
	v_fmac_f32_dpp v39, v39, v49 row_shr:2 row_mask:0xf bank_mask:0xf bound_ctrl:1
	v_mov_b32_e32 v48, v46
	v_mul_f32_dpp v48, v46, v46 row_shr:4 row_mask:0xf bank_mask:0xf
	v_mov_b32_e32 v49, v47
	v_mul_f32_dpp v49, v47, v47 row_shr:4 row_mask:0xf bank_mask:0xf
	v_fmac_f32_dpp v38, v38, v46 row_shr:4 row_mask:0xf bank_mask:0xf bound_ctrl:1
	v_fmac_f32_dpp v39, v39, v47 row_shr:4 row_mask:0xf bank_mask:0xf bound_ctrl:1
	s_nop 1
	v_fmac_f32_dpp v38, v38, v48 row_shr:8 row_mask:0xf bank_mask:0xf bound_ctrl:1
	v_fmac_f32_dpp v39, v39, v49 row_shr:8 row_mask:0xf bank_mask:0xf bound_ctrl:1
	v_mov_b32_e32 v44, v48
	v_mul_f32_dpp v44, v48, v48 row_shr:8 row_mask:0xf bank_mask:0xf
	v_mov_b32_e32 v45, v49
	v_mul_f32_dpp v45, v49, v49 row_shr:8 row_mask:0xf bank_mask:0xf
	s_waitcnt lgkmcnt(0)
; #define LAS __attribute__((address_space(3)))
; __device__ __forceinline__ void lds_barrier() { asm volatile("s_waitcnt lgkmcnt(0)" ::: "memory"); __builtin_amdgcn_s_barrier(); asm volatile("" ::: "memory"); }
; __device__ __forceinline__ float fsigmoid(float x) { return __builtin_amdgcn_rcpf(1.0f + __expf(-x)); }
; __device__ __forceinline__ float bperm_f(int idx4, float x) { return __builtin_bit_cast(float, __builtin_amdgcn_ds_bpermute(idx4, __builtin_bit_cast(int, x))); }
; template <int PASS, bool REV> ...
;     ...
;             for (int j = 0; j < 4; ++j) { const float r = fsigmoid(aa[tg][j] + bav[j]), ig = fsigmoid(ax[tg][j] + bxv[j]); const float la = -8.0f * r * sp[j];
;                 float Av = __expf(la); const float om = __builtin_fmaf(-Av, Av, 1.0f);
;                 float Bv = __builtin_amdgcn_sqrtf(om) * (ig * uv[j]);
;                 rg_scan_step<REV, 1>(Av, Bv); rg_scan_step<REV, 2>(Av, Bv); rg_scan_step<REV, 4>(Av, Bv); rg_scan_step<REV, 8>(Av, Bv);
;                 aa[tg][j] = Av; ax[tg][j] = Bv; } }
;         const int lastl4 = ((lane & 48) | (REV ? 0 : 15)) << 2;
;         if (PASS == 1) {
;             f32x4 At = (f32x4){1.f, 1.f, 1.f, 1.f}, Bt = (f32x4){0.f, 0.f, 0.f, 0.f};
; #pragma unroll
;             for (int t4 = 0; t4 < 4; ++t4) { const int tg = REV ? 3 - t4 : t4;
; #pragma unroll
;                 for (int j = 0; j < 4; ++j) { const float ta = bperm_f(lastl4, aa[tg][j]), tb = bperm_f(lastl4, ax[tg][j]); Bt[j] = ta * Bt[j] + tb; At[j] = At[j] * ta; } }
;             if (fr == 0) { f32x4* cp = (f32x4*)(CAR + ((size_t)u * 2 + d) * 256 + ch); cp[0] = (f32x4){At[0], Bt[0], At[1], Bt[1]}; cp[1] = (f32x4){At[2], Bt[2], At[3], Bt[3]}; }
;         } else {
;             f32x4 hin = *(const LAS f32x4*)(CIN + d * 256 + ch);
; #pragma unroll
;             for (int t4 = 0; t4 < 4; ++t4) { const int tg = REV ? 3 - t4 : t4;
; #pragma unroll
;                 for (int j = 0; j < 4; ++j) { const float h = aa[tg][j] * hin[j] + ax[tg][j]; ax[tg][j] = h; hin[j] = bperm_f(lastl4, h); } }
;             LAS float* hs = HS + (ng & 1) * 4096;
;             if (!REV) {
; #pragma unroll
;                 for (int tg = 0; tg < 4; ++tg) *(LAS f32x4*)(hs + (tg * 16 + fr) * 64 + blk * 16 + fq * 4) = ax[tg];
;             }
;             lds_barrier();
	v_pk_fma_f32 v[26:27], v[44:45], v[26:27], v[38:39]
	v_lshlrev_b32_e32 v44, 16, v36
	v_and_b32_e32 v45, 0xffff0000, v36
	v_pk_mul_f32 v[42:43], v[42:43], v[44:45]
	v_pk_mul_f32 v[42:43], v[50:51], v[42:43]
	v_mov_b32_e32 v46, v28
	v_mul_f32_dpp v46, v28, v28 row_shr:1 row_mask:0xf bank_mask:0xf
	v_mov_b32_e32 v47, v29
	v_mul_f32_dpp v47, v29, v29 row_shr:1 row_mask:0xf bank_mask:0xf
	v_fmac_f32_dpp v42, v42, v28 row_shr:1 row_mask:0xf bank_mask:0xf bound_ctrl:1
	v_mov_b32_e32 v28, v42
	v_fmac_f32_dpp v43, v43, v29 row_shr:1 row_mask:0xf bank_mask:0xf bound_ctrl:1
	v_mov_b32_e32 v29, v43
	v_lshlrev_b32_e32 v36, 16, v37
	v_and_b32_e32 v37, 0xffff0000, v37
	v_pk_mul_f32 v[32:33], v[32:33], v[36:37]
	v_mov_b32_e32 v44, v46
	v_mul_f32_dpp v44, v46, v46 row_shr:2 row_mask:0xf bank_mask:0xf
	v_mov_b32_e32 v45, v47
	v_mul_f32_dpp v45, v47, v47 row_shr:2 row_mask:0xf bank_mask:0xf
	v_fmac_f32_dpp v28, v28, v46 row_shr:2 row_mask:0xf bank_mask:0xf bound_ctrl:1
	v_fmac_f32_dpp v29, v29, v47 row_shr:2 row_mask:0xf bank_mask:0xf bound_ctrl:1
	v_pk_mul_f32 v[32:33], v[34:35], v[32:33]
	v_mov_b32_e32 v46, v44
	v_mul_f32_dpp v46, v44, v44 row_shr:4 row_mask:0xf bank_mask:0xf
	v_mov_b32_e32 v47, v45
	v_mul_f32_dpp v47, v45, v45 row_shr:4 row_mask:0xf bank_mask:0xf
	v_fmac_f32_dpp v28, v28, v44 row_shr:4 row_mask:0xf bank_mask:0xf bound_ctrl:1
	v_fmac_f32_dpp v29, v29, v45 row_shr:4 row_mask:0xf bank_mask:0xf bound_ctrl:1
	v_mov_b32_e32 v36, v30
	v_mul_f32_dpp v36, v30, v30 row_shr:1 row_mask:0xf bank_mask:0xf
	v_mov_b32_e32 v37, v31
	v_mul_f32_dpp v37, v31, v31 row_shr:1 row_mask:0xf bank_mask:0xf
	v_fmac_f32_dpp v32, v32, v30 row_shr:1 row_mask:0xf bank_mask:0xf bound_ctrl:1
	v_mov_b32_e32 v30, v32
	v_fmac_f32_dpp v33, v33, v31 row_shr:1 row_mask:0xf bank_mask:0xf bound_ctrl:1
	v_mov_b32_e32 v31, v33
	ds_bpermute_b32 v40, v155, v24
	ds_bpermute_b32 v41, v155, v25
	ds_bpermute_b32 v38, v155, v26
	ds_bpermute_b32 v39, v155, v27
	v_mov_b32_e32 v34, v36
	v_mul_f32_dpp v34, v36, v36 row_shr:2 row_mask:0xf bank_mask:0xf
	v_mov_b32_e32 v35, v37
	v_mul_f32_dpp v35, v37, v37 row_shr:2 row_mask:0xf bank_mask:0xf
	v_fmac_f32_dpp v30, v30, v36 row_shr:2 row_mask:0xf bank_mask:0xf bound_ctrl:1
	v_fmac_f32_dpp v31, v31, v37 row_shr:2 row_mask:0xf bank_mask:0xf bound_ctrl:1
	v_mov_b32_e32 v36, v34
	v_mul_f32_dpp v36, v34, v34 row_shr:4 row_mask:0xf bank_mask:0xf
	v_mov_b32_e32 v37, v35
	v_mul_f32_dpp v37, v35, v35 row_shr:4 row_mask:0xf bank_mask:0xf
	v_fmac_f32_dpp v30, v30, v34 row_shr:4 row_mask:0xf bank_mask:0xf bound_ctrl:1
	v_fmac_f32_dpp v31, v31, v35 row_shr:4 row_mask:0xf bank_mask:0xf bound_ctrl:1
	v_lshl_add_u32 v34, s4, 2, v156
	ds_write_b128 v34, v[16:19] offset:36864
	ds_write_b128 v34, v[20:23] offset:40960
	ds_write_b128 v34, v[24:27] offset:45056
	v_mov_b32_e32 v16, v28
	v_fmac_f32_dpp v16, v28, v46 row_shr:8 row_mask:0xf bank_mask:0xf bound_ctrl:1
	v_mov_b32_e32 v17, v29
	v_fmac_f32_dpp v17, v29, v47 row_shr:8 row_mask:0xf bank_mask:0xf bound_ctrl:1
	v_mov_b32_e32 v18, v30
	v_fmac_f32_dpp v18, v30, v36 row_shr:8 row_mask:0xf bank_mask:0xf bound_ctrl:1
	v_mov_b32_e32 v19, v31
	v_fmac_f32_dpp v19, v31, v37 row_shr:8 row_mask:0xf bank_mask:0xf bound_ctrl:1
	v_mov_b32_e32 v20, v46
	v_mul_f32_dpp v20, v46, v46 row_shr:8 row_mask:0xf bank_mask:0xf
	v_mov_b32_e32 v21, v47
	v_mul_f32_dpp v21, v47, v47 row_shr:8 row_mask:0xf bank_mask:0xf
	v_mov_b32_e32 v22, v36
	v_mul_f32_dpp v22, v36, v36 row_shr:8 row_mask:0xf bank_mask:0xf
	v_mov_b32_e32 v23, v37
	v_mul_f32_dpp v23, v37, v37 row_shr:8 row_mask:0xf bank_mask:0xf
	s_waitcnt lgkmcnt(5)
	v_pk_fma_f32 v[16:17], v[20:21], v[40:41], v[16:17]
	s_waitcnt lgkmcnt(3)
	v_pk_fma_f32 v[18:19], v[22:23], v[38:39], v[18:19]
	ds_write_b128 v34, v[16:19] offset:49152
	s_waitcnt lgkmcnt(0)
	s_barrier
	v_add_u32_e32 v111, 32, v111
	s_cbranch_scc0 .LBB0_770
	s_branch .LBB0_656
